# PEER int8 table stores (consumed ten phases later) tagged nt
# speedup vs baseline: 1.0275x; 1.0001x over previous
; __device__ __forceinline__ void pt_load(const float* tu, const float* tv, f32x4* v, int r, int lane) {
;     const f32x4* sp = (const f32x4*)(((r >> 14) ? tv : tu) + (size_t)(r & 16383) * D) + lane;
; #pragma unroll
;     for (int j = 0; j < 16; ++j) v[j] = sp[64 * j];
; }
; __device__ __forceinline__ void pt_proc(unsigned char* PT, const f32x4* v, int r, int lane) {
;     const int tb = r >> 14, e = r & 16383; unsigned char* tab = PT + (tb ? PT_V8 : 0); float amax = 0.f;
; #pragma unroll
;     for (int j = 0; j < 16; ++j) amax = fmaxf(fmaxf(amax, fmaxf(fabsf(v[j].x), fabsf(v[j].y))), fmaxf(fabsf(v[j].z), fabsf(v[j].w)));
.Lside_loop:
	s_add_i32 s23, s23, 8
	s_add_i32 s25, s25, 0x8000
	s_and_b32 s38, s25, 0x3fff000
	s_add_i32 s40, s66, s23
	s_lshl_b32 s36, s38, 2
	s_cmpk_lt_u32 s40, 0x4000
	s_cselect_b64 s[38:39], -1, 0
	s_and_b64 s[34:35], s[38:39], exec
	s_cselect_b32 s34, s12, s14
	s_cselect_b32 s35, s13, s15
	s_cselect_b32 s41, 0, 0x4000000
	s_add_u32 s34, s34, s36
	s_addc_u32 s35, s35, 0
	v_lshlrev_b32_e32 v204, 4, v194
	s_movk_i32 s36, 0x2000
	v_lshl_add_u64 v[136:137], s[34:35], 0, v[204:205]
	v_add_co_u32_e32 v138, vcc, s36, v136
	global_load_dwordx4 v[216:219], v204, s[34:35] nt
	global_load_dwordx4 v[220:223], v204, s[34:35] offset:1024 nt
	global_load_dwordx4 v[188:191], v204, s[34:35] offset:2048 nt
	global_load_dwordx4 v[184:187], v204, s[34:35] offset:3072 nt
	v_addc_co_u32_e32 v139, vcc, 0, v137, vcc
	global_load_dwordx4 v[180:183], v[138:139], off offset:-4096 nt
	s_movk_i32 s37, 0x1000
	v_add_co_u32_e32 v140, vcc, s37, v136
	s_movk_i32 s34, 0x3000
	s_nop 0
	v_addc_co_u32_e32 v141, vcc, 0, v137, vcc
	global_load_dwordx4 v[176:179], v[140:141], off offset:1024 nt
	global_load_dwordx4 v[172:175], v[140:141], off offset:2048 nt
	global_load_dwordx4 v[168:171], v[140:141], off offset:3072 nt
	global_load_dwordx4 v[164:167], v[138:139], off nt
	global_load_dwordx4 v[160:163], v[138:139], off offset:1024 nt
	global_load_dwordx4 v[156:159], v[138:139], off offset:2048 nt
	v_add_co_u32_e32 v136, vcc, s34, v136
	v_lshlrev_b32_e32 v204, 2, v194
	s_nop 0
	v_addc_co_u32_e32 v137, vcc, 0, v137, vcc
	global_load_dwordx4 v[152:155], v[138:139], off offset:3072 nt
	global_load_dwordx4 v[148:151], v[136:137], off nt
	global_load_dwordx4 v[144:147], v[136:137], off offset:1024 nt
	global_load_dwordx4 v[140:143], v[136:137], off offset:2048 nt
	s_nop 0
	global_load_dwordx4 v[136:139], v[136:137], off offset:3072 nt
	s_waitcnt vmcnt(48)
	v_max_f32_e64 v58, |v69|, |v69|
	v_max_f32_e64 v59, |v68|, |v68|
	v_max_f32_e64 v66, |v71|, |v71|
	v_max_f32_e64 v67, |v70|, |v70|
	s_waitcnt vmcnt(47)
	v_max_f32_e64 v76, |v73|, |v73|
	v_max_f32_e64 v77, |v72|, |v72|
	v_max_f32_e64 v78, |v75|, |v75|
	v_max_f32_e64 v79, |v74|, |v74|
	v_max_f32_e32 v58, v59, v58
	v_max_f32_e32 v59, v67, v66
	s_waitcnt vmcnt(46)
	v_max_f32_e64 v80, |v55|, |v55|
	v_max_f32_e64 v81, |v54|, |v54|
	v_max_f32_e64 v82, |v57|, |v57|
	v_max_f32_e64 v83, |v56|, |v56|
	v_max_f32_e32 v66, v77, v76
	v_max_f32_e32 v67, v79, v78
	v_max3_f32 v58, v58, 0, v59
	s_waitcnt vmcnt(45)
	v_max_f32_e64 v84, |v51|, |v51|
	v_max_f32_e64 v85, |v50|, |v50|
	v_max_f32_e64 v86, |v53|, |v53|
	v_max_f32_e64 v87, |v52|, |v52|
	v_max_f32_e32 v76, v81, v80
	v_max_f32_e32 v77, v83, v82
	v_max3_f32 v58, v58, v66, v67
	v_max_f32_e32 v78, v85, v84
	v_max_f32_e32 v79, v87, v86
	s_waitcnt vmcnt(44)
	v_max_f32_e64 v59, |v47|, |v47|
	v_max_f32_e64 v80, |v46|, |v46|
	v_max_f32_e64 v81, |v49|, |v49|
	v_max_f32_e64 v82, |v48|, |v48|
	v_max3_f32 v58, v58, v76, v77
	s_waitcnt vmcnt(43)
	v_max_f32_e64 v83, |v43|, |v43|
	v_max_f32_e64 v84, |v42|, |v42|
	v_max_f32_e64 v85, |v45|, |v45|
	v_max_f32_e64 v86, |v44|, |v44|
	v_max_f32_e32 v59, v80, v59
	v_max_f32_e32 v66, v82, v81
	v_max3_f32 v58, v58, v78, v79
	s_waitcnt vmcnt(42)
	v_max_f32_e64 v87, |v39|, |v39|
	v_max_f32_e64 v88, |v38|, |v38|
	v_max_f32_e64 v89, |v41|, |v41|
	v_max_f32_e64 v90, |v40|, |v40|
	v_max_f32_e32 v67, v84, v83
	v_max_f32_e32 v80, v86, v85
	v_max3_f32 v58, v58, v59, v66
	s_waitcnt vmcnt(41)
	v_max_f32_e64 v91, |v35|, |v35|
	v_max_f32_e64 v92, |v34|, |v34|
	v_max_f32_e64 v93, |v37|, |v37|
	v_max_f32_e64 v94, |v36|, |v36|
	v_max_f32_e32 v81, v88, v87
	v_max_f32_e32 v82, v90, v89
	v_max3_f32 v58, v58, v67, v80
	s_waitcnt vmcnt(40)
	v_max_f32_e64 v95, |v31|, |v31|
	v_max_f32_e32 v83, v92, v91
	v_max_f32_e32 v84, v94, v93
	v_max3_f32 v58, v58, v81, v82
	v_max_f32_e64 v59, |v30|, |v30|
	v_max_f32_e64 v66, |v33|, |v33|
	v_max_f32_e64 v67, |v32|, |v32|
	v_max3_f32 v58, v58, v83, v84
	v_max_f32_e32 v59, v59, v95
	v_max_f32_e32 v66, v67, v66
	v_max3_f32 v58, v58, v59, v66
	s_waitcnt vmcnt(39)
	v_max_f32_e64 v59, |v27|, |v27|
	v_max_f32_e64 v66, |v26|, |v26|
	v_max_f32_e32 v59, v66, v59
	v_max_f32_e64 v66, |v29|, |v29|
	v_max_f32_e64 v67, |v28|, |v28|
	v_max_f32_e32 v66, v67, v66
	v_max3_f32 v58, v58, v59, v66
	s_waitcnt vmcnt(38)
	v_max_f32_e64 v59, |v23|, |v23|
	v_max_f32_e64 v66, |v22|, |v22|
	v_max_f32_e32 v59, v66, v59
	v_max_f32_e64 v66, |v25|, |v25|
	v_max_f32_e64 v67, |v24|, |v24|
	v_max_f32_e32 v66, v67, v66
	v_max3_f32 v58, v58, v59, v66
	s_waitcnt vmcnt(37)
	v_max_f32_e64 v59, |v19|, |v19|
	v_max_f32_e64 v66, |v18|, |v18|
	v_max_f32_e32 v59, v66, v59
	v_max_f32_e64 v66, |v21|, |v21|
	v_max_f32_e64 v67, |v20|, |v20|
	v_max_f32_e32 v66, v67, v66
	v_max3_f32 v58, v58, v59, v66
	s_waitcnt vmcnt(36)
	v_max_f32_e64 v59, |v15|, |v15|
	v_max_f32_e64 v66, |v14|, |v14|
	v_max_f32_e32 v59, v66, v59
	v_max_f32_e64 v66, |v17|, |v17|
	v_max_f32_e64 v67, |v16|, |v16|
	v_max_f32_e32 v66, v67, v66
	v_max3_f32 v58, v58, v59, v66
	s_waitcnt vmcnt(35)
	v_max_f32_e64 v59, |v11|, |v11|
	v_max_f32_e64 v66, |v10|, |v10|
	v_max_f32_e32 v59, v66, v59
	v_max_f32_e64 v66, |v13|, |v13|
	v_max_f32_e64 v67, |v12|, |v12|
	v_max_f32_e32 v66, v67, v66
	v_max3_f32 v58, v58, v59, v66
	s_waitcnt vmcnt(34)
	v_max_f32_e64 v59, |v7|, |v7|
	v_max_f32_e64 v66, |v6|, |v6|
	v_max_f32_e32 v59, v66, v59
	v_max_f32_e64 v66, |v9|, |v9|
	v_max_f32_e64 v67, |v8|, |v8|
	v_max_f32_e32 v66, v67, v66
	v_max3_f32 v58, v58, v59, v66
	s_waitcnt vmcnt(33)
	v_max_f32_e64 v59, |v3|, |v3|
	v_max_f32_e64 v66, |v2|, |v2|
	v_max_f32_e32 v59, v66, v59
	v_max_f32_e64 v66, |v5|, |v5|
	v_max_f32_e64 v67, |v4|, |v4|
	v_max_f32_e32 v66, v67, v66
	v_max3_f32 v58, v58, v59, v66
	ds_bpermute_b32 v59, v60, v58
	s_waitcnt lgkmcnt(0)
; __device__ __forceinline__ void pt_proc(unsigned char* PT, const f32x4* v, int r, int lane) {
;     ...
;     amax = wave_max(amax); const float scale = amax > 0.f ? 127.f / amax : 0.f;
; #pragma unroll
;     for (int j = 0; j < 16; ++j) ((unsigned*)(tab + (size_t)j * PT_SLICE + (size_t)e * 256))[lane] = pack_i8x4(v[j].x * scale, v[j].y * scale, v[j].z * scale, v[j].w * scale);
	v_max_f32_e32 v59, v59, v59
	v_max_f32_e32 v58, v58, v59
	ds_bpermute_b32 v59, v61, v58
	s_waitcnt lgkmcnt(0)
	v_max_f32_e32 v59, v59, v59
	v_max_f32_e32 v58, v58, v59
	ds_bpermute_b32 v59, v62, v58
	s_waitcnt lgkmcnt(0)
	v_max_f32_e32 v59, v59, v59
	v_max_f32_e32 v58, v58, v59
	ds_bpermute_b32 v59, v63, v58
	s_waitcnt lgkmcnt(0)
	v_max_f32_e32 v59, v59, v59
	v_max_f32_e32 v58, v58, v59
	ds_bpermute_b32 v59, v64, v58
	s_waitcnt lgkmcnt(0)
	v_max_f32_e32 v59, v59, v59
	v_max_f32_e32 v58, v58, v59
	ds_bpermute_b32 v59, v65, v58
	s_waitcnt lgkmcnt(0)
	v_max_f32_e32 v59, v59, v59
	v_max_f32_e32 v66, v58, v59
	v_div_scale_f32 v58, s[34:35], v66, v66, s69
	v_rcp_f32_e32 v59, v58
	s_and_b32 s34, s30, 0x3fff
	s_add_u32 s30, s33, s31
	s_addc_u32 s31, s46, 0
	v_fma_f32 v67, -v58, v59, 1.0
	v_fmac_f32_e32 v59, v67, v59
	v_div_scale_f32 v67, vcc, s69, v66, s69
	v_mul_f32_e32 v76, v67, v59
	v_fma_f32 v77, -v58, v76, v67
	v_fmac_f32_e32 v76, v77, v59
	v_fma_f32 v58, -v58, v76, v67
	v_div_fmas_f32 v58, v58, v59, v76
	v_div_fixup_f32 v58, v58, v66, s69
	v_cmp_lt_f32_e32 vcc, 0, v66
	s_lshl_b32 s35, s34, 8
	s_add_u32 s30, s30, s35
	v_cndmask_b32_e32 v67, 0, v58, vcc
	v_mul_f32_e32 v69, v69, v67
	v_mul_f32_e32 v68, v68, v67
	v_mul_f32_e32 v70, v70, v67
	v_mul_f32_e32 v71, v71, v67
	v_rndne_f32_e32 v69, v69
	v_rndne_f32_e32 v68, v68
	v_cvt_i32_f32_e32 v69, v69
	v_rndne_f32_e32 v70, v70
	v_rndne_f32_e32 v71, v71
	v_cvt_i32_f32_e32 v68, v68
	v_cvt_i32_f32_sdwa v70, v70 dst_sel:WORD_1 dst_unused:UNUSED_PAD src0_sel:DWORD
	v_cvt_i32_f32_e32 v71, v71
	v_lshlrev_b32_e32 v69, 8, v69
	v_and_b32_e32 v69, 0xff00, v69
	v_and_b32_e32 v70, 0xff0000, v70
	v_perm_b32 v68, v71, v68, s70
	s_addc_u32 s31, s31, 0
	v_or3_b32 v68, v68, v69, v70
	v_mul_f32_e32 v69, v73, v67
	global_store_dword v204, v68, s[30:31] nt
	v_mul_f32_e32 v68, v72, v67
	v_mul_f32_e32 v70, v74, v67
	v_mul_f32_e32 v71, v75, v67
	v_rndne_f32_e32 v69, v69
	v_rndne_f32_e32 v68, v68
	v_cvt_i32_f32_e32 v69, v69
	v_rndne_f32_e32 v70, v70
	v_rndne_f32_e32 v71, v71
	v_mul_f32_e32 v55, v55, v67
	v_cvt_i32_f32_e32 v68, v68
	v_cvt_i32_f32_sdwa v70, v70 dst_sel:WORD_1 dst_unused:UNUSED_PAD src0_sel:DWORD
	v_cvt_i32_f32_e32 v71, v71
	v_mul_f32_e32 v54, v54, v67
	v_mul_f32_e32 v56, v56, v67
	v_mul_f32_e32 v57, v57, v67
	v_rndne_f32_e32 v55, v55
	v_rndne_f32_e32 v54, v54
	v_cvt_i32_f32_e32 v55, v55
	v_rndne_f32_e32 v56, v56
	v_rndne_f32_e32 v57, v57
	v_mul_f32_e32 v51, v51, v67
	v_cvt_i32_f32_e32 v54, v54
	v_cvt_i32_f32_sdwa v56, v56 dst_sel:WORD_1 dst_unused:UNUSED_PAD src0_sel:DWORD
	v_cvt_i32_f32_e32 v57, v57
	v_mul_f32_e32 v50, v50, v67
	v_mul_f32_e32 v52, v52, v67
	v_mul_f32_e32 v53, v53, v67
	v_rndne_f32_e32 v51, v51
	v_lshlrev_b32_e32 v69, 8, v69
	v_rndne_f32_e32 v50, v50
	v_cvt_i32_f32_e32 v51, v51
	v_rndne_f32_e32 v52, v52
	v_rndne_f32_e32 v53, v53
	v_mul_f32_e32 v47, v47, v67
	v_lshl_add_u64 v[58:59], s[30:31], 0, v[204:205]
	v_and_b32_e32 v69, 0xff00, v69
	v_and_b32_e32 v70, 0xff0000, v70
	v_perm_b32 v68, v71, v68, s70
	s_mov_b32 s30, 0x400000
	v_cvt_i32_f32_e32 v50, v50
	v_cvt_i32_f32_sdwa v52, v52 dst_sel:WORD_1 dst_unused:UNUSED_PAD src0_sel:DWORD
	v_cvt_i32_f32_e32 v53, v53
	v_mul_f32_e32 v46, v46, v67
	v_mul_f32_e32 v48, v48, v67
	v_mul_f32_e32 v49, v49, v67
	v_rndne_f32_e32 v47, v47
	v_or3_b32 v70, v68, v69, v70
	v_add_co_u32_e32 v68, vcc, s30, v58
	v_lshlrev_b32_e32 v55, 8, v55
	v_rndne_f32_e32 v46, v46
	v_cvt_i32_f32_e32 v47, v47
	v_rndne_f32_e32 v48, v48
	v_rndne_f32_e32 v49, v49
	v_mul_f32_e32 v43, v43, v67
	v_addc_co_u32_e32 v69, vcc, 0, v59, vcc
	v_and_b32_e32 v55, 0xff00, v55
	v_and_b32_e32 v56, 0xff0000, v56
	v_perm_b32 v54, v57, v54, s70
	s_mov_b32 s30, 0x800000
	v_cvt_i32_f32_e32 v46, v46
	v_cvt_i32_f32_sdwa v48, v48 dst_sel:WORD_1 dst_unused:UNUSED_PAD src0_sel:DWORD
	v_cvt_i32_f32_e32 v49, v49
	v_mul_f32_e32 v42, v42, v67
	v_mul_f32_e32 v44, v44, v67
	v_mul_f32_e32 v45, v45, v67
	v_rndne_f32_e32 v43, v43
	v_or3_b32 v56, v54, v55, v56
	v_add_co_u32_e32 v54, vcc, s30, v58
	v_lshlrev_b32_e32 v51, 8, v51
	v_rndne_f32_e32 v42, v42
	v_cvt_i32_f32_e32 v43, v43
	v_rndne_f32_e32 v44, v44
	v_rndne_f32_e32 v45, v45
	v_mul_f32_e32 v39, v39, v67
	v_addc_co_u32_e32 v55, vcc, 0, v59, vcc
	v_and_b32_e32 v51, 0xff00, v51
	v_and_b32_e32 v52, 0xff0000, v52
	v_perm_b32 v50, v53, v50, s70
	s_mov_b32 s30, 0xc00000
	v_cvt_i32_f32_e32 v42, v42
	v_cvt_i32_f32_sdwa v44, v44 dst_sel:WORD_1 dst_unused:UNUSED_PAD src0_sel:DWORD
	v_cvt_i32_f32_e32 v45, v45
	v_mul_f32_e32 v38, v38, v67
	v_mul_f32_e32 v40, v40, v67
	v_mul_f32_e32 v41, v41, v67
	v_rndne_f32_e32 v39, v39
	v_or3_b32 v52, v50, v51, v52
	v_add_co_u32_e32 v50, vcc, s30, v58
	v_lshlrev_b32_e32 v47, 8, v47
	v_rndne_f32_e32 v38, v38
	v_cvt_i32_f32_e32 v39, v39
	v_rndne_f32_e32 v40, v40
	v_rndne_f32_e32 v41, v41
	v_mul_f32_e32 v35, v35, v67
	v_addc_co_u32_e32 v51, vcc, 0, v59, vcc
	v_and_b32_e32 v47, 0xff00, v47
	v_and_b32_e32 v48, 0xff0000, v48
	v_perm_b32 v46, v49, v46, s70
	s_mov_b32 s30, 0x1000000
	v_cvt_i32_f32_e32 v38, v38
	v_cvt_i32_f32_sdwa v40, v40 dst_sel:WORD_1 dst_unused:UNUSED_PAD src0_sel:DWORD
	v_cvt_i32_f32_e32 v41, v41
	v_mul_f32_e32 v34, v34, v67
	v_mul_f32_e32 v36, v36, v67
	v_mul_f32_e32 v37, v37, v67
	v_rndne_f32_e32 v35, v35
	v_or3_b32 v48, v46, v47, v48
	v_add_co_u32_e32 v46, vcc, s30, v58
	v_lshlrev_b32_e32 v43, 8, v43
	v_rndne_f32_e32 v34, v34
	v_cvt_i32_f32_e32 v35, v35
	v_rndne_f32_e32 v36, v36
	v_rndne_f32_e32 v37, v37
	v_mul_f32_e32 v31, v31, v67
	v_addc_co_u32_e32 v47, vcc, 0, v59, vcc
	v_and_b32_e32 v43, 0xff00, v43
	v_and_b32_e32 v44, 0xff0000, v44
	v_perm_b32 v42, v45, v42, s70
	s_mov_b32 s30, 0x1400000
	v_cvt_i32_f32_e32 v34, v34
; __device__ __forceinline__ void pt_proc(unsigned char* PT, const f32x4* v, int r, int lane) {
;     ...
;     for (int j = 0; j < 16; ++j) ((unsigned*)(tab + (size_t)j * PT_SLICE + (size_t)e * 256))[lane] = pack_i8x4(v[j].x * scale, v[j].y * scale, v[j].z * scale, v[j].w * scale);
;     if (lane == 0) ((float*)(PT + (tb ? PT_VS : PT_US)))[e] = amax * (1.f / 127.f);
	v_cvt_i32_f32_sdwa v36, v36 dst_sel:WORD_1 dst_unused:UNUSED_PAD src0_sel:DWORD
	v_cvt_i32_f32_e32 v37, v37
	v_mul_f32_e32 v30, v30, v67
	v_mul_f32_e32 v32, v32, v67
	v_mul_f32_e32 v33, v33, v67
	v_rndne_f32_e32 v31, v31
	v_or3_b32 v44, v42, v43, v44
	v_add_co_u32_e32 v42, vcc, s30, v58
	v_lshlrev_b32_e32 v39, 8, v39
	v_rndne_f32_e32 v30, v30
	v_cvt_i32_f32_e32 v31, v31
	v_rndne_f32_e32 v32, v32
	v_rndne_f32_e32 v33, v33
	v_mul_f32_e32 v27, v27, v67
	v_addc_co_u32_e32 v43, vcc, 0, v59, vcc
	v_and_b32_e32 v39, 0xff00, v39
	v_and_b32_e32 v40, 0xff0000, v40
	v_perm_b32 v38, v41, v38, s70
	s_mov_b32 s30, 0x1800000
	v_cvt_i32_f32_e32 v30, v30
	v_cvt_i32_f32_sdwa v32, v32 dst_sel:WORD_1 dst_unused:UNUSED_PAD src0_sel:DWORD
	v_cvt_i32_f32_e32 v33, v33
	v_mul_f32_e32 v26, v26, v67
	v_mul_f32_e32 v28, v28, v67
	v_mul_f32_e32 v29, v29, v67
	v_rndne_f32_e32 v27, v27
	v_or3_b32 v40, v38, v39, v40
	v_add_co_u32_e32 v38, vcc, s30, v58
	v_lshlrev_b32_e32 v35, 8, v35
	v_rndne_f32_e32 v26, v26
	v_cvt_i32_f32_e32 v27, v27
	v_rndne_f32_e32 v28, v28
	v_rndne_f32_e32 v29, v29
	v_mul_f32_e32 v23, v23, v67
	v_addc_co_u32_e32 v39, vcc, 0, v59, vcc
	v_and_b32_e32 v35, 0xff00, v35
	v_and_b32_e32 v36, 0xff0000, v36
	v_perm_b32 v34, v37, v34, s70
	s_mov_b32 s30, 0x1c00000
	v_cvt_i32_f32_e32 v26, v26
	v_cvt_i32_f32_sdwa v28, v28 dst_sel:WORD_1 dst_unused:UNUSED_PAD src0_sel:DWORD
	v_cvt_i32_f32_e32 v29, v29
	v_mul_f32_e32 v22, v22, v67
	v_mul_f32_e32 v24, v24, v67
	v_mul_f32_e32 v25, v25, v67
	v_rndne_f32_e32 v23, v23
	v_or3_b32 v36, v34, v35, v36
	v_add_co_u32_e32 v34, vcc, s30, v58
	v_lshlrev_b32_e32 v31, 8, v31
	v_rndne_f32_e32 v22, v22
	v_cvt_i32_f32_e32 v23, v23
	v_rndne_f32_e32 v24, v24
	v_rndne_f32_e32 v25, v25
	v_mul_f32_e32 v19, v19, v67
	v_addc_co_u32_e32 v35, vcc, 0, v59, vcc
	v_and_b32_e32 v31, 0xff00, v31
	v_and_b32_e32 v32, 0xff0000, v32
	v_perm_b32 v30, v33, v30, s70
	s_brev_b32 s30, 64
	v_cvt_i32_f32_e32 v22, v22
	v_cvt_i32_f32_sdwa v24, v24 dst_sel:WORD_1 dst_unused:UNUSED_PAD src0_sel:DWORD
	v_cvt_i32_f32_e32 v25, v25
	v_mul_f32_e32 v18, v18, v67
	v_mul_f32_e32 v20, v20, v67
	v_mul_f32_e32 v21, v21, v67
	v_rndne_f32_e32 v19, v19
	v_or3_b32 v32, v30, v31, v32
	v_add_co_u32_e32 v30, vcc, s30, v58
	v_lshlrev_b32_e32 v27, 8, v27
	v_rndne_f32_e32 v18, v18
	v_cvt_i32_f32_e32 v19, v19
	v_rndne_f32_e32 v20, v20
	v_rndne_f32_e32 v21, v21
	v_mul_f32_e32 v15, v15, v67
	v_addc_co_u32_e32 v31, vcc, 0, v59, vcc
	v_and_b32_e32 v27, 0xff00, v27
	v_and_b32_e32 v28, 0xff0000, v28
	v_perm_b32 v26, v29, v26, s70
	s_mov_b32 s30, 0x2400000
	v_cvt_i32_f32_e32 v18, v18
	v_cvt_i32_f32_sdwa v20, v20 dst_sel:WORD_1 dst_unused:UNUSED_PAD src0_sel:DWORD
	v_cvt_i32_f32_e32 v21, v21
	v_mul_f32_e32 v14, v14, v67
	v_mul_f32_e32 v16, v16, v67
	v_mul_f32_e32 v17, v17, v67
	v_rndne_f32_e32 v15, v15
	v_or3_b32 v28, v26, v27, v28
	v_add_co_u32_e32 v26, vcc, s30, v58
	v_lshlrev_b32_e32 v23, 8, v23
	v_rndne_f32_e32 v14, v14
	v_cvt_i32_f32_e32 v15, v15
	v_rndne_f32_e32 v16, v16
	v_rndne_f32_e32 v17, v17
	v_mul_f32_e32 v11, v11, v67
	v_addc_co_u32_e32 v27, vcc, 0, v59, vcc
	v_and_b32_e32 v23, 0xff00, v23
	v_and_b32_e32 v24, 0xff0000, v24
	v_perm_b32 v22, v25, v22, s70
	s_mov_b32 s30, 0x2800000
	v_cvt_i32_f32_e32 v14, v14
	v_cvt_i32_f32_sdwa v16, v16 dst_sel:WORD_1 dst_unused:UNUSED_PAD src0_sel:DWORD
	v_cvt_i32_f32_e32 v17, v17
	v_mul_f32_e32 v10, v10, v67
	v_mul_f32_e32 v12, v12, v67
	v_mul_f32_e32 v13, v13, v67
	v_rndne_f32_e32 v11, v11
	v_or3_b32 v24, v22, v23, v24
	v_add_co_u32_e32 v22, vcc, s30, v58
	v_lshlrev_b32_e32 v19, 8, v19
	v_rndne_f32_e32 v10, v10
	v_cvt_i32_f32_e32 v11, v11
	v_rndne_f32_e32 v12, v12
	v_rndne_f32_e32 v13, v13
	v_mul_f32_e32 v7, v7, v67
	v_addc_co_u32_e32 v23, vcc, 0, v59, vcc
	v_and_b32_e32 v19, 0xff00, v19
	v_and_b32_e32 v20, 0xff0000, v20
	v_perm_b32 v18, v21, v18, s70
	v_cvt_i32_f32_e32 v10, v10
	v_cvt_i32_f32_sdwa v12, v12 dst_sel:WORD_1 dst_unused:UNUSED_PAD src0_sel:DWORD
	v_cvt_i32_f32_e32 v13, v13
	v_mul_f32_e32 v6, v6, v67
	v_mul_f32_e32 v8, v8, v67
	v_mul_f32_e32 v9, v9, v67
	v_rndne_f32_e32 v7, v7
	v_or3_b32 v20, v18, v19, v20
	v_add_co_u32_e32 v18, vcc, s71, v58
	v_lshlrev_b32_e32 v15, 8, v15
	v_rndne_f32_e32 v6, v6
	v_cvt_i32_f32_e32 v7, v7
	v_rndne_f32_e32 v8, v8
	v_rndne_f32_e32 v9, v9
	v_mul_f32_e32 v3, v3, v67
	v_addc_co_u32_e32 v19, vcc, 0, v59, vcc
	v_and_b32_e32 v15, 0xff00, v15
	v_and_b32_e32 v16, 0xff0000, v16
	v_perm_b32 v14, v17, v14, s70
	v_cvt_i32_f32_e32 v6, v6
	v_cvt_i32_f32_sdwa v8, v8 dst_sel:WORD_1 dst_unused:UNUSED_PAD src0_sel:DWORD
	v_cvt_i32_f32_e32 v9, v9
	v_mul_f32_e32 v2, v2, v67
	v_mul_f32_e32 v4, v4, v67
	v_mul_f32_e32 v5, v5, v67
	v_rndne_f32_e32 v3, v3
	v_or3_b32 v16, v14, v15, v16
	v_add_co_u32_e32 v14, vcc, s72, v58
	v_lshlrev_b32_e32 v11, 8, v11
	v_rndne_f32_e32 v2, v2
	v_cvt_i32_f32_e32 v3, v3
	v_rndne_f32_e32 v4, v4
	v_rndne_f32_e32 v5, v5
	v_addc_co_u32_e32 v15, vcc, 0, v59, vcc
	v_and_b32_e32 v11, 0xff00, v11
	v_and_b32_e32 v12, 0xff0000, v12
	v_perm_b32 v10, v13, v10, s70
	v_cvt_i32_f32_e32 v2, v2
	v_cvt_i32_f32_sdwa v4, v4 dst_sel:WORD_1 dst_unused:UNUSED_PAD src0_sel:DWORD
	v_cvt_i32_f32_e32 v5, v5
	v_or3_b32 v12, v10, v11, v12
	v_add_co_u32_e32 v10, vcc, s73, v58
	v_lshlrev_b32_e32 v7, 8, v7
	s_nop 0
	v_addc_co_u32_e32 v11, vcc, 0, v59, vcc
	v_and_b32_e32 v7, 0xff00, v7
	v_and_b32_e32 v8, 0xff0000, v8
	v_perm_b32 v6, v9, v6, s70
	v_or3_b32 v8, v6, v7, v8
	v_add_co_u32_e32 v6, vcc, s74, v58
	v_lshlrev_b32_e32 v3, 8, v3
	s_nop 0
	v_addc_co_u32_e32 v7, vcc, 0, v59, vcc
	v_and_b32_e32 v3, 0xff00, v3
	v_and_b32_e32 v4, 0xff0000, v4
	v_perm_b32 v2, v5, v2, s70
	v_or3_b32 v4, v2, v3, v4
	v_add_co_u32_e32 v2, vcc, 0x3c00000, v58
	global_store_dword v[68:69], v70, off nt
	s_nop 0
	v_addc_co_u32_e32 v3, vcc, 0, v59, vcc
	global_store_dword v[54:55], v56, off nt
	global_store_dword v[50:51], v52, off nt
	global_store_dword v[46:47], v48, off nt
	global_store_dword v[42:43], v44, off nt
	global_store_dword v[38:39], v40, off nt
	global_store_dword v[34:35], v36, off nt
	global_store_dword v[30:31], v32, off nt
	global_store_dword v[26:27], v28, off nt
	global_store_dword v[22:23], v24, off nt
	global_store_dword v[18:19], v20, off nt
	global_store_dword v[14:15], v16, off nt
	global_store_dword v[10:11], v12, off nt
	global_store_dword v[6:7], v8, off nt
	global_store_dword v[2:3], v4, off nt
	s_and_saveexec_b64 s[30:31], s[6:7]
	s_cbranch_execz .Lside_jA
	s_and_b64 s[10:11], s[10:11], exec
	s_cselect_b32 s10, s75, 0x8010000
	s_add_u32 s10, s33, s10
	s_addc_u32 s11, s46, 0
	s_lshl_b32 s34, s34, 2
	v_mul_f32_e32 v2, 0x3c010204, v66
	v_mov_b32_e32 v3, s34
	global_store_dword v3, v2, s[10:11] nt
	s_branch .Lside_jA

; __device__ __forceinline__ void pt_proc(unsigned char* PT, const f32x4* v, int r, int lane) {
;     const int tb = r >> 14, e = r & 16383; unsigned char* tab = PT + (tb ? PT_V8 : 0); float amax = 0.f;
; #pragma unroll
;     for (int j = 0; j < 16; ++j) amax = fmaxf(fmaxf(amax, fmaxf(fabsf(v[j].x), fabsf(v[j].y))), fmaxf(fabsf(v[j].z), fabsf(v[j].w)));
;     amax = wave_max(amax); const float scale = amax > 0.f ? 127.f / amax : 0.f;
.Lside_pB:
	s_waitcnt vmcnt(48)
	v_max_f32_e64 v58, |v217|, |v217|
	v_max_f32_e64 v59, |v216|, |v216|
	v_max_f32_e64 v66, |v219|, |v219|
	v_max_f32_e64 v67, |v218|, |v218|
	s_waitcnt vmcnt(47)
	v_max_f32_e64 v76, |v221|, |v221|
	v_max_f32_e64 v77, |v220|, |v220|
	v_max_f32_e64 v78, |v223|, |v223|
	v_max_f32_e64 v79, |v222|, |v222|
	v_max_f32_e32 v58, v59, v58
	v_max_f32_e32 v59, v67, v66
	s_waitcnt vmcnt(46)
	v_max_f32_e64 v80, |v189|, |v189|
	v_max_f32_e64 v81, |v188|, |v188|
	v_max_f32_e64 v82, |v191|, |v191|
	v_max_f32_e64 v83, |v190|, |v190|
	v_max_f32_e32 v66, v77, v76
	v_max_f32_e32 v67, v79, v78
	v_max3_f32 v58, v58, 0, v59
	s_waitcnt vmcnt(45)
	v_max_f32_e64 v84, |v185|, |v185|
	v_max_f32_e64 v85, |v184|, |v184|
	v_max_f32_e64 v86, |v187|, |v187|
	v_max_f32_e64 v87, |v186|, |v186|
	v_max_f32_e32 v76, v81, v80
	v_max_f32_e32 v77, v83, v82
	v_max3_f32 v58, v58, v66, v67
	v_max_f32_e32 v78, v85, v84
	v_max_f32_e32 v79, v87, v86
	s_waitcnt vmcnt(44)
	v_max_f32_e64 v59, |v181|, |v181|
	v_max_f32_e64 v80, |v180|, |v180|
	v_max_f32_e64 v81, |v183|, |v183|
	v_max_f32_e64 v82, |v182|, |v182|
	v_max3_f32 v58, v58, v76, v77
	s_waitcnt vmcnt(43)
	v_max_f32_e64 v83, |v177|, |v177|
	v_max_f32_e64 v84, |v176|, |v176|
	v_max_f32_e64 v85, |v179|, |v179|
	v_max_f32_e64 v86, |v178|, |v178|
	v_max_f32_e32 v59, v80, v59
	v_max_f32_e32 v66, v82, v81
	v_max3_f32 v58, v58, v78, v79
	s_waitcnt vmcnt(42)
	v_max_f32_e64 v87, |v173|, |v173|
	v_max_f32_e64 v88, |v172|, |v172|
	v_max_f32_e64 v89, |v175|, |v175|
	v_max_f32_e64 v90, |v174|, |v174|
	v_max_f32_e32 v67, v84, v83
	v_max_f32_e32 v80, v86, v85
	v_max3_f32 v58, v58, v59, v66
	s_waitcnt vmcnt(41)
	v_max_f32_e64 v91, |v169|, |v169|
	v_max_f32_e64 v92, |v168|, |v168|
	v_max_f32_e64 v93, |v171|, |v171|
	v_max_f32_e64 v94, |v170|, |v170|
	v_max_f32_e32 v81, v88, v87
	v_max_f32_e32 v82, v90, v89
	v_max3_f32 v58, v58, v67, v80
	s_waitcnt vmcnt(40)
	v_max_f32_e64 v95, |v165|, |v165|
	v_max_f32_e32 v83, v92, v91
	v_max_f32_e32 v84, v94, v93
	v_max3_f32 v58, v58, v81, v82
	v_max_f32_e64 v59, |v164|, |v164|
	v_max_f32_e64 v66, |v167|, |v167|
	v_max_f32_e64 v67, |v166|, |v166|
	v_max3_f32 v58, v58, v83, v84
	v_max_f32_e32 v59, v59, v95
	v_max_f32_e32 v66, v67, v66
	v_max3_f32 v58, v58, v59, v66
	s_waitcnt vmcnt(39)
	v_max_f32_e64 v59, |v161|, |v161|
	v_max_f32_e64 v66, |v160|, |v160|
	v_max_f32_e32 v59, v66, v59
	v_max_f32_e64 v66, |v163|, |v163|
	v_max_f32_e64 v67, |v162|, |v162|
	v_max_f32_e32 v66, v67, v66
	v_max3_f32 v58, v58, v59, v66
	s_waitcnt vmcnt(38)
	v_max_f32_e64 v59, |v157|, |v157|
	v_max_f32_e64 v66, |v156|, |v156|
	v_max_f32_e32 v59, v66, v59
	v_max_f32_e64 v66, |v159|, |v159|
	v_max_f32_e64 v67, |v158|, |v158|
	v_max_f32_e32 v66, v67, v66
	v_max3_f32 v58, v58, v59, v66
	s_waitcnt vmcnt(37)
	v_max_f32_e64 v59, |v153|, |v153|
	v_max_f32_e64 v66, |v152|, |v152|
	v_max_f32_e32 v59, v66, v59
	v_max_f32_e64 v66, |v155|, |v155|
	v_max_f32_e64 v67, |v154|, |v154|
	v_max_f32_e32 v66, v67, v66
	v_max3_f32 v58, v58, v59, v66
	s_waitcnt vmcnt(36)
	v_max_f32_e64 v59, |v149|, |v149|
	v_max_f32_e64 v66, |v148|, |v148|
	v_max_f32_e32 v59, v66, v59
	v_max_f32_e64 v66, |v151|, |v151|
	v_max_f32_e64 v67, |v150|, |v150|
	v_max_f32_e32 v66, v67, v66
	v_max3_f32 v58, v58, v59, v66
	s_waitcnt vmcnt(35)
	v_max_f32_e64 v59, |v145|, |v145|
	v_max_f32_e64 v66, |v144|, |v144|
	v_max_f32_e32 v59, v66, v59
	v_max_f32_e64 v66, |v147|, |v147|
	v_max_f32_e64 v67, |v146|, |v146|
	v_max_f32_e32 v66, v67, v66
	v_max3_f32 v58, v58, v59, v66
	s_waitcnt vmcnt(34)
	v_max_f32_e64 v59, |v141|, |v141|
	v_max_f32_e64 v66, |v140|, |v140|
	v_max_f32_e32 v59, v66, v59
	v_max_f32_e64 v66, |v143|, |v143|
	v_max_f32_e64 v67, |v142|, |v142|
	v_max_f32_e32 v66, v67, v66
	v_max3_f32 v58, v58, v59, v66
	s_waitcnt vmcnt(33)
	v_max_f32_e64 v59, |v137|, |v137|
	v_max_f32_e64 v66, |v136|, |v136|
	v_max_f32_e32 v59, v66, v59
	v_max_f32_e64 v66, |v139|, |v139|
	v_max_f32_e64 v67, |v138|, |v138|
	v_max_f32_e32 v66, v67, v66
	v_max3_f32 v58, v58, v59, v66
	ds_bpermute_b32 v59, v60, v58
	s_waitcnt lgkmcnt(0)
	v_max_f32_e32 v59, v59, v59
	v_max_f32_e32 v58, v58, v59
	ds_bpermute_b32 v59, v61, v58
	s_waitcnt lgkmcnt(0)
	v_max_f32_e32 v59, v59, v59
	v_max_f32_e32 v58, v58, v59
	ds_bpermute_b32 v59, v62, v58
	s_waitcnt lgkmcnt(0)
	v_max_f32_e32 v59, v59, v59
	v_max_f32_e32 v58, v58, v59
	ds_bpermute_b32 v59, v63, v58
	s_waitcnt lgkmcnt(0)
	v_max_f32_e32 v59, v59, v59
	v_max_f32_e32 v58, v58, v59
	ds_bpermute_b32 v59, v64, v58
	s_waitcnt lgkmcnt(0)
	v_max_f32_e32 v59, v59, v59
	v_max_f32_e32 v58, v58, v59
	ds_bpermute_b32 v59, v65, v58
	s_waitcnt lgkmcnt(0)
; __device__ __forceinline__ void pt_proc(unsigned char* PT, const f32x4* v, int r, int lane) {
;     ...
;     amax = wave_max(amax); const float scale = amax > 0.f ? 127.f / amax : 0.f;
; #pragma unroll
;     for (int j = 0; j < 16; ++j) ((unsigned*)(tab + (size_t)j * PT_SLICE + (size_t)e * 256))[lane] = pack_i8x4(v[j].x * scale, v[j].y * scale, v[j].z * scale, v[j].w * scale);
	v_max_f32_e32 v59, v59, v59
	v_max_f32_e32 v66, v58, v59
	v_div_scale_f32 v58, s[34:35], v66, v66, s69
	v_rcp_f32_e32 v59, v58
	s_and_b32 s34, s40, 0x3fff
	s_add_u32 s40, s33, s41
	s_addc_u32 s41, s46, 0
	v_fma_f32 v67, -v58, v59, 1.0
	v_fmac_f32_e32 v59, v67, v59
	v_div_scale_f32 v67, vcc, s69, v66, s69
	v_mul_f32_e32 v76, v67, v59
	v_fma_f32 v77, -v58, v76, v67
	v_fmac_f32_e32 v76, v77, v59
	v_fma_f32 v58, -v58, v76, v67
	v_div_fmas_f32 v58, v58, v59, v76
	v_div_fixup_f32 v58, v58, v66, s69
	v_cmp_lt_f32_e32 vcc, 0, v66
	s_lshl_b32 s35, s34, 8
	s_add_u32 s40, s40, s35
	v_cndmask_b32_e32 v67, 0, v58, vcc
	v_mul_f32_e32 v217, v217, v67
	v_mul_f32_e32 v216, v216, v67
	v_mul_f32_e32 v218, v218, v67
	v_mul_f32_e32 v219, v219, v67
	v_rndne_f32_e32 v217, v217
	v_rndne_f32_e32 v216, v216
	v_cvt_i32_f32_e32 v217, v217
	v_rndne_f32_e32 v218, v218
	v_rndne_f32_e32 v219, v219
	v_cvt_i32_f32_e32 v216, v216
	v_cvt_i32_f32_sdwa v218, v218 dst_sel:WORD_1 dst_unused:UNUSED_PAD src0_sel:DWORD
	v_cvt_i32_f32_e32 v219, v219
	v_lshlrev_b32_e32 v217, 8, v217
	v_and_b32_e32 v217, 0xff00, v217
	v_and_b32_e32 v218, 0xff0000, v218
	v_perm_b32 v216, v219, v216, s70
	s_addc_u32 s41, s41, 0
	v_or3_b32 v216, v216, v217, v218
	v_mul_f32_e32 v217, v221, v67
	global_store_dword v204, v216, s[40:41] nt
	v_mul_f32_e32 v216, v220, v67
	v_mul_f32_e32 v218, v222, v67
	v_mul_f32_e32 v219, v223, v67
	v_rndne_f32_e32 v217, v217
	v_rndne_f32_e32 v216, v216
	v_cvt_i32_f32_e32 v217, v217
	v_rndne_f32_e32 v218, v218
	v_rndne_f32_e32 v219, v219
	v_mul_f32_e32 v189, v189, v67
	v_cvt_i32_f32_e32 v216, v216
	v_cvt_i32_f32_sdwa v218, v218 dst_sel:WORD_1 dst_unused:UNUSED_PAD src0_sel:DWORD
	v_cvt_i32_f32_e32 v219, v219
	v_mul_f32_e32 v188, v188, v67
	v_mul_f32_e32 v190, v190, v67
	v_mul_f32_e32 v191, v191, v67
	v_rndne_f32_e32 v189, v189
	v_rndne_f32_e32 v188, v188
	v_cvt_i32_f32_e32 v189, v189
	v_rndne_f32_e32 v190, v190
	v_rndne_f32_e32 v191, v191
	v_mul_f32_e32 v185, v185, v67
	v_cvt_i32_f32_e32 v188, v188
	v_cvt_i32_f32_sdwa v190, v190 dst_sel:WORD_1 dst_unused:UNUSED_PAD src0_sel:DWORD
	v_cvt_i32_f32_e32 v191, v191
	v_mul_f32_e32 v184, v184, v67
	v_mul_f32_e32 v186, v186, v67
	v_mul_f32_e32 v187, v187, v67
	v_rndne_f32_e32 v185, v185
	v_lshlrev_b32_e32 v217, 8, v217
	v_rndne_f32_e32 v184, v184
	v_cvt_i32_f32_e32 v185, v185
	v_rndne_f32_e32 v186, v186
	v_rndne_f32_e32 v187, v187
	v_mul_f32_e32 v181, v181, v67
	v_lshl_add_u64 v[58:59], s[40:41], 0, v[204:205]
	v_and_b32_e32 v217, 0xff00, v217
	v_and_b32_e32 v218, 0xff0000, v218
	v_perm_b32 v216, v219, v216, s70
	s_mov_b32 s40, 0x400000
	v_cvt_i32_f32_e32 v184, v184
	v_cvt_i32_f32_sdwa v186, v186 dst_sel:WORD_1 dst_unused:UNUSED_PAD src0_sel:DWORD
	v_cvt_i32_f32_e32 v187, v187
	v_mul_f32_e32 v180, v180, v67
	v_mul_f32_e32 v182, v182, v67
	v_mul_f32_e32 v183, v183, v67
	v_rndne_f32_e32 v181, v181
	v_or3_b32 v218, v216, v217, v218
	v_add_co_u32_e32 v216, vcc, s40, v58
	v_lshlrev_b32_e32 v189, 8, v189
	v_rndne_f32_e32 v180, v180
	v_cvt_i32_f32_e32 v181, v181
	v_rndne_f32_e32 v182, v182
	v_rndne_f32_e32 v183, v183
	v_mul_f32_e32 v177, v177, v67
	v_addc_co_u32_e32 v217, vcc, 0, v59, vcc
	v_and_b32_e32 v189, 0xff00, v189
	v_and_b32_e32 v190, 0xff0000, v190
	v_perm_b32 v188, v191, v188, s70
	s_mov_b32 s40, 0x800000
	v_cvt_i32_f32_e32 v180, v180
	v_cvt_i32_f32_sdwa v182, v182 dst_sel:WORD_1 dst_unused:UNUSED_PAD src0_sel:DWORD
	v_cvt_i32_f32_e32 v183, v183
	v_mul_f32_e32 v176, v176, v67
	v_mul_f32_e32 v178, v178, v67
	v_mul_f32_e32 v179, v179, v67
	v_rndne_f32_e32 v177, v177
	v_or3_b32 v190, v188, v189, v190
	v_add_co_u32_e32 v188, vcc, s40, v58
	v_lshlrev_b32_e32 v185, 8, v185
	v_rndne_f32_e32 v176, v176
	v_cvt_i32_f32_e32 v177, v177
	v_rndne_f32_e32 v178, v178
	v_rndne_f32_e32 v179, v179
	v_mul_f32_e32 v173, v173, v67
	v_addc_co_u32_e32 v189, vcc, 0, v59, vcc
	v_and_b32_e32 v185, 0xff00, v185
	v_and_b32_e32 v186, 0xff0000, v186
	v_perm_b32 v184, v187, v184, s70
	s_mov_b32 s40, 0xc00000
	v_cvt_i32_f32_e32 v176, v176
	v_cvt_i32_f32_sdwa v178, v178 dst_sel:WORD_1 dst_unused:UNUSED_PAD src0_sel:DWORD
	v_cvt_i32_f32_e32 v179, v179
	v_mul_f32_e32 v172, v172, v67
	v_mul_f32_e32 v174, v174, v67
	v_mul_f32_e32 v175, v175, v67
	v_rndne_f32_e32 v173, v173
	v_or3_b32 v186, v184, v185, v186
	v_add_co_u32_e32 v184, vcc, s40, v58
	v_lshlrev_b32_e32 v181, 8, v181
	v_rndne_f32_e32 v172, v172
	v_cvt_i32_f32_e32 v173, v173
	v_rndne_f32_e32 v174, v174
	v_rndne_f32_e32 v175, v175
	v_mul_f32_e32 v169, v169, v67
	v_addc_co_u32_e32 v185, vcc, 0, v59, vcc
	v_and_b32_e32 v181, 0xff00, v181
	v_and_b32_e32 v182, 0xff0000, v182
	v_perm_b32 v180, v183, v180, s70
	s_mov_b32 s40, 0x1000000
	v_cvt_i32_f32_e32 v172, v172
	v_cvt_i32_f32_sdwa v174, v174 dst_sel:WORD_1 dst_unused:UNUSED_PAD src0_sel:DWORD
	v_cvt_i32_f32_e32 v175, v175
	v_mul_f32_e32 v168, v168, v67
	v_mul_f32_e32 v170, v170, v67
	v_mul_f32_e32 v171, v171, v67
	v_rndne_f32_e32 v169, v169
	v_or3_b32 v182, v180, v181, v182
	v_add_co_u32_e32 v180, vcc, s40, v58
	v_lshlrev_b32_e32 v177, 8, v177
	v_rndne_f32_e32 v168, v168
	v_cvt_i32_f32_e32 v169, v169
	v_rndne_f32_e32 v170, v170
	v_rndne_f32_e32 v171, v171
	v_mul_f32_e32 v165, v165, v67
	v_addc_co_u32_e32 v181, vcc, 0, v59, vcc
	v_and_b32_e32 v177, 0xff00, v177
	v_and_b32_e32 v178, 0xff0000, v178
	v_perm_b32 v176, v179, v176, s70
	s_mov_b32 s40, 0x1400000
	v_cvt_i32_f32_e32 v168, v168
	v_cvt_i32_f32_sdwa v170, v170 dst_sel:WORD_1 dst_unused:UNUSED_PAD src0_sel:DWORD
	v_cvt_i32_f32_e32 v171, v171
	v_mul_f32_e32 v164, v164, v67
	v_mul_f32_e32 v166, v166, v67
	v_mul_f32_e32 v167, v167, v67
	v_rndne_f32_e32 v165, v165
	v_or3_b32 v178, v176, v177, v178
; __device__ __forceinline__ void pt_proc(unsigned char* PT, const f32x4* v, int r, int lane) {
;     ...
;     for (int j = 0; j < 16; ++j) ((unsigned*)(tab + (size_t)j * PT_SLICE + (size_t)e * 256))[lane] = pack_i8x4(v[j].x * scale, v[j].y * scale, v[j].z * scale, v[j].w * scale);
;     if (lane == 0) ((float*)(PT + (tb ? PT_VS : PT_US)))[e] = amax * (1.f / 127.f);
	v_add_co_u32_e32 v176, vcc, s40, v58
	v_lshlrev_b32_e32 v173, 8, v173
	v_rndne_f32_e32 v164, v164
	v_cvt_i32_f32_e32 v165, v165
	v_rndne_f32_e32 v166, v166
	v_rndne_f32_e32 v167, v167
	v_mul_f32_e32 v161, v161, v67
	v_addc_co_u32_e32 v177, vcc, 0, v59, vcc
	v_and_b32_e32 v173, 0xff00, v173
	v_and_b32_e32 v174, 0xff0000, v174
	v_perm_b32 v172, v175, v172, s70
	s_mov_b32 s40, 0x1800000
	v_cvt_i32_f32_e32 v164, v164
	v_cvt_i32_f32_sdwa v166, v166 dst_sel:WORD_1 dst_unused:UNUSED_PAD src0_sel:DWORD
	v_cvt_i32_f32_e32 v167, v167
	v_mul_f32_e32 v160, v160, v67
	v_mul_f32_e32 v162, v162, v67
	v_mul_f32_e32 v163, v163, v67
	v_rndne_f32_e32 v161, v161
	v_or3_b32 v174, v172, v173, v174
	v_add_co_u32_e32 v172, vcc, s40, v58
	v_lshlrev_b32_e32 v169, 8, v169
	v_rndne_f32_e32 v160, v160
	v_cvt_i32_f32_e32 v161, v161
	v_rndne_f32_e32 v162, v162
	v_rndne_f32_e32 v163, v163
	v_mul_f32_e32 v157, v157, v67
	v_addc_co_u32_e32 v173, vcc, 0, v59, vcc
	v_and_b32_e32 v169, 0xff00, v169
	v_and_b32_e32 v170, 0xff0000, v170
	v_perm_b32 v168, v171, v168, s70
	s_mov_b32 s40, 0x1c00000
	v_cvt_i32_f32_e32 v160, v160
	v_cvt_i32_f32_sdwa v162, v162 dst_sel:WORD_1 dst_unused:UNUSED_PAD src0_sel:DWORD
	v_cvt_i32_f32_e32 v163, v163
	v_mul_f32_e32 v156, v156, v67
	v_mul_f32_e32 v158, v158, v67
	v_mul_f32_e32 v159, v159, v67
	v_rndne_f32_e32 v157, v157
	v_or3_b32 v170, v168, v169, v170
	v_add_co_u32_e32 v168, vcc, s40, v58
	v_lshlrev_b32_e32 v165, 8, v165
	v_rndne_f32_e32 v156, v156
	v_cvt_i32_f32_e32 v157, v157
	v_rndne_f32_e32 v158, v158
	v_rndne_f32_e32 v159, v159
	v_mul_f32_e32 v153, v153, v67
	v_addc_co_u32_e32 v169, vcc, 0, v59, vcc
	v_and_b32_e32 v165, 0xff00, v165
	v_and_b32_e32 v166, 0xff0000, v166
	v_perm_b32 v164, v167, v164, s70
	s_brev_b32 s40, 64
	v_cvt_i32_f32_e32 v156, v156
	v_cvt_i32_f32_sdwa v158, v158 dst_sel:WORD_1 dst_unused:UNUSED_PAD src0_sel:DWORD
	v_cvt_i32_f32_e32 v159, v159
	v_mul_f32_e32 v152, v152, v67
	v_mul_f32_e32 v154, v154, v67
	v_mul_f32_e32 v155, v155, v67
	v_rndne_f32_e32 v153, v153
	v_or3_b32 v166, v164, v165, v166
	v_add_co_u32_e32 v164, vcc, s40, v58
	v_lshlrev_b32_e32 v161, 8, v161
	v_rndne_f32_e32 v152, v152
	v_cvt_i32_f32_e32 v153, v153
	v_rndne_f32_e32 v154, v154
	v_rndne_f32_e32 v155, v155
	v_mul_f32_e32 v149, v149, v67
	v_addc_co_u32_e32 v165, vcc, 0, v59, vcc
	v_and_b32_e32 v161, 0xff00, v161
	v_and_b32_e32 v162, 0xff0000, v162
	v_perm_b32 v160, v163, v160, s70
	s_mov_b32 s40, 0x2400000
	v_cvt_i32_f32_e32 v152, v152
	v_cvt_i32_f32_sdwa v154, v154 dst_sel:WORD_1 dst_unused:UNUSED_PAD src0_sel:DWORD
	v_cvt_i32_f32_e32 v155, v155
	v_mul_f32_e32 v148, v148, v67
	v_mul_f32_e32 v150, v150, v67
	v_mul_f32_e32 v151, v151, v67
	v_rndne_f32_e32 v149, v149
	v_or3_b32 v162, v160, v161, v162
	v_add_co_u32_e32 v160, vcc, s40, v58
	v_lshlrev_b32_e32 v157, 8, v157
	v_rndne_f32_e32 v148, v148
	v_cvt_i32_f32_e32 v149, v149
	v_rndne_f32_e32 v150, v150
	v_rndne_f32_e32 v151, v151
	v_mul_f32_e32 v145, v145, v67
	v_addc_co_u32_e32 v161, vcc, 0, v59, vcc
	v_and_b32_e32 v157, 0xff00, v157
	v_and_b32_e32 v158, 0xff0000, v158
	v_perm_b32 v156, v159, v156, s70
	s_mov_b32 s40, 0x2800000
	v_cvt_i32_f32_e32 v148, v148
	v_cvt_i32_f32_sdwa v150, v150 dst_sel:WORD_1 dst_unused:UNUSED_PAD src0_sel:DWORD
	v_cvt_i32_f32_e32 v151, v151
	v_mul_f32_e32 v144, v144, v67
	v_mul_f32_e32 v146, v146, v67
	v_mul_f32_e32 v147, v147, v67
	v_rndne_f32_e32 v145, v145
	v_or3_b32 v158, v156, v157, v158
	v_add_co_u32_e32 v156, vcc, s40, v58
	v_lshlrev_b32_e32 v153, 8, v153
	v_rndne_f32_e32 v144, v144
	v_cvt_i32_f32_e32 v145, v145
	v_rndne_f32_e32 v146, v146
	v_rndne_f32_e32 v147, v147
	v_mul_f32_e32 v141, v141, v67
	v_addc_co_u32_e32 v157, vcc, 0, v59, vcc
	v_and_b32_e32 v153, 0xff00, v153
	v_and_b32_e32 v154, 0xff0000, v154
	v_perm_b32 v152, v155, v152, s70
	v_cvt_i32_f32_e32 v144, v144
	v_cvt_i32_f32_sdwa v146, v146 dst_sel:WORD_1 dst_unused:UNUSED_PAD src0_sel:DWORD
	v_cvt_i32_f32_e32 v147, v147
	v_mul_f32_e32 v140, v140, v67
	v_mul_f32_e32 v142, v142, v67
	v_mul_f32_e32 v143, v143, v67
	v_rndne_f32_e32 v141, v141
	v_or3_b32 v154, v152, v153, v154
	v_add_co_u32_e32 v152, vcc, s71, v58
	v_lshlrev_b32_e32 v149, 8, v149
	v_rndne_f32_e32 v140, v140
	v_cvt_i32_f32_e32 v141, v141
	v_rndne_f32_e32 v142, v142
	v_rndne_f32_e32 v143, v143
	v_mul_f32_e32 v137, v137, v67
	v_addc_co_u32_e32 v153, vcc, 0, v59, vcc
	v_and_b32_e32 v149, 0xff00, v149
	v_and_b32_e32 v150, 0xff0000, v150
	v_perm_b32 v148, v151, v148, s70
	v_cvt_i32_f32_e32 v140, v140
	v_cvt_i32_f32_sdwa v142, v142 dst_sel:WORD_1 dst_unused:UNUSED_PAD src0_sel:DWORD
	v_cvt_i32_f32_e32 v143, v143
	v_mul_f32_e32 v136, v136, v67
	v_mul_f32_e32 v138, v138, v67
	v_mul_f32_e32 v139, v139, v67
	v_rndne_f32_e32 v137, v137
	v_or3_b32 v150, v148, v149, v150
	v_add_co_u32_e32 v148, vcc, s72, v58
	v_lshlrev_b32_e32 v145, 8, v145
	v_rndne_f32_e32 v136, v136
	v_cvt_i32_f32_e32 v137, v137
	v_rndne_f32_e32 v138, v138
	v_rndne_f32_e32 v139, v139
	v_addc_co_u32_e32 v149, vcc, 0, v59, vcc
	v_and_b32_e32 v145, 0xff00, v145
	v_and_b32_e32 v146, 0xff0000, v146
	v_perm_b32 v144, v147, v144, s70
	v_cvt_i32_f32_e32 v136, v136
	v_cvt_i32_f32_sdwa v138, v138 dst_sel:WORD_1 dst_unused:UNUSED_PAD src0_sel:DWORD
	v_cvt_i32_f32_e32 v139, v139
	v_or3_b32 v146, v144, v145, v146
	v_add_co_u32_e32 v144, vcc, s73, v58
	v_lshlrev_b32_e32 v141, 8, v141
	s_nop 0
	v_addc_co_u32_e32 v145, vcc, 0, v59, vcc
	v_and_b32_e32 v141, 0xff00, v141
	v_and_b32_e32 v142, 0xff0000, v142
	v_perm_b32 v140, v143, v140, s70
	v_or3_b32 v142, v140, v141, v142
	v_add_co_u32_e32 v140, vcc, s74, v58
	v_lshlrev_b32_e32 v137, 8, v137
	s_nop 0
	v_addc_co_u32_e32 v141, vcc, 0, v59, vcc
	v_and_b32_e32 v137, 0xff00, v137
	v_and_b32_e32 v138, 0xff0000, v138
	v_perm_b32 v136, v139, v136, s70
	v_or3_b32 v138, v136, v137, v138
	v_add_co_u32_e32 v136, vcc, 0x3c00000, v58
	global_store_dword v[216:217], v218, off nt
	s_nop 0
	v_addc_co_u32_e32 v137, vcc, 0, v59, vcc
	global_store_dword v[188:189], v190, off nt
	global_store_dword v[184:185], v186, off nt
	global_store_dword v[180:181], v182, off nt
	global_store_dword v[176:177], v178, off nt
	global_store_dword v[172:173], v174, off nt
	global_store_dword v[168:169], v170, off nt
	global_store_dword v[164:165], v166, off nt
	global_store_dword v[160:161], v162, off nt
	global_store_dword v[156:157], v158, off nt
	global_store_dword v[152:153], v154, off nt
	global_store_dword v[148:149], v150, off nt
	global_store_dword v[144:145], v146, off nt
	global_store_dword v[140:141], v142, off nt
	global_store_dword v[136:137], v138, off nt
	s_and_saveexec_b64 s[40:41], s[6:7]
	s_cbranch_execz .Lside_jB
	s_and_b64 s[38:39], s[38:39], exec
	s_cselect_b32 s38, s75, 0x8010000
	s_add_u32 s38, s33, s38
	s_addc_u32 s39, s46, 0
	s_lshl_b32 s34, s34, 2
	v_mul_f32_e32 v136, 0x3c010204, v66
	v_mov_b32_e32 v137, s34
	global_store_dword v137, v136, s[38:39] nt
	s_branch .Lside_jB

; __device__ __forceinline__ void pt_proc(unsigned char* PT, const f32x4* v, int r, int lane) {
;     const int tb = r >> 14, e = r & 16383; unsigned char* tab = PT + (tb ? PT_V8 : 0); float amax = 0.f;
; #pragma unroll
;     for (int j = 0; j < 16; ++j) amax = fmaxf(fmaxf(amax, fmaxf(fabsf(v[j].x), fabsf(v[j].y))), fmaxf(fabsf(v[j].z), fabsf(v[j].w)));
;     amax = wave_max(amax); const float scale = amax > 0.f ? 127.f / amax : 0.f;
.LBB0_216:
	s_waitcnt vmcnt(1)
	v_max_f32_e64 v131, |v27|, |v27|
	v_max_f32_e64 v132, |v26|, |v26|
	v_max_f32_e32 v131, v132, v131
	v_max_f32_e64 v132, |v29|, |v29|
	v_max_f32_e64 v134, |v28|, |v28|
	v_max_f32_e32 v132, v134, v132
	v_max3_f32 v131, v131, 0, v132
	v_max_f32_e64 v132, |v3|, |v3|
	v_max_f32_e64 v134, |v2|, |v2|
	v_max_f32_e32 v132, v134, v132
	v_max_f32_e64 v134, |v5|, |v5|
	v_max_f32_e64 v135, |v4|, |v4|
	v_max_f32_e32 v134, v135, v134
	v_max3_f32 v131, v131, v132, v134
	v_max_f32_e64 v132, |v7|, |v7|
	v_max_f32_e64 v134, |v6|, |v6|
	v_max_f32_e32 v132, v134, v132
	v_max_f32_e64 v134, |v9|, |v9|
	v_max_f32_e64 v135, |v8|, |v8|
	v_max_f32_e32 v134, v135, v134
	v_max3_f32 v131, v131, v132, v134
	v_max_f32_e64 v132, |v11|, |v11|
	v_max_f32_e64 v134, |v10|, |v10|
	v_max_f32_e32 v132, v134, v132
	v_max_f32_e64 v134, |v13|, |v13|
	v_max_f32_e64 v135, |v12|, |v12|
	v_max_f32_e32 v134, v135, v134
	v_max3_f32 v131, v131, v132, v134
	v_max_f32_e64 v132, |v15|, |v15|
	v_max_f32_e64 v134, |v14|, |v14|
	v_max_f32_e32 v132, v134, v132
	v_max_f32_e64 v134, |v17|, |v17|
	v_max_f32_e64 v135, |v16|, |v16|
	v_max_f32_e32 v134, v135, v134
	v_max3_f32 v131, v131, v132, v134
	v_max_f32_e64 v132, |v19|, |v19|
	v_max_f32_e64 v134, |v18|, |v18|
	v_max_f32_e32 v132, v134, v132
	v_max_f32_e64 v134, |v21|, |v21|
	v_max_f32_e64 v135, |v20|, |v20|
	v_max_f32_e32 v134, v135, v134
	v_max3_f32 v131, v131, v132, v134
	v_max_f32_e64 v132, |v23|, |v23|
	v_max_f32_e64 v134, |v22|, |v22|
	v_max_f32_e32 v132, v134, v132
	v_max_f32_e64 v134, |v25|, |v25|
	v_max_f32_e64 v135, |v24|, |v24|
	v_max_f32_e32 v134, v135, v134
	v_max3_f32 v131, v131, v132, v134
	v_max_f32_e64 v132, |v39|, |v39|
	v_max_f32_e64 v134, |v38|, |v38|
	v_max_f32_e32 v132, v134, v132
	v_max_f32_e64 v134, |v41|, |v41|
	v_max_f32_e64 v135, |v40|, |v40|
	v_max_f32_e32 v134, v135, v134
	v_max3_f32 v131, v131, v132, v134
	v_max_f32_e64 v132, |v31|, |v31|
	v_max_f32_e64 v134, |v30|, |v30|
	v_max_f32_e32 v132, v134, v132
	v_max_f32_e64 v134, |v33|, |v33|
	v_max_f32_e64 v135, |v32|, |v32|
	v_max_f32_e32 v134, v135, v134
	v_max3_f32 v131, v131, v132, v134
	v_max_f32_e64 v132, |v35|, |v35|
	v_max_f32_e64 v134, |v34|, |v34|
	v_max_f32_e32 v132, v134, v132
	v_max_f32_e64 v134, |v37|, |v37|
	v_max_f32_e64 v135, |v36|, |v36|
	v_max_f32_e32 v134, v135, v134
	v_max3_f32 v131, v131, v132, v134
	v_max_f32_e64 v132, |v43|, |v43|
	v_max_f32_e64 v134, |v42|, |v42|
	v_max_f32_e32 v132, v134, v132
	v_max_f32_e64 v134, |v45|, |v45|
	v_max_f32_e64 v135, |v44|, |v44|
	v_max_f32_e32 v134, v135, v134
	v_max3_f32 v131, v131, v132, v134
	v_max_f32_e64 v132, |v47|, |v47|
	v_max_f32_e64 v134, |v46|, |v46|
	v_max_f32_e32 v132, v134, v132
	v_max_f32_e64 v134, |v49|, |v49|
	v_max_f32_e64 v135, |v48|, |v48|
	v_max_f32_e32 v134, v135, v134
	v_max3_f32 v131, v131, v132, v134
	v_max_f32_e64 v132, |v51|, |v51|
	v_max_f32_e64 v134, |v50|, |v50|
	v_max_f32_e32 v132, v134, v132
	v_max_f32_e64 v134, |v53|, |v53|
	v_max_f32_e64 v135, |v52|, |v52|
	v_max_f32_e32 v134, v135, v134
	v_max3_f32 v131, v131, v132, v134
	v_max_f32_e64 v132, |v55|, |v55|
	v_max_f32_e64 v134, |v54|, |v54|
	v_max_f32_e32 v132, v134, v132
	v_max_f32_e64 v134, |v57|, |v57|
	v_max_f32_e64 v135, |v56|, |v56|
	v_max_f32_e32 v134, v135, v134
	v_max3_f32 v131, v131, v132, v134
	v_max_f32_e64 v132, |v59|, |v59|
	v_max_f32_e64 v134, |v58|, |v58|
	v_max_f32_e32 v132, v134, v132
	v_max_f32_e64 v134, |v61|, |v61|
	v_max_f32_e64 v135, |v60|, |v60|
	v_max_f32_e32 v134, v135, v134
	v_max3_f32 v131, v131, v132, v134
	s_waitcnt vmcnt(0)
	v_max_f32_e64 v132, |v63|, |v63|
	v_max_f32_e64 v134, |v62|, |v62|
	v_max_f32_e32 v132, v134, v132
	v_max_f32_e64 v134, |v65|, |v65|
	v_max_f32_e64 v135, |v64|, |v64|
	v_max_f32_e32 v134, v135, v134
	v_max3_f32 v131, v131, v132, v134
	ds_bpermute_b32 v132, v1, v131
	s_add_i32 s45, s16, s17
	s_cmpk_lt_u32 s45, 0x4000
	s_cselect_b64 s[2:3], -1, 0
	s_and_b64 s[4:5], s[2:3], exec
	s_waitcnt lgkmcnt(0)
	v_max_f32_e32 v132, v132, v132
	v_max_f32_e32 v131, v131, v132
	ds_bpermute_b32 v132, v136, v131
	s_cselect_b32 s47, 0, 0x4000000
	s_and_b32 s45, s45, 0x3fff
	s_waitcnt lgkmcnt(0)
	v_max_f32_e32 v132, v132, v132
	v_max_f32_e32 v131, v131, v132
	ds_bpermute_b32 v132, v137, v131
	s_waitcnt lgkmcnt(0)
	v_max_f32_e32 v132, v132, v132
	v_max_f32_e32 v131, v131, v132
	ds_bpermute_b32 v132, v138, v131
	s_waitcnt lgkmcnt(0)
	v_max_f32_e32 v132, v132, v132
	v_max_f32_e32 v131, v131, v132
	ds_bpermute_b32 v132, v139, v131
	s_waitcnt lgkmcnt(0)
	v_max_f32_e32 v132, v132, v132
	v_max_f32_e32 v131, v131, v132
	ds_bpermute_b32 v132, v140, v131
	s_waitcnt lgkmcnt(0)
; __device__ __forceinline__ void pt_proc(unsigned char* PT, const f32x4* v, int r, int lane) {
;     ...
;     amax = wave_max(amax); const float scale = amax > 0.f ? 127.f / amax : 0.f;
; #pragma unroll
;     for (int j = 0; j < 16; ++j) ((unsigned*)(tab + (size_t)j * PT_SLICE + (size_t)e * 256))[lane] = pack_i8x4(v[j].x * scale, v[j].y * scale, v[j].z * scale, v[j].w * scale);
	v_max_f32_e32 v132, v132, v132
	v_max_f32_e32 v131, v131, v132
	v_div_scale_f32 v132, s[4:5], v131, v131, s25
	v_rcp_f32_e32 v134, v132
	s_add_u32 s4, s33, s47
	s_addc_u32 s5, s46, 0
	s_lshl_b32 s47, s45, 8
	v_fma_f32 v135, -v132, v134, 1.0
	v_fmac_f32_e32 v134, v135, v134
	v_div_scale_f32 v135, vcc, s25, v131, s25
	v_mul_f32_e32 v141, v135, v134
	v_fma_f32 v142, -v132, v141, v135
	v_fmac_f32_e32 v141, v142, v134
	v_fma_f32 v132, -v132, v141, v135
	v_div_fmas_f32 v132, v132, v134, v141
	v_div_fixup_f32 v132, v132, v131, s25
	v_cmp_lt_f32_e32 vcc, 0, v131
	s_add_u32 s4, s4, s47
	s_addc_u32 s5, s5, 0
	v_cndmask_b32_e32 v141, 0, v132, vcc
	v_mul_f32_e32 v143, v27, v141
	v_mul_f32_e32 v142, v26, v141
	v_mul_f32_e32 v144, v28, v141
	v_mul_f32_e32 v145, v29, v141
	v_rndne_f32_e32 v143, v143
	v_rndne_f32_e32 v142, v142
	v_cvt_i32_f32_e32 v143, v143
	v_rndne_f32_e32 v144, v144
	v_rndne_f32_e32 v145, v145
	v_cvt_i32_f32_e32 v142, v142
	v_cvt_i32_f32_sdwa v144, v144 dst_sel:WORD_1 dst_unused:UNUSED_PAD src0_sel:DWORD
	v_cvt_i32_f32_e32 v145, v145
	v_lshlrev_b32_e32 v143, 8, v143
	v_and_b32_e32 v143, 0xff00, v143
	v_and_b32_e32 v144, 0xff0000, v144
	v_perm_b32 v142, v145, v142, s26
	v_lshlrev_b32_e32 v132, 2, v194
	v_or3_b32 v142, v142, v143, v144
	v_mul_f32_e32 v143, v3, v141
	global_store_dword v132, v142, s[4:5] nt
	v_mul_f32_e32 v142, v2, v141
	v_mul_f32_e32 v144, v4, v141
	v_mul_f32_e32 v145, v5, v141
	v_rndne_f32_e32 v143, v143
	v_rndne_f32_e32 v142, v142
	v_cvt_i32_f32_e32 v143, v143
	v_rndne_f32_e32 v144, v144
	v_rndne_f32_e32 v145, v145
	v_cvt_i32_f32_e32 v142, v142
	v_cvt_i32_f32_sdwa v144, v144 dst_sel:WORD_1 dst_unused:UNUSED_PAD src0_sel:DWORD
	v_cvt_i32_f32_e32 v145, v145
	v_lshlrev_b32_e32 v143, 8, v143
	v_lshl_add_u64 v[134:135], s[4:5], 0, v[132:133]
	v_and_b32_e32 v143, 0xff00, v143
	v_and_b32_e32 v144, 0xff0000, v144
	v_perm_b32 v142, v145, v142, s26
	v_or3_b32 v144, v142, v143, v144
	v_add_co_u32_e32 v142, vcc, s27, v134
	v_mul_f32_e32 v145, v9, v141
	s_nop 0
	v_addc_co_u32_e32 v143, vcc, 0, v135, vcc
	global_store_dword v[142:143], v144, off nt
	v_mul_f32_e32 v143, v7, v141
	v_mul_f32_e32 v142, v6, v141
	v_mul_f32_e32 v144, v8, v141
	v_rndne_f32_e32 v143, v143
	v_rndne_f32_e32 v142, v142
	v_cvt_i32_f32_e32 v143, v143
	v_rndne_f32_e32 v144, v144
	v_rndne_f32_e32 v145, v145
	v_cvt_i32_f32_e32 v142, v142
	v_cvt_i32_f32_sdwa v144, v144 dst_sel:WORD_1 dst_unused:UNUSED_PAD src0_sel:DWORD
	v_cvt_i32_f32_e32 v145, v145
	v_lshlrev_b32_e32 v143, 8, v143
	v_and_b32_e32 v143, 0xff00, v143
	v_and_b32_e32 v144, 0xff0000, v144
	v_perm_b32 v142, v145, v142, s26
	v_or3_b32 v144, v142, v143, v144
	v_add_co_u32_e32 v142, vcc, s28, v134
	v_mul_f32_e32 v145, v13, v141
	s_nop 0
	v_addc_co_u32_e32 v143, vcc, 0, v135, vcc
	global_store_dword v[142:143], v144, off nt
	v_mul_f32_e32 v143, v11, v141
	v_mul_f32_e32 v142, v10, v141
	v_mul_f32_e32 v144, v12, v141
	v_rndne_f32_e32 v143, v143
	v_rndne_f32_e32 v142, v142
	v_cvt_i32_f32_e32 v143, v143
	v_rndne_f32_e32 v144, v144
	v_rndne_f32_e32 v145, v145
	v_cvt_i32_f32_e32 v142, v142
	v_cvt_i32_f32_sdwa v144, v144 dst_sel:WORD_1 dst_unused:UNUSED_PAD src0_sel:DWORD
	v_cvt_i32_f32_e32 v145, v145
	v_lshlrev_b32_e32 v143, 8, v143
	v_and_b32_e32 v143, 0xff00, v143
	v_and_b32_e32 v144, 0xff0000, v144
	v_perm_b32 v142, v145, v142, s26
	v_or3_b32 v144, v142, v143, v144
	v_add_co_u32_e32 v142, vcc, s29, v134
	v_mul_f32_e32 v145, v17, v141
	s_nop 0
	v_addc_co_u32_e32 v143, vcc, 0, v135, vcc
	global_store_dword v[142:143], v144, off nt
	v_mul_f32_e32 v143, v15, v141
	v_mul_f32_e32 v142, v14, v141
	v_mul_f32_e32 v144, v16, v141
	v_rndne_f32_e32 v143, v143
	v_rndne_f32_e32 v142, v142
	v_cvt_i32_f32_e32 v143, v143
	v_rndne_f32_e32 v144, v144
	v_rndne_f32_e32 v145, v145
	v_cvt_i32_f32_e32 v142, v142
	v_cvt_i32_f32_sdwa v144, v144 dst_sel:WORD_1 dst_unused:UNUSED_PAD src0_sel:DWORD
	v_cvt_i32_f32_e32 v145, v145
	v_lshlrev_b32_e32 v143, 8, v143
	v_and_b32_e32 v143, 0xff00, v143
	v_and_b32_e32 v144, 0xff0000, v144
	v_perm_b32 v142, v145, v142, s26
	v_or3_b32 v144, v142, v143, v144
	v_add_co_u32_e32 v142, vcc, s30, v134
	v_mul_f32_e32 v145, v21, v141
	s_nop 0
	v_addc_co_u32_e32 v143, vcc, 0, v135, vcc
	global_store_dword v[142:143], v144, off nt
	v_mul_f32_e32 v143, v19, v141
	v_mul_f32_e32 v142, v18, v141
	v_mul_f32_e32 v144, v20, v141
	v_rndne_f32_e32 v143, v143
	v_rndne_f32_e32 v142, v142
	v_cvt_i32_f32_e32 v143, v143
	v_rndne_f32_e32 v144, v144
	v_rndne_f32_e32 v145, v145
	v_cvt_i32_f32_e32 v142, v142
	v_cvt_i32_f32_sdwa v144, v144 dst_sel:WORD_1 dst_unused:UNUSED_PAD src0_sel:DWORD
	v_cvt_i32_f32_e32 v145, v145
	v_lshlrev_b32_e32 v143, 8, v143
	v_and_b32_e32 v143, 0xff00, v143
	v_and_b32_e32 v144, 0xff0000, v144
	v_perm_b32 v142, v145, v142, s26
	v_or3_b32 v144, v142, v143, v144
	v_add_co_u32_e32 v142, vcc, s31, v134
	v_mul_f32_e32 v145, v25, v141
	s_nop 0
	v_addc_co_u32_e32 v143, vcc, 0, v135, vcc
	global_store_dword v[142:143], v144, off nt
	v_mul_f32_e32 v143, v23, v141
	v_mul_f32_e32 v142, v22, v141
	v_mul_f32_e32 v144, v24, v141
	v_rndne_f32_e32 v143, v143
	v_rndne_f32_e32 v142, v142
	v_cvt_i32_f32_e32 v143, v143
	v_rndne_f32_e32 v144, v144
	v_rndne_f32_e32 v145, v145
	v_cvt_i32_f32_e32 v142, v142
	v_cvt_i32_f32_sdwa v144, v144 dst_sel:WORD_1 dst_unused:UNUSED_PAD src0_sel:DWORD
	v_cvt_i32_f32_e32 v145, v145
	v_lshlrev_b32_e32 v143, 8, v143
	v_and_b32_e32 v143, 0xff00, v143
	v_and_b32_e32 v144, 0xff0000, v144
	v_perm_b32 v142, v145, v142, s26
	v_or3_b32 v144, v142, v143, v144
	v_add_co_u32_e32 v142, vcc, s34, v134
	v_mul_f32_e32 v145, v41, v141
	s_nop 0
	v_addc_co_u32_e32 v143, vcc, 0, v135, vcc
; __device__ __forceinline__ void pt_proc(unsigned char* PT, const f32x4* v, int r, int lane) {
;     ...
;     for (int j = 0; j < 16; ++j) ((unsigned*)(tab + (size_t)j * PT_SLICE + (size_t)e * 256))[lane] = pack_i8x4(v[j].x * scale, v[j].y * scale, v[j].z * scale, v[j].w * scale);
;     if (lane == 0) ((float*)(PT + (tb ? PT_VS : PT_US)))[e] = amax * (1.f / 127.f);
; __device__ __forceinline__ void phase_peer_tables(const Frame& F, const Args& a, int r_lo, int r_hi, int gw, int NGW) {
;     ...
;     for (;;) {
;         const int r1 = r + NGW; const bool h1 = r1 < r_hi;
;         if (h1) pt_load(a.in[17], a.in[18], vB, r1, lane);
;         pt_proc(PT, vA, r, lane);
;         if (!h1) break;
;         const int r2 = r1 + NGW; const bool h2 = r2 < r_hi;
;         if (h2) pt_load(a.in[17], a.in[18], vA, r2, lane);
;         pt_proc(PT, vB, r1, lane);
;         if (!h2) break;
;         r = r2;
;     }
	global_store_dword v[142:143], v144, off nt
	v_mul_f32_e32 v143, v39, v141
	v_mul_f32_e32 v142, v38, v141
	v_mul_f32_e32 v144, v40, v141
	v_rndne_f32_e32 v143, v143
	v_rndne_f32_e32 v142, v142
	v_cvt_i32_f32_e32 v143, v143
	v_rndne_f32_e32 v144, v144
	v_rndne_f32_e32 v145, v145
	v_cvt_i32_f32_e32 v142, v142
	v_cvt_i32_f32_sdwa v144, v144 dst_sel:WORD_1 dst_unused:UNUSED_PAD src0_sel:DWORD
	v_cvt_i32_f32_e32 v145, v145
	v_lshlrev_b32_e32 v143, 8, v143
	v_and_b32_e32 v143, 0xff00, v143
	v_and_b32_e32 v144, 0xff0000, v144
	v_perm_b32 v142, v145, v142, s26
	v_or3_b32 v144, v142, v143, v144
	v_add_co_u32_e32 v142, vcc, s35, v134
	v_mul_f32_e32 v145, v33, v141
	s_nop 0
	v_addc_co_u32_e32 v143, vcc, 0, v135, vcc
	global_store_dword v[142:143], v144, off nt
	v_mul_f32_e32 v143, v31, v141
	v_mul_f32_e32 v142, v30, v141
	v_mul_f32_e32 v144, v32, v141
	v_rndne_f32_e32 v143, v143
	v_rndne_f32_e32 v142, v142
	v_cvt_i32_f32_e32 v143, v143
	v_rndne_f32_e32 v144, v144
	v_rndne_f32_e32 v145, v145
	v_cvt_i32_f32_e32 v142, v142
	v_cvt_i32_f32_sdwa v144, v144 dst_sel:WORD_1 dst_unused:UNUSED_PAD src0_sel:DWORD
	v_cvt_i32_f32_e32 v145, v145
	v_lshlrev_b32_e32 v143, 8, v143
	v_and_b32_e32 v143, 0xff00, v143
	v_and_b32_e32 v144, 0xff0000, v144
	v_perm_b32 v142, v145, v142, s26
	v_or3_b32 v144, v142, v143, v144
	v_add_co_u32_e32 v142, vcc, s36, v134
	v_mul_f32_e32 v145, v37, v141
	s_nop 0
	v_addc_co_u32_e32 v143, vcc, 0, v135, vcc
	global_store_dword v[142:143], v144, off nt
	v_mul_f32_e32 v143, v35, v141
	v_mul_f32_e32 v142, v34, v141
	v_mul_f32_e32 v144, v36, v141
	v_rndne_f32_e32 v143, v143
	v_rndne_f32_e32 v142, v142
	v_cvt_i32_f32_e32 v143, v143
	v_rndne_f32_e32 v144, v144
	v_rndne_f32_e32 v145, v145
	v_cvt_i32_f32_e32 v142, v142
	v_cvt_i32_f32_sdwa v144, v144 dst_sel:WORD_1 dst_unused:UNUSED_PAD src0_sel:DWORD
	v_cvt_i32_f32_e32 v145, v145
	v_lshlrev_b32_e32 v143, 8, v143
	v_and_b32_e32 v143, 0xff00, v143
	v_and_b32_e32 v144, 0xff0000, v144
	v_perm_b32 v142, v145, v142, s26
	v_or3_b32 v144, v142, v143, v144
	v_add_co_u32_e32 v142, vcc, s37, v134
	v_mul_f32_e32 v145, v45, v141
	s_nop 0
	v_addc_co_u32_e32 v143, vcc, 0, v135, vcc
	global_store_dword v[142:143], v144, off nt
	v_mul_f32_e32 v143, v43, v141
	v_mul_f32_e32 v142, v42, v141
	v_mul_f32_e32 v144, v44, v141
	v_rndne_f32_e32 v143, v143
	v_rndne_f32_e32 v142, v142
	v_cvt_i32_f32_e32 v143, v143
	v_rndne_f32_e32 v144, v144
	v_rndne_f32_e32 v145, v145
	v_cvt_i32_f32_e32 v142, v142
	v_cvt_i32_f32_sdwa v144, v144 dst_sel:WORD_1 dst_unused:UNUSED_PAD src0_sel:DWORD
	v_cvt_i32_f32_e32 v145, v145
	v_lshlrev_b32_e32 v143, 8, v143
	v_and_b32_e32 v143, 0xff00, v143
	v_and_b32_e32 v144, 0xff0000, v144
	v_perm_b32 v142, v145, v142, s26
	v_or3_b32 v144, v142, v143, v144
	v_add_co_u32_e32 v142, vcc, s38, v134
	v_mul_f32_e32 v145, v49, v141
	s_nop 0
	v_addc_co_u32_e32 v143, vcc, 0, v135, vcc
	global_store_dword v[142:143], v144, off nt
	v_mul_f32_e32 v143, v47, v141
	v_mul_f32_e32 v142, v46, v141
	v_mul_f32_e32 v144, v48, v141
	v_rndne_f32_e32 v143, v143
	v_rndne_f32_e32 v142, v142
	v_cvt_i32_f32_e32 v143, v143
	v_rndne_f32_e32 v144, v144
	v_rndne_f32_e32 v145, v145
	v_cvt_i32_f32_e32 v142, v142
	v_cvt_i32_f32_sdwa v144, v144 dst_sel:WORD_1 dst_unused:UNUSED_PAD src0_sel:DWORD
	v_cvt_i32_f32_e32 v145, v145
	v_lshlrev_b32_e32 v143, 8, v143
	v_and_b32_e32 v143, 0xff00, v143
	v_and_b32_e32 v144, 0xff0000, v144
	v_perm_b32 v142, v145, v142, s26
	v_or3_b32 v144, v142, v143, v144
	v_add_co_u32_e32 v142, vcc, s39, v134
	v_mul_f32_e32 v145, v53, v141
	s_nop 0
	v_addc_co_u32_e32 v143, vcc, 0, v135, vcc
	global_store_dword v[142:143], v144, off nt
	v_mul_f32_e32 v143, v51, v141
	v_mul_f32_e32 v142, v50, v141
	v_mul_f32_e32 v144, v52, v141
	v_rndne_f32_e32 v143, v143
	v_rndne_f32_e32 v142, v142
	v_cvt_i32_f32_e32 v143, v143
	v_rndne_f32_e32 v144, v144
	v_rndne_f32_e32 v145, v145
	v_cvt_i32_f32_e32 v142, v142
	v_cvt_i32_f32_sdwa v144, v144 dst_sel:WORD_1 dst_unused:UNUSED_PAD src0_sel:DWORD
	v_cvt_i32_f32_e32 v145, v145
	v_lshlrev_b32_e32 v143, 8, v143
	v_and_b32_e32 v143, 0xff00, v143
	v_and_b32_e32 v144, 0xff0000, v144
	v_perm_b32 v142, v145, v142, s26
	v_or3_b32 v144, v142, v143, v144
	v_add_co_u32_e32 v142, vcc, s40, v134
	v_mul_f32_e32 v145, v57, v141
	s_nop 0
	v_addc_co_u32_e32 v143, vcc, 0, v135, vcc
	global_store_dword v[142:143], v144, off nt
	v_mul_f32_e32 v143, v55, v141
	v_mul_f32_e32 v142, v54, v141
	v_mul_f32_e32 v144, v56, v141
	v_rndne_f32_e32 v143, v143
	v_rndne_f32_e32 v142, v142
	v_cvt_i32_f32_e32 v143, v143
	v_rndne_f32_e32 v144, v144
	v_rndne_f32_e32 v145, v145
	v_cvt_i32_f32_e32 v142, v142
	v_cvt_i32_f32_sdwa v144, v144 dst_sel:WORD_1 dst_unused:UNUSED_PAD src0_sel:DWORD
	v_cvt_i32_f32_e32 v145, v145
	v_lshlrev_b32_e32 v143, 8, v143
	v_and_b32_e32 v143, 0xff00, v143
	v_and_b32_e32 v144, 0xff0000, v144
	v_perm_b32 v142, v145, v142, s26
	v_or3_b32 v144, v142, v143, v144
	v_add_co_u32_e32 v142, vcc, s41, v134
	v_mul_f32_e32 v145, v61, v141
	s_nop 0
	v_addc_co_u32_e32 v143, vcc, 0, v135, vcc
	global_store_dword v[142:143], v144, off nt
	v_mul_f32_e32 v143, v59, v141
	v_mul_f32_e32 v142, v58, v141
	v_mul_f32_e32 v144, v60, v141
	v_rndne_f32_e32 v143, v143
	v_rndne_f32_e32 v142, v142
	v_cvt_i32_f32_e32 v143, v143
	v_rndne_f32_e32 v144, v144
	v_rndne_f32_e32 v145, v145
	v_cvt_i32_f32_e32 v142, v142
	v_cvt_i32_f32_sdwa v144, v144 dst_sel:WORD_1 dst_unused:UNUSED_PAD src0_sel:DWORD
	v_cvt_i32_f32_e32 v145, v145
	v_lshlrev_b32_e32 v143, 8, v143
	v_and_b32_e32 v143, 0xff00, v143
	v_and_b32_e32 v144, 0xff0000, v144
	v_perm_b32 v142, v145, v142, s26
	v_or3_b32 v144, v142, v143, v144
	v_add_co_u32_e32 v142, vcc, s42, v134
	s_nop 1
	v_addc_co_u32_e32 v143, vcc, 0, v135, vcc
	global_store_dword v[142:143], v144, off nt
	v_mul_f32_e32 v143, v63, v141
	v_mul_f32_e32 v142, v62, v141
	v_mul_f32_e32 v144, v64, v141
	v_mul_f32_e32 v141, v65, v141
	v_rndne_f32_e32 v143, v143
	v_rndne_f32_e32 v142, v142
	v_cvt_i32_f32_e32 v143, v143
	v_rndne_f32_e32 v144, v144
	v_rndne_f32_e32 v141, v141
	v_cvt_i32_f32_e32 v142, v142
	v_cvt_i32_f32_sdwa v144, v144 dst_sel:WORD_1 dst_unused:UNUSED_PAD src0_sel:DWORD
	v_cvt_i32_f32_e32 v141, v141
	v_lshlrev_b32_e32 v143, 8, v143
	v_and_b32_e32 v143, 0xff00, v143
	v_and_b32_e32 v144, 0xff0000, v144
	v_perm_b32 v141, v141, v142, s26
	v_add_co_u32_e32 v134, vcc, 0x3c00000, v134
	v_or3_b32 v141, v141, v143, v144
	s_nop 0
	v_addc_co_u32_e32 v135, vcc, 0, v135, vcc
	global_store_dword v[134:135], v141, off nt
	s_and_saveexec_b64 s[4:5], s[6:7]
	s_cbranch_execnz .LBB0_218
	s_or_b64 exec, exec, s[4:5]
	s_andn2_b64 vcc, exec, s[0:1]
	s_mov_b64 s[0:1], -1
	s_cbranch_vccnz .LBB0_213
	s_branch .LBB0_219
.LBB0_218:
	s_and_b64 s[2:3], s[2:3], exec
	s_cselect_b32 s2, s43, 0x8010000
	s_add_u32 s2, s33, s2
	s_addc_u32 s3, s46, 0
	s_lshl_b32 s45, s45, 2
	v_mul_f32_e32 v131, 0x3c010204, v131
	v_mov_b32_e32 v134, s45
	global_store_dword v134, v131, s[2:3] nt
	s_or_b64 exec, exec, s[4:5]
	s_andn2_b64 vcc, exec, s[0:1]
	s_mov_b64 s[0:1], -1
	s_cbranch_vccnz .LBB0_213

; __device__ __forceinline__ void pt_proc(unsigned char* PT, const f32x4* v, int r, int lane) {
;     const int tb = r >> 14, e = r & 16383; unsigned char* tab = PT + (tb ? PT_V8 : 0); float amax = 0.f;
; #pragma unroll
;     for (int j = 0; j < 16; ++j) amax = fmaxf(fmaxf(amax, fmaxf(fabsf(v[j].x), fabsf(v[j].y))), fmaxf(fabsf(v[j].z), fabsf(v[j].w)));
;     amax = wave_max(amax); const float scale = amax > 0.f ? 127.f / amax : 0.f;
.LBB0_221:
	v_max_f32_e64 v131, |v79|, |v79|
	v_max_f32_e64 v134, |v78|, |v78|
	v_max_f32_e32 v131, v134, v131
	v_max_f32_e64 v134, |v81|, |v81|
	v_max_f32_e64 v135, |v80|, |v80|
	v_max_f32_e32 v134, v135, v134
	v_max3_f32 v131, v131, 0, v134
	v_max_f32_e64 v134, |v75|, |v75|
	v_max_f32_e64 v135, |v74|, |v74|
	v_max_f32_e32 v134, v135, v134
	v_max_f32_e64 v135, |v77|, |v77|
	v_max_f32_e64 v141, |v76|, |v76|
	v_max_f32_e32 v135, v141, v135
	v_max3_f32 v131, v131, v134, v135
	v_max_f32_e64 v134, |v71|, |v71|
	v_max_f32_e64 v135, |v70|, |v70|
	v_max_f32_e32 v134, v135, v134
	v_max_f32_e64 v135, |v73|, |v73|
	v_max_f32_e64 v141, |v72|, |v72|
	v_max_f32_e32 v135, v141, v135
	v_max3_f32 v131, v131, v134, v135
	v_max_f32_e64 v134, |v67|, |v67|
	v_max_f32_e64 v135, |v66|, |v66|
	v_max_f32_e32 v134, v135, v134
	v_max_f32_e64 v135, |v69|, |v69|
	v_max_f32_e64 v141, |v68|, |v68|
	v_max_f32_e32 v135, v141, v135
	v_max3_f32 v131, v131, v134, v135
	v_max_f32_e64 v134, |v95|, |v95|
	v_max_f32_e64 v135, |v94|, |v94|
	v_max_f32_e32 v134, v135, v134
	v_max_f32_e64 v135, |v97|, |v97|
	v_max_f32_e64 v141, |v96|, |v96|
	v_max_f32_e32 v135, v141, v135
	v_max3_f32 v131, v131, v134, v135
	v_max_f32_e64 v134, |v91|, |v91|
	v_max_f32_e64 v135, |v90|, |v90|
	v_max_f32_e32 v134, v135, v134
	v_max_f32_e64 v135, |v93|, |v93|
	v_max_f32_e64 v141, |v92|, |v92|
	v_max_f32_e32 v135, v141, v135
	v_max3_f32 v131, v131, v134, v135
	v_max_f32_e64 v134, |v87|, |v87|
	v_max_f32_e64 v135, |v86|, |v86|
	v_max_f32_e32 v134, v135, v134
	v_max_f32_e64 v135, |v89|, |v89|
	v_max_f32_e64 v141, |v88|, |v88|
	v_max_f32_e32 v135, v141, v135
	v_max3_f32 v131, v131, v134, v135
	v_max_f32_e64 v134, |v83|, |v83|
	v_max_f32_e64 v135, |v82|, |v82|
	v_max_f32_e32 v134, v135, v134
	v_max_f32_e64 v135, |v85|, |v85|
	v_max_f32_e64 v141, |v84|, |v84|
	v_max_f32_e32 v135, v141, v135
	v_max3_f32 v131, v131, v134, v135
	v_max_f32_e64 v134, |v111|, |v111|
	v_max_f32_e64 v135, |v110|, |v110|
	v_max_f32_e32 v134, v135, v134
	v_max_f32_e64 v135, |v113|, |v113|
	v_max_f32_e64 v141, |v112|, |v112|
	v_max_f32_e32 v135, v141, v135
	v_max3_f32 v131, v131, v134, v135
	v_max_f32_e64 v134, |v107|, |v107|
	v_max_f32_e64 v135, |v106|, |v106|
	v_max_f32_e32 v134, v135, v134
	v_max_f32_e64 v135, |v109|, |v109|
	v_max_f32_e64 v141, |v108|, |v108|
	v_max_f32_e32 v135, v141, v135
	v_max3_f32 v131, v131, v134, v135
	v_max_f32_e64 v134, |v103|, |v103|
	v_max_f32_e64 v135, |v102|, |v102|
	v_max_f32_e32 v134, v135, v134
	v_max_f32_e64 v135, |v105|, |v105|
	v_max_f32_e64 v141, |v104|, |v104|
	v_max_f32_e32 v135, v141, v135
	v_max3_f32 v131, v131, v134, v135
	v_max_f32_e64 v134, |v99|, |v99|
	v_max_f32_e64 v135, |v98|, |v98|
	v_max_f32_e32 v134, v135, v134
	v_max_f32_e64 v135, |v101|, |v101|
	v_max_f32_e64 v141, |v100|, |v100|
	v_max_f32_e32 v135, v141, v135
	v_max3_f32 v131, v131, v134, v135
	v_max_f32_e64 v134, |v127|, |v127|
	v_max_f32_e64 v135, |v126|, |v126|
	v_max_f32_e32 v134, v135, v134
	v_max_f32_e64 v135, |v129|, |v129|
	v_max_f32_e64 v141, |v128|, |v128|
	v_max_f32_e32 v135, v141, v135
	v_max3_f32 v131, v131, v134, v135
	v_max_f32_e64 v134, |v123|, |v123|
	v_max_f32_e64 v135, |v122|, |v122|
	v_max_f32_e32 v134, v135, v134
	v_max_f32_e64 v135, |v125|, |v125|
	v_max_f32_e64 v141, |v124|, |v124|
	v_max_f32_e32 v135, v141, v135
	v_max3_f32 v131, v131, v134, v135
	v_max_f32_e64 v134, |v119|, |v119|
	v_max_f32_e64 v135, |v118|, |v118|
	v_max_f32_e32 v134, v135, v134
	v_max_f32_e64 v135, |v121|, |v121|
	v_max_f32_e64 v141, |v120|, |v120|
	v_max_f32_e32 v135, v141, v135
	v_max3_f32 v131, v131, v134, v135
	v_max_f32_e64 v134, |v115|, |v115|
	v_max_f32_e64 v135, |v114|, |v114|
	v_max_f32_e32 v134, v135, v134
	v_max_f32_e64 v135, |v117|, |v117|
	v_max_f32_e64 v141, |v116|, |v116|
	v_max_f32_e32 v135, v141, v135
	v_max3_f32 v131, v131, v134, v135
	ds_bpermute_b32 v134, v1, v131
	s_cmpk_lt_u32 s44, 0x4000
	s_cselect_b64 s[0:1], -1, 0
	s_and_b64 s[2:3], s[0:1], exec
	s_cselect_b32 s5, 0, 0x4000000
	s_waitcnt lgkmcnt(0)
	v_max_f32_e32 v134, v134, v134
	v_max_f32_e32 v131, v131, v134
	ds_bpermute_b32 v134, v136, v131
	s_and_b32 s4, s44, 0x3fff
	s_waitcnt lgkmcnt(0)
	v_max_f32_e32 v134, v134, v134
	v_max_f32_e32 v131, v131, v134
	ds_bpermute_b32 v134, v137, v131
	s_waitcnt lgkmcnt(0)
	v_max_f32_e32 v134, v134, v134
	v_max_f32_e32 v131, v131, v134
	ds_bpermute_b32 v134, v138, v131
	s_waitcnt lgkmcnt(0)
	v_max_f32_e32 v134, v134, v134
	v_max_f32_e32 v131, v131, v134
	ds_bpermute_b32 v134, v139, v131
	s_waitcnt lgkmcnt(0)
	v_max_f32_e32 v134, v134, v134
	v_max_f32_e32 v131, v131, v134
	ds_bpermute_b32 v134, v140, v131
	s_waitcnt lgkmcnt(0)
; __device__ __forceinline__ void pt_proc(unsigned char* PT, const f32x4* v, int r, int lane) {
;     ...
;     amax = wave_max(amax); const float scale = amax > 0.f ? 127.f / amax : 0.f;
; #pragma unroll
;     for (int j = 0; j < 16; ++j) ((unsigned*)(tab + (size_t)j * PT_SLICE + (size_t)e * 256))[lane] = pack_i8x4(v[j].x * scale, v[j].y * scale, v[j].z * scale, v[j].w * scale);
	v_max_f32_e32 v134, v134, v134
	v_max_f32_e32 v131, v131, v134
	v_div_scale_f32 v134, s[2:3], v131, v131, s25
	v_rcp_f32_e32 v135, v134
	s_add_u32 s2, s33, s5
	s_addc_u32 s3, s46, 0
	s_lshl_b32 s5, s4, 8
	v_fma_f32 v141, -v134, v135, 1.0
	v_fmac_f32_e32 v135, v141, v135
	v_div_scale_f32 v141, vcc, s25, v131, s25
	v_mul_f32_e32 v142, v141, v135
	v_fma_f32 v143, -v134, v142, v141
	v_fmac_f32_e32 v142, v143, v135
	v_fma_f32 v134, -v134, v142, v141
	v_div_fmas_f32 v134, v134, v135, v142
	v_div_fixup_f32 v134, v134, v131, s25
	v_cmp_lt_f32_e32 vcc, 0, v131
	s_add_u32 s2, s2, s5
	s_addc_u32 s3, s3, 0
	v_cndmask_b32_e32 v141, 0, v134, vcc
	v_mul_f32_e32 v143, v79, v141
	v_mul_f32_e32 v142, v78, v141
	v_mul_f32_e32 v144, v80, v141
	v_mul_f32_e32 v145, v81, v141
	v_rndne_f32_e32 v143, v143
	v_rndne_f32_e32 v142, v142
	v_cvt_i32_f32_e32 v143, v143
	v_rndne_f32_e32 v144, v144
	v_rndne_f32_e32 v145, v145
	v_cvt_i32_f32_e32 v142, v142
	v_cvt_i32_f32_sdwa v144, v144 dst_sel:WORD_1 dst_unused:UNUSED_PAD src0_sel:DWORD
	v_cvt_i32_f32_e32 v145, v145
	v_lshlrev_b32_e32 v143, 8, v143
	v_and_b32_e32 v143, 0xff00, v143
	v_and_b32_e32 v144, 0xff0000, v144
	v_perm_b32 v142, v145, v142, s26
	v_or3_b32 v142, v142, v143, v144
	global_store_dword v132, v142, s[2:3] nt
	v_mul_f32_e32 v142, v75, v141
	v_lshl_add_u64 v[134:135], s[2:3], 0, v[132:133]
	v_mul_f32_e32 v132, v74, v141
	v_mul_f32_e32 v143, v76, v141
	v_mul_f32_e32 v144, v77, v141
	v_rndne_f32_e32 v142, v142
	v_rndne_f32_e32 v132, v132
	v_cvt_i32_f32_e32 v142, v142
	v_rndne_f32_e32 v143, v143
	v_rndne_f32_e32 v144, v144
	v_cvt_i32_f32_e32 v132, v132
	v_cvt_i32_f32_sdwa v143, v143 dst_sel:WORD_1 dst_unused:UNUSED_PAD src0_sel:DWORD
	v_cvt_i32_f32_e32 v144, v144
	v_lshlrev_b32_e32 v142, 8, v142
	v_and_b32_e32 v142, 0xff00, v142
	v_and_b32_e32 v143, 0xff0000, v143
	v_perm_b32 v132, v144, v132, s26
	v_or3_b32 v132, v132, v142, v143
	v_add_co_u32_e32 v142, vcc, s27, v134
	v_mul_f32_e32 v144, v73, v141
	s_nop 0
	v_addc_co_u32_e32 v143, vcc, 0, v135, vcc
	global_store_dword v[142:143], v132, off nt
	v_mul_f32_e32 v142, v71, v141
	v_mul_f32_e32 v132, v70, v141
	v_mul_f32_e32 v143, v72, v141
	v_rndne_f32_e32 v142, v142
	v_rndne_f32_e32 v132, v132
	v_cvt_i32_f32_e32 v142, v142
	v_rndne_f32_e32 v143, v143
	v_rndne_f32_e32 v144, v144
	v_cvt_i32_f32_e32 v132, v132
	v_cvt_i32_f32_sdwa v143, v143 dst_sel:WORD_1 dst_unused:UNUSED_PAD src0_sel:DWORD
	v_cvt_i32_f32_e32 v144, v144
	v_lshlrev_b32_e32 v142, 8, v142
	v_and_b32_e32 v142, 0xff00, v142
	v_and_b32_e32 v143, 0xff0000, v143
	v_perm_b32 v132, v144, v132, s26
	v_or3_b32 v132, v132, v142, v143
	v_add_co_u32_e32 v142, vcc, s28, v134
	v_mul_f32_e32 v144, v69, v141
	s_nop 0
	v_addc_co_u32_e32 v143, vcc, 0, v135, vcc
	global_store_dword v[142:143], v132, off nt
	v_mul_f32_e32 v142, v67, v141
	v_mul_f32_e32 v132, v66, v141
	v_mul_f32_e32 v143, v68, v141
	v_rndne_f32_e32 v142, v142
	v_rndne_f32_e32 v132, v132
	v_cvt_i32_f32_e32 v142, v142
	v_rndne_f32_e32 v143, v143
	v_rndne_f32_e32 v144, v144
	v_cvt_i32_f32_e32 v132, v132
	v_cvt_i32_f32_sdwa v143, v143 dst_sel:WORD_1 dst_unused:UNUSED_PAD src0_sel:DWORD
	v_cvt_i32_f32_e32 v144, v144
	v_lshlrev_b32_e32 v142, 8, v142
	v_and_b32_e32 v142, 0xff00, v142
	v_and_b32_e32 v143, 0xff0000, v143
	v_perm_b32 v132, v144, v132, s26
	v_or3_b32 v132, v132, v142, v143
	v_add_co_u32_e32 v142, vcc, s29, v134
	v_mul_f32_e32 v144, v97, v141
	s_nop 0
	v_addc_co_u32_e32 v143, vcc, 0, v135, vcc
	global_store_dword v[142:143], v132, off nt
	v_mul_f32_e32 v142, v95, v141
	v_mul_f32_e32 v132, v94, v141
	v_mul_f32_e32 v143, v96, v141
	v_rndne_f32_e32 v142, v142
	v_rndne_f32_e32 v132, v132
	v_cvt_i32_f32_e32 v142, v142
	v_rndne_f32_e32 v143, v143
	v_rndne_f32_e32 v144, v144
	v_cvt_i32_f32_e32 v132, v132
	v_cvt_i32_f32_sdwa v143, v143 dst_sel:WORD_1 dst_unused:UNUSED_PAD src0_sel:DWORD
	v_cvt_i32_f32_e32 v144, v144
	v_lshlrev_b32_e32 v142, 8, v142
	v_and_b32_e32 v142, 0xff00, v142
	v_and_b32_e32 v143, 0xff0000, v143
	v_perm_b32 v132, v144, v132, s26
	v_or3_b32 v132, v132, v142, v143
	v_add_co_u32_e32 v142, vcc, s30, v134
	v_mul_f32_e32 v144, v93, v141
	s_nop 0
	v_addc_co_u32_e32 v143, vcc, 0, v135, vcc
	global_store_dword v[142:143], v132, off nt
	v_mul_f32_e32 v142, v91, v141
	v_mul_f32_e32 v132, v90, v141
	v_mul_f32_e32 v143, v92, v141
	v_rndne_f32_e32 v142, v142
	v_rndne_f32_e32 v132, v132
	v_cvt_i32_f32_e32 v142, v142
	v_rndne_f32_e32 v143, v143
	v_rndne_f32_e32 v144, v144
	v_cvt_i32_f32_e32 v132, v132
	v_cvt_i32_f32_sdwa v143, v143 dst_sel:WORD_1 dst_unused:UNUSED_PAD src0_sel:DWORD
	v_cvt_i32_f32_e32 v144, v144
	v_lshlrev_b32_e32 v142, 8, v142
	v_and_b32_e32 v142, 0xff00, v142
	v_and_b32_e32 v143, 0xff0000, v143
	v_perm_b32 v132, v144, v132, s26
	v_or3_b32 v132, v132, v142, v143
	v_add_co_u32_e32 v142, vcc, s31, v134
	v_mul_f32_e32 v144, v89, v141
	s_nop 0
	v_addc_co_u32_e32 v143, vcc, 0, v135, vcc
	global_store_dword v[142:143], v132, off nt
	v_mul_f32_e32 v142, v87, v141
	v_mul_f32_e32 v132, v86, v141
	v_mul_f32_e32 v143, v88, v141
	v_rndne_f32_e32 v142, v142
	v_rndne_f32_e32 v132, v132
	v_cvt_i32_f32_e32 v142, v142
	v_rndne_f32_e32 v143, v143
	v_rndne_f32_e32 v144, v144
	v_cvt_i32_f32_e32 v132, v132
	v_cvt_i32_f32_sdwa v143, v143 dst_sel:WORD_1 dst_unused:UNUSED_PAD src0_sel:DWORD
	v_cvt_i32_f32_e32 v144, v144
	v_lshlrev_b32_e32 v142, 8, v142
	v_and_b32_e32 v142, 0xff00, v142
	v_and_b32_e32 v143, 0xff0000, v143
	v_perm_b32 v132, v144, v132, s26
	v_or3_b32 v132, v132, v142, v143
	v_add_co_u32_e32 v142, vcc, s34, v134
	v_mul_f32_e32 v144, v85, v141
	s_nop 0
	v_addc_co_u32_e32 v143, vcc, 0, v135, vcc
	global_store_dword v[142:143], v132, off nt
; __device__ __forceinline__ void pt_proc(unsigned char* PT, const f32x4* v, int r, int lane) {
;     ...
;     for (int j = 0; j < 16; ++j) ((unsigned*)(tab + (size_t)j * PT_SLICE + (size_t)e * 256))[lane] = pack_i8x4(v[j].x * scale, v[j].y * scale, v[j].z * scale, v[j].w * scale);
;     if (lane == 0) ((float*)(PT + (tb ? PT_VS : PT_US)))[e] = amax * (1.f / 127.f);
; __device__ __forceinline__ void phase_peer_tables(const Frame& F, const Args& a, int r_lo, int r_hi, int gw, int NGW) {
;     ...
;     for (;;) {
;         const int r1 = r + NGW; const bool h1 = r1 < r_hi;
;         if (h1) pt_load(a.in[17], a.in[18], vB, r1, lane);
;         pt_proc(PT, vA, r, lane);
;         if (!h1) break;
;         const int r2 = r1 + NGW; const bool h2 = r2 < r_hi;
;         if (h2) pt_load(a.in[17], a.in[18], vA, r2, lane);
;         pt_proc(PT, vB, r1, lane);
;         if (!h2) break;
;         r = r2;
;     }
	v_mul_f32_e32 v142, v83, v141
	v_mul_f32_e32 v132, v82, v141
	v_mul_f32_e32 v143, v84, v141
	v_rndne_f32_e32 v142, v142
	v_rndne_f32_e32 v132, v132
	v_cvt_i32_f32_e32 v142, v142
	v_rndne_f32_e32 v143, v143
	v_rndne_f32_e32 v144, v144
	v_cvt_i32_f32_e32 v132, v132
	v_cvt_i32_f32_sdwa v143, v143 dst_sel:WORD_1 dst_unused:UNUSED_PAD src0_sel:DWORD
	v_cvt_i32_f32_e32 v144, v144
	v_lshlrev_b32_e32 v142, 8, v142
	v_and_b32_e32 v142, 0xff00, v142
	v_and_b32_e32 v143, 0xff0000, v143
	v_perm_b32 v132, v144, v132, s26
	v_or3_b32 v132, v132, v142, v143
	v_add_co_u32_e32 v142, vcc, s35, v134
	v_mul_f32_e32 v144, v113, v141
	s_nop 0
	v_addc_co_u32_e32 v143, vcc, 0, v135, vcc
	global_store_dword v[142:143], v132, off nt
	v_mul_f32_e32 v142, v111, v141
	v_mul_f32_e32 v132, v110, v141
	v_mul_f32_e32 v143, v112, v141
	v_rndne_f32_e32 v142, v142
	v_rndne_f32_e32 v132, v132
	v_cvt_i32_f32_e32 v142, v142
	v_rndne_f32_e32 v143, v143
	v_rndne_f32_e32 v144, v144
	v_cvt_i32_f32_e32 v132, v132
	v_cvt_i32_f32_sdwa v143, v143 dst_sel:WORD_1 dst_unused:UNUSED_PAD src0_sel:DWORD
	v_cvt_i32_f32_e32 v144, v144
	v_lshlrev_b32_e32 v142, 8, v142
	v_and_b32_e32 v142, 0xff00, v142
	v_and_b32_e32 v143, 0xff0000, v143
	v_perm_b32 v132, v144, v132, s26
	v_or3_b32 v132, v132, v142, v143
	v_add_co_u32_e32 v142, vcc, s36, v134
	v_mul_f32_e32 v144, v109, v141
	s_nop 0
	v_addc_co_u32_e32 v143, vcc, 0, v135, vcc
	global_store_dword v[142:143], v132, off nt
	v_mul_f32_e32 v142, v107, v141
	v_mul_f32_e32 v132, v106, v141
	v_mul_f32_e32 v143, v108, v141
	v_rndne_f32_e32 v142, v142
	v_rndne_f32_e32 v132, v132
	v_cvt_i32_f32_e32 v142, v142
	v_rndne_f32_e32 v143, v143
	v_rndne_f32_e32 v144, v144
	v_cvt_i32_f32_e32 v132, v132
	v_cvt_i32_f32_sdwa v143, v143 dst_sel:WORD_1 dst_unused:UNUSED_PAD src0_sel:DWORD
	v_cvt_i32_f32_e32 v144, v144
	v_lshlrev_b32_e32 v142, 8, v142
	v_and_b32_e32 v142, 0xff00, v142
	v_and_b32_e32 v143, 0xff0000, v143
	v_perm_b32 v132, v144, v132, s26
	v_or3_b32 v132, v132, v142, v143
	v_add_co_u32_e32 v142, vcc, s37, v134
	v_mul_f32_e32 v144, v105, v141
	s_nop 0
	v_addc_co_u32_e32 v143, vcc, 0, v135, vcc
	global_store_dword v[142:143], v132, off nt
	v_mul_f32_e32 v142, v103, v141
	v_mul_f32_e32 v132, v102, v141
	v_mul_f32_e32 v143, v104, v141
	v_rndne_f32_e32 v142, v142
	v_rndne_f32_e32 v132, v132
	v_cvt_i32_f32_e32 v142, v142
	v_rndne_f32_e32 v143, v143
	v_rndne_f32_e32 v144, v144
	v_cvt_i32_f32_e32 v132, v132
	v_cvt_i32_f32_sdwa v143, v143 dst_sel:WORD_1 dst_unused:UNUSED_PAD src0_sel:DWORD
	v_cvt_i32_f32_e32 v144, v144
	v_lshlrev_b32_e32 v142, 8, v142
	v_and_b32_e32 v142, 0xff00, v142
	v_and_b32_e32 v143, 0xff0000, v143
	v_perm_b32 v132, v144, v132, s26
	v_or3_b32 v132, v132, v142, v143
	v_add_co_u32_e32 v142, vcc, s38, v134
	v_mul_f32_e32 v144, v101, v141
	s_nop 0
	v_addc_co_u32_e32 v143, vcc, 0, v135, vcc
	global_store_dword v[142:143], v132, off nt
	v_mul_f32_e32 v142, v99, v141
	v_mul_f32_e32 v132, v98, v141
	v_mul_f32_e32 v143, v100, v141
	v_rndne_f32_e32 v142, v142
	v_rndne_f32_e32 v132, v132
	v_cvt_i32_f32_e32 v142, v142
	v_rndne_f32_e32 v143, v143
	v_rndne_f32_e32 v144, v144
	v_cvt_i32_f32_e32 v132, v132
	v_cvt_i32_f32_sdwa v143, v143 dst_sel:WORD_1 dst_unused:UNUSED_PAD src0_sel:DWORD
	v_cvt_i32_f32_e32 v144, v144
	v_lshlrev_b32_e32 v142, 8, v142
	v_and_b32_e32 v142, 0xff00, v142
	v_and_b32_e32 v143, 0xff0000, v143
	v_perm_b32 v132, v144, v132, s26
	v_or3_b32 v132, v132, v142, v143
	v_add_co_u32_e32 v142, vcc, s39, v134
	v_mul_f32_e32 v144, v129, v141
	s_nop 0
	v_addc_co_u32_e32 v143, vcc, 0, v135, vcc
	global_store_dword v[142:143], v132, off nt
	v_mul_f32_e32 v142, v127, v141
	v_mul_f32_e32 v132, v126, v141
	v_mul_f32_e32 v143, v128, v141
	v_rndne_f32_e32 v142, v142
	v_rndne_f32_e32 v132, v132
	v_cvt_i32_f32_e32 v142, v142
	v_rndne_f32_e32 v143, v143
	v_rndne_f32_e32 v144, v144
	v_cvt_i32_f32_e32 v132, v132
	v_cvt_i32_f32_sdwa v143, v143 dst_sel:WORD_1 dst_unused:UNUSED_PAD src0_sel:DWORD
	v_cvt_i32_f32_e32 v144, v144
	v_lshlrev_b32_e32 v142, 8, v142
	v_and_b32_e32 v142, 0xff00, v142
	v_and_b32_e32 v143, 0xff0000, v143
	v_perm_b32 v132, v144, v132, s26
	v_or3_b32 v132, v132, v142, v143
	v_add_co_u32_e32 v142, vcc, s40, v134
	v_mul_f32_e32 v144, v125, v141
	s_nop 0
	v_addc_co_u32_e32 v143, vcc, 0, v135, vcc
	global_store_dword v[142:143], v132, off nt
	v_mul_f32_e32 v142, v123, v141
	v_mul_f32_e32 v132, v122, v141
	v_mul_f32_e32 v143, v124, v141
	v_rndne_f32_e32 v142, v142
	v_rndne_f32_e32 v132, v132
	v_cvt_i32_f32_e32 v142, v142
	v_rndne_f32_e32 v143, v143
	v_rndne_f32_e32 v144, v144
	v_cvt_i32_f32_e32 v132, v132
	v_cvt_i32_f32_sdwa v143, v143 dst_sel:WORD_1 dst_unused:UNUSED_PAD src0_sel:DWORD
	v_cvt_i32_f32_e32 v144, v144
	v_lshlrev_b32_e32 v142, 8, v142
	v_and_b32_e32 v142, 0xff00, v142
	v_and_b32_e32 v143, 0xff0000, v143
	v_perm_b32 v132, v144, v132, s26
	v_or3_b32 v132, v132, v142, v143
	v_add_co_u32_e32 v142, vcc, s41, v134
	v_mul_f32_e32 v144, v121, v141
	s_nop 0
	v_addc_co_u32_e32 v143, vcc, 0, v135, vcc
	global_store_dword v[142:143], v132, off nt
	v_mul_f32_e32 v142, v119, v141
	v_mul_f32_e32 v132, v118, v141
	v_mul_f32_e32 v143, v120, v141
	v_rndne_f32_e32 v142, v142
	v_rndne_f32_e32 v132, v132
	v_cvt_i32_f32_e32 v142, v142
	v_rndne_f32_e32 v143, v143
	v_rndne_f32_e32 v144, v144
	v_cvt_i32_f32_e32 v132, v132
	v_cvt_i32_f32_sdwa v143, v143 dst_sel:WORD_1 dst_unused:UNUSED_PAD src0_sel:DWORD
	v_cvt_i32_f32_e32 v144, v144
	v_lshlrev_b32_e32 v142, 8, v142
	v_and_b32_e32 v142, 0xff00, v142
	v_and_b32_e32 v143, 0xff0000, v143
	v_perm_b32 v132, v144, v132, s26
	v_or3_b32 v132, v132, v142, v143
	v_add_co_u32_e32 v142, vcc, s42, v134
	s_nop 1
	v_addc_co_u32_e32 v143, vcc, 0, v135, vcc
	global_store_dword v[142:143], v132, off nt
	v_mul_f32_e32 v142, v115, v141
	v_mul_f32_e32 v132, v114, v141
	v_mul_f32_e32 v143, v116, v141
	v_mul_f32_e32 v141, v117, v141
	v_rndne_f32_e32 v142, v142
	v_rndne_f32_e32 v132, v132
	v_cvt_i32_f32_e32 v142, v142
	v_rndne_f32_e32 v143, v143
	v_rndne_f32_e32 v141, v141
	v_cvt_i32_f32_e32 v132, v132
	v_cvt_i32_f32_sdwa v143, v143 dst_sel:WORD_1 dst_unused:UNUSED_PAD src0_sel:DWORD
	v_cvt_i32_f32_e32 v141, v141
	v_lshlrev_b32_e32 v142, 8, v142
	v_and_b32_e32 v142, 0xff00, v142
	v_and_b32_e32 v143, 0xff0000, v143
	v_perm_b32 v132, v141, v132, s26
	v_add_co_u32_e32 v134, vcc, 0x3c00000, v134
	v_or3_b32 v132, v132, v142, v143
	s_nop 0
	v_addc_co_u32_e32 v135, vcc, 0, v135, vcc
	global_store_dword v[134:135], v132, off nt
	s_and_saveexec_b64 s[2:3], s[6:7]
	s_cbranch_execz .LBB0_212
	s_and_b64 s[0:1], s[0:1], exec
	s_cselect_b32 s0, s43, 0x8010000
	s_add_u32 s0, s33, s0
	s_addc_u32 s1, s46, 0
	s_lshl_b32 s4, s4, 2
	v_mul_f32_e32 v131, 0x3c010204, v131
	v_mov_b32_e32 v132, s4
	global_store_dword v132, v131, s[0:1] nt
	s_branch .LBB0_212

; __device__ __forceinline__ void pt_proc(unsigned char* PT, const f32x4* v, int r, int lane) {
;     const int tb = r >> 14, e = r & 16383; unsigned char* tab = PT + (tb ? PT_V8 : 0); float amax = 0.f;
; #pragma unroll
;     for (int j = 0; j < 16; ++j) amax = fmaxf(fmaxf(amax, fmaxf(fabsf(v[j].x), fabsf(v[j].y))), fmaxf(fabsf(v[j].z), fabsf(v[j].w)));
;     amax = wave_max(amax); const float scale = amax > 0.f ? 127.f / amax : 0.f;
.LBB0_231:
	s_waitcnt vmcnt(1)
	v_max_f32_e64 v131, |v27|, |v27|
	v_max_f32_e64 v132, |v26|, |v26|
	v_max_f32_e32 v131, v132, v131
	v_max_f32_e64 v132, |v29|, |v29|
	v_max_f32_e64 v134, |v28|, |v28|
	v_max_f32_e32 v132, v134, v132
	v_max3_f32 v131, v131, 0, v132
	v_max_f32_e64 v132, |v3|, |v3|
	v_max_f32_e64 v134, |v2|, |v2|
	v_max_f32_e32 v132, v134, v132
	v_max_f32_e64 v134, |v5|, |v5|
	v_max_f32_e64 v135, |v4|, |v4|
	v_max_f32_e32 v134, v135, v134
	v_max3_f32 v131, v131, v132, v134
	v_max_f32_e64 v132, |v7|, |v7|
	v_max_f32_e64 v134, |v6|, |v6|
	v_max_f32_e32 v132, v134, v132
	v_max_f32_e64 v134, |v9|, |v9|
	v_max_f32_e64 v135, |v8|, |v8|
	v_max_f32_e32 v134, v135, v134
	v_max3_f32 v131, v131, v132, v134
	v_max_f32_e64 v132, |v11|, |v11|
	v_max_f32_e64 v134, |v10|, |v10|
	v_max_f32_e32 v132, v134, v132
	v_max_f32_e64 v134, |v13|, |v13|
	v_max_f32_e64 v135, |v12|, |v12|
	v_max_f32_e32 v134, v135, v134
	v_max3_f32 v131, v131, v132, v134
	v_max_f32_e64 v132, |v15|, |v15|
	v_max_f32_e64 v134, |v14|, |v14|
	v_max_f32_e32 v132, v134, v132
	v_max_f32_e64 v134, |v17|, |v17|
	v_max_f32_e64 v135, |v16|, |v16|
	v_max_f32_e32 v134, v135, v134
	v_max3_f32 v131, v131, v132, v134
	v_max_f32_e64 v132, |v19|, |v19|
	v_max_f32_e64 v134, |v18|, |v18|
	v_max_f32_e32 v132, v134, v132
	v_max_f32_e64 v134, |v21|, |v21|
	v_max_f32_e64 v135, |v20|, |v20|
	v_max_f32_e32 v134, v135, v134
	v_max3_f32 v131, v131, v132, v134
	v_max_f32_e64 v132, |v23|, |v23|
	v_max_f32_e64 v134, |v22|, |v22|
	v_max_f32_e32 v132, v134, v132
	v_max_f32_e64 v134, |v25|, |v25|
	v_max_f32_e64 v135, |v24|, |v24|
	v_max_f32_e32 v134, v135, v134
	v_max3_f32 v131, v131, v132, v134
	v_max_f32_e64 v132, |v39|, |v39|
	v_max_f32_e64 v134, |v38|, |v38|
	v_max_f32_e32 v132, v134, v132
	v_max_f32_e64 v134, |v41|, |v41|
	v_max_f32_e64 v135, |v40|, |v40|
	v_max_f32_e32 v134, v135, v134
	v_max3_f32 v131, v131, v132, v134
	v_max_f32_e64 v132, |v31|, |v31|
	v_max_f32_e64 v134, |v30|, |v30|
	v_max_f32_e32 v132, v134, v132
	v_max_f32_e64 v134, |v33|, |v33|
	v_max_f32_e64 v135, |v32|, |v32|
	v_max_f32_e32 v134, v135, v134
	v_max3_f32 v131, v131, v132, v134
	v_max_f32_e64 v132, |v35|, |v35|
	v_max_f32_e64 v134, |v34|, |v34|
	v_max_f32_e32 v132, v134, v132
	v_max_f32_e64 v134, |v37|, |v37|
	v_max_f32_e64 v135, |v36|, |v36|
	v_max_f32_e32 v134, v135, v134
	v_max3_f32 v131, v131, v132, v134
	v_max_f32_e64 v132, |v43|, |v43|
	v_max_f32_e64 v134, |v42|, |v42|
	v_max_f32_e32 v132, v134, v132
	v_max_f32_e64 v134, |v45|, |v45|
	v_max_f32_e64 v135, |v44|, |v44|
	v_max_f32_e32 v134, v135, v134
	v_max3_f32 v131, v131, v132, v134
	v_max_f32_e64 v132, |v47|, |v47|
	v_max_f32_e64 v134, |v46|, |v46|
	v_max_f32_e32 v132, v134, v132
	v_max_f32_e64 v134, |v49|, |v49|
	v_max_f32_e64 v135, |v48|, |v48|
	v_max_f32_e32 v134, v135, v134
	v_max3_f32 v131, v131, v132, v134
	v_max_f32_e64 v132, |v51|, |v51|
	v_max_f32_e64 v134, |v50|, |v50|
	v_max_f32_e32 v132, v134, v132
	v_max_f32_e64 v134, |v53|, |v53|
	v_max_f32_e64 v135, |v52|, |v52|
	v_max_f32_e32 v134, v135, v134
	v_max3_f32 v131, v131, v132, v134
	v_max_f32_e64 v132, |v55|, |v55|
	v_max_f32_e64 v134, |v54|, |v54|
	v_max_f32_e32 v132, v134, v132
	v_max_f32_e64 v134, |v57|, |v57|
	v_max_f32_e64 v135, |v56|, |v56|
	v_max_f32_e32 v134, v135, v134
	v_max3_f32 v131, v131, v132, v134
	v_max_f32_e64 v132, |v59|, |v59|
	v_max_f32_e64 v134, |v58|, |v58|
	v_max_f32_e32 v132, v134, v132
	v_max_f32_e64 v134, |v61|, |v61|
	v_max_f32_e64 v135, |v60|, |v60|
	v_max_f32_e32 v134, v135, v134
	v_max3_f32 v131, v131, v132, v134
	s_waitcnt vmcnt(0)
	v_max_f32_e64 v132, |v63|, |v63|
	v_max_f32_e64 v134, |v62|, |v62|
	v_max_f32_e32 v132, v134, v132
	v_max_f32_e64 v134, |v65|, |v65|
	v_max_f32_e64 v135, |v64|, |v64|
	v_max_f32_e32 v134, v135, v134
	v_max3_f32 v131, v131, v132, v134
	ds_bpermute_b32 v132, v1, v131
	s_cmpk_lt_u32 s39, 0x4000
	s_cselect_b64 s[2:3], -1, 0
	s_and_b64 s[4:5], s[2:3], exec
	s_cselect_b32 s41, 0, 0x4000000
	s_waitcnt lgkmcnt(0)
	v_max_f32_e32 v132, v132, v132
	v_max_f32_e32 v131, v131, v132
	ds_bpermute_b32 v132, v136, v131
	s_and_b32 s40, s39, 0x3fff
	s_waitcnt lgkmcnt(0)
	v_max_f32_e32 v132, v132, v132
	v_max_f32_e32 v131, v131, v132
	ds_bpermute_b32 v132, v137, v131
	s_waitcnt lgkmcnt(0)
	v_max_f32_e32 v132, v132, v132
	v_max_f32_e32 v131, v131, v132
	ds_bpermute_b32 v132, v138, v131
	s_waitcnt lgkmcnt(0)
	v_max_f32_e32 v132, v132, v132
	v_max_f32_e32 v131, v131, v132
	ds_bpermute_b32 v132, v139, v131
	s_waitcnt lgkmcnt(0)
	v_max_f32_e32 v132, v132, v132
	v_max_f32_e32 v131, v131, v132
	ds_bpermute_b32 v132, v140, v131
	s_waitcnt lgkmcnt(0)
; __device__ __forceinline__ void pt_proc(unsigned char* PT, const f32x4* v, int r, int lane) {
;     ...
;     amax = wave_max(amax); const float scale = amax > 0.f ? 127.f / amax : 0.f;
; #pragma unroll
;     for (int j = 0; j < 16; ++j) ((unsigned*)(tab + (size_t)j * PT_SLICE + (size_t)e * 256))[lane] = pack_i8x4(v[j].x * scale, v[j].y * scale, v[j].z * scale, v[j].w * scale);
	v_max_f32_e32 v132, v132, v132
	v_max_f32_e32 v131, v131, v132
	v_div_scale_f32 v132, s[4:5], v131, v131, s19
	v_rcp_f32_e32 v134, v132
	s_add_u32 s4, s33, s41
	s_addc_u32 s5, s46, 0
	s_lshl_b32 s41, s40, 8
	v_fma_f32 v135, -v132, v134, 1.0
	v_fmac_f32_e32 v134, v135, v134
	v_div_scale_f32 v135, vcc, s19, v131, s19
	v_mul_f32_e32 v141, v135, v134
	v_fma_f32 v142, -v132, v141, v135
	v_fmac_f32_e32 v141, v142, v134
	v_fma_f32 v132, -v132, v141, v135
	v_div_fmas_f32 v132, v132, v134, v141
	v_div_fixup_f32 v132, v132, v131, s19
	v_cmp_lt_f32_e32 vcc, 0, v131
	s_add_u32 s4, s4, s41
	s_addc_u32 s5, s5, 0
	v_cndmask_b32_e32 v141, 0, v132, vcc
	v_mul_f32_e32 v143, v27, v141
	v_mul_f32_e32 v142, v26, v141
	v_mul_f32_e32 v144, v28, v141
	v_mul_f32_e32 v145, v29, v141
	v_rndne_f32_e32 v143, v143
	v_rndne_f32_e32 v142, v142
	v_cvt_i32_f32_e32 v143, v143
	v_rndne_f32_e32 v144, v144
	v_rndne_f32_e32 v145, v145
	v_cvt_i32_f32_e32 v142, v142
	v_cvt_i32_f32_sdwa v144, v144 dst_sel:WORD_1 dst_unused:UNUSED_PAD src0_sel:DWORD
	v_cvt_i32_f32_e32 v145, v145
	v_lshlrev_b32_e32 v143, 8, v143
	v_and_b32_e32 v143, 0xff00, v143
	v_and_b32_e32 v144, 0xff0000, v144
	v_perm_b32 v142, v145, v142, s20
	v_lshlrev_b32_e32 v132, 2, v194
	v_or3_b32 v142, v142, v143, v144
	v_mul_f32_e32 v143, v3, v141
	global_store_dword v132, v142, s[4:5] nt
	v_mul_f32_e32 v142, v2, v141
	v_mul_f32_e32 v144, v4, v141
	v_mul_f32_e32 v145, v5, v141
	v_rndne_f32_e32 v143, v143
	v_rndne_f32_e32 v142, v142
	v_cvt_i32_f32_e32 v143, v143
	v_rndne_f32_e32 v144, v144
	v_rndne_f32_e32 v145, v145
	v_cvt_i32_f32_e32 v142, v142
	v_cvt_i32_f32_sdwa v144, v144 dst_sel:WORD_1 dst_unused:UNUSED_PAD src0_sel:DWORD
	v_cvt_i32_f32_e32 v145, v145
	v_lshlrev_b32_e32 v143, 8, v143
	v_lshl_add_u64 v[134:135], s[4:5], 0, v[132:133]
	v_and_b32_e32 v143, 0xff00, v143
	v_and_b32_e32 v144, 0xff0000, v144
	v_perm_b32 v142, v145, v142, s20
	v_or3_b32 v144, v142, v143, v144
	v_add_co_u32_e32 v142, vcc, s21, v134
	v_mul_f32_e32 v145, v9, v141
	s_nop 0
	v_addc_co_u32_e32 v143, vcc, 0, v135, vcc
	global_store_dword v[142:143], v144, off nt
	v_mul_f32_e32 v143, v7, v141
	v_mul_f32_e32 v142, v6, v141
	v_mul_f32_e32 v144, v8, v141
	v_rndne_f32_e32 v143, v143
	v_rndne_f32_e32 v142, v142
	v_cvt_i32_f32_e32 v143, v143
	v_rndne_f32_e32 v144, v144
	v_rndne_f32_e32 v145, v145
	v_cvt_i32_f32_e32 v142, v142
	v_cvt_i32_f32_sdwa v144, v144 dst_sel:WORD_1 dst_unused:UNUSED_PAD src0_sel:DWORD
	v_cvt_i32_f32_e32 v145, v145
	v_lshlrev_b32_e32 v143, 8, v143
	v_and_b32_e32 v143, 0xff00, v143
	v_and_b32_e32 v144, 0xff0000, v144
	v_perm_b32 v142, v145, v142, s20
	v_or3_b32 v144, v142, v143, v144
	v_add_co_u32_e32 v142, vcc, s22, v134
	v_mul_f32_e32 v145, v13, v141
	s_nop 0
	v_addc_co_u32_e32 v143, vcc, 0, v135, vcc
	global_store_dword v[142:143], v144, off nt
	v_mul_f32_e32 v143, v11, v141
	v_mul_f32_e32 v142, v10, v141
	v_mul_f32_e32 v144, v12, v141
	v_rndne_f32_e32 v143, v143
	v_rndne_f32_e32 v142, v142
	v_cvt_i32_f32_e32 v143, v143
	v_rndne_f32_e32 v144, v144
	v_rndne_f32_e32 v145, v145
	v_cvt_i32_f32_e32 v142, v142
	v_cvt_i32_f32_sdwa v144, v144 dst_sel:WORD_1 dst_unused:UNUSED_PAD src0_sel:DWORD
	v_cvt_i32_f32_e32 v145, v145
	v_lshlrev_b32_e32 v143, 8, v143
	v_and_b32_e32 v143, 0xff00, v143
	v_and_b32_e32 v144, 0xff0000, v144
	v_perm_b32 v142, v145, v142, s20
	v_or3_b32 v144, v142, v143, v144
	v_add_co_u32_e32 v142, vcc, s23, v134
	v_mul_f32_e32 v145, v17, v141
	s_nop 0
	v_addc_co_u32_e32 v143, vcc, 0, v135, vcc
	global_store_dword v[142:143], v144, off nt
	v_mul_f32_e32 v143, v15, v141
	v_mul_f32_e32 v142, v14, v141
	v_mul_f32_e32 v144, v16, v141
	v_rndne_f32_e32 v143, v143
	v_rndne_f32_e32 v142, v142
	v_cvt_i32_f32_e32 v143, v143
	v_rndne_f32_e32 v144, v144
	v_rndne_f32_e32 v145, v145
	v_cvt_i32_f32_e32 v142, v142
	v_cvt_i32_f32_sdwa v144, v144 dst_sel:WORD_1 dst_unused:UNUSED_PAD src0_sel:DWORD
	v_cvt_i32_f32_e32 v145, v145
	v_lshlrev_b32_e32 v143, 8, v143
	v_and_b32_e32 v143, 0xff00, v143
	v_and_b32_e32 v144, 0xff0000, v144
	v_perm_b32 v142, v145, v142, s20
	v_or3_b32 v144, v142, v143, v144
	v_add_co_u32_e32 v142, vcc, s24, v134
	v_mul_f32_e32 v145, v21, v141
	s_nop 0
	v_addc_co_u32_e32 v143, vcc, 0, v135, vcc
	global_store_dword v[142:143], v144, off nt
	v_mul_f32_e32 v143, v19, v141
	v_mul_f32_e32 v142, v18, v141
	v_mul_f32_e32 v144, v20, v141
	v_rndne_f32_e32 v143, v143
	v_rndne_f32_e32 v142, v142
	v_cvt_i32_f32_e32 v143, v143
	v_rndne_f32_e32 v144, v144
	v_rndne_f32_e32 v145, v145
	v_cvt_i32_f32_e32 v142, v142
	v_cvt_i32_f32_sdwa v144, v144 dst_sel:WORD_1 dst_unused:UNUSED_PAD src0_sel:DWORD
	v_cvt_i32_f32_e32 v145, v145
	v_lshlrev_b32_e32 v143, 8, v143
	v_and_b32_e32 v143, 0xff00, v143
	v_and_b32_e32 v144, 0xff0000, v144
	v_perm_b32 v142, v145, v142, s20
	v_or3_b32 v144, v142, v143, v144
	v_add_co_u32_e32 v142, vcc, s25, v134
	v_mul_f32_e32 v145, v25, v141
	s_nop 0
	v_addc_co_u32_e32 v143, vcc, 0, v135, vcc
	global_store_dword v[142:143], v144, off nt
	v_mul_f32_e32 v143, v23, v141
	v_mul_f32_e32 v142, v22, v141
	v_mul_f32_e32 v144, v24, v141
	v_rndne_f32_e32 v143, v143
	v_rndne_f32_e32 v142, v142
	v_cvt_i32_f32_e32 v143, v143
	v_rndne_f32_e32 v144, v144
	v_rndne_f32_e32 v145, v145
	v_cvt_i32_f32_e32 v142, v142
	v_cvt_i32_f32_sdwa v144, v144 dst_sel:WORD_1 dst_unused:UNUSED_PAD src0_sel:DWORD
	v_cvt_i32_f32_e32 v145, v145
	v_lshlrev_b32_e32 v143, 8, v143
	v_and_b32_e32 v143, 0xff00, v143
	v_and_b32_e32 v144, 0xff0000, v144
	v_perm_b32 v142, v145, v142, s20
	v_or3_b32 v144, v142, v143, v144
	v_add_co_u32_e32 v142, vcc, s26, v134
	v_mul_f32_e32 v145, v41, v141
	s_nop 0
	v_addc_co_u32_e32 v143, vcc, 0, v135, vcc
; __device__ __forceinline__ void pt_proc(unsigned char* PT, const f32x4* v, int r, int lane) {
;     ...
;     for (int j = 0; j < 16; ++j) ((unsigned*)(tab + (size_t)j * PT_SLICE + (size_t)e * 256))[lane] = pack_i8x4(v[j].x * scale, v[j].y * scale, v[j].z * scale, v[j].w * scale);
;     if (lane == 0) ((float*)(PT + (tb ? PT_VS : PT_US)))[e] = amax * (1.f / 127.f);
; __device__ __forceinline__ void phase_peer_tables(const Frame& F, const Args& a, int r_lo, int r_hi, int gw, int NGW) {
;     ...
;     for (;;) {
;         const int r1 = r + NGW; const bool h1 = r1 < r_hi;
;         if (h1) pt_load(a.in[17], a.in[18], vB, r1, lane);
;         pt_proc(PT, vA, r, lane);
;         if (!h1) break;
;         const int r2 = r1 + NGW; const bool h2 = r2 < r_hi;
;         if (h2) pt_load(a.in[17], a.in[18], vA, r2, lane);
;         pt_proc(PT, vB, r1, lane);
;         if (!h2) break;
;         r = r2;
;     }
	global_store_dword v[142:143], v144, off nt
	v_mul_f32_e32 v143, v39, v141
	v_mul_f32_e32 v142, v38, v141
	v_mul_f32_e32 v144, v40, v141
	v_rndne_f32_e32 v143, v143
	v_rndne_f32_e32 v142, v142
	v_cvt_i32_f32_e32 v143, v143
	v_rndne_f32_e32 v144, v144
	v_rndne_f32_e32 v145, v145
	v_cvt_i32_f32_e32 v142, v142
	v_cvt_i32_f32_sdwa v144, v144 dst_sel:WORD_1 dst_unused:UNUSED_PAD src0_sel:DWORD
	v_cvt_i32_f32_e32 v145, v145
	v_lshlrev_b32_e32 v143, 8, v143
	v_and_b32_e32 v143, 0xff00, v143
	v_and_b32_e32 v144, 0xff0000, v144
	v_perm_b32 v142, v145, v142, s20
	v_or3_b32 v144, v142, v143, v144
	v_add_co_u32_e32 v142, vcc, s27, v134
	v_mul_f32_e32 v145, v33, v141
	s_nop 0
	v_addc_co_u32_e32 v143, vcc, 0, v135, vcc
	global_store_dword v[142:143], v144, off nt
	v_mul_f32_e32 v143, v31, v141
	v_mul_f32_e32 v142, v30, v141
	v_mul_f32_e32 v144, v32, v141
	v_rndne_f32_e32 v143, v143
	v_rndne_f32_e32 v142, v142
	v_cvt_i32_f32_e32 v143, v143
	v_rndne_f32_e32 v144, v144
	v_rndne_f32_e32 v145, v145
	v_cvt_i32_f32_e32 v142, v142
	v_cvt_i32_f32_sdwa v144, v144 dst_sel:WORD_1 dst_unused:UNUSED_PAD src0_sel:DWORD
	v_cvt_i32_f32_e32 v145, v145
	v_lshlrev_b32_e32 v143, 8, v143
	v_and_b32_e32 v143, 0xff00, v143
	v_and_b32_e32 v144, 0xff0000, v144
	v_perm_b32 v142, v145, v142, s20
	v_or3_b32 v144, v142, v143, v144
	v_add_co_u32_e32 v142, vcc, s28, v134
	v_mul_f32_e32 v145, v37, v141
	s_nop 0
	v_addc_co_u32_e32 v143, vcc, 0, v135, vcc
	global_store_dword v[142:143], v144, off nt
	v_mul_f32_e32 v143, v35, v141
	v_mul_f32_e32 v142, v34, v141
	v_mul_f32_e32 v144, v36, v141
	v_rndne_f32_e32 v143, v143
	v_rndne_f32_e32 v142, v142
	v_cvt_i32_f32_e32 v143, v143
	v_rndne_f32_e32 v144, v144
	v_rndne_f32_e32 v145, v145
	v_cvt_i32_f32_e32 v142, v142
	v_cvt_i32_f32_sdwa v144, v144 dst_sel:WORD_1 dst_unused:UNUSED_PAD src0_sel:DWORD
	v_cvt_i32_f32_e32 v145, v145
	v_lshlrev_b32_e32 v143, 8, v143
	v_and_b32_e32 v143, 0xff00, v143
	v_and_b32_e32 v144, 0xff0000, v144
	v_perm_b32 v142, v145, v142, s20
	v_or3_b32 v144, v142, v143, v144
	v_add_co_u32_e32 v142, vcc, s29, v134
	v_mul_f32_e32 v145, v45, v141
	s_nop 0
	v_addc_co_u32_e32 v143, vcc, 0, v135, vcc
	global_store_dword v[142:143], v144, off nt
	v_mul_f32_e32 v143, v43, v141
	v_mul_f32_e32 v142, v42, v141
	v_mul_f32_e32 v144, v44, v141
	v_rndne_f32_e32 v143, v143
	v_rndne_f32_e32 v142, v142
	v_cvt_i32_f32_e32 v143, v143
	v_rndne_f32_e32 v144, v144
	v_rndne_f32_e32 v145, v145
	v_cvt_i32_f32_e32 v142, v142
	v_cvt_i32_f32_sdwa v144, v144 dst_sel:WORD_1 dst_unused:UNUSED_PAD src0_sel:DWORD
	v_cvt_i32_f32_e32 v145, v145
	v_lshlrev_b32_e32 v143, 8, v143
	v_and_b32_e32 v143, 0xff00, v143
	v_and_b32_e32 v144, 0xff0000, v144
	v_perm_b32 v142, v145, v142, s20
	v_or3_b32 v144, v142, v143, v144
	v_add_co_u32_e32 v142, vcc, s30, v134
	v_mul_f32_e32 v145, v49, v141
	s_nop 0
	v_addc_co_u32_e32 v143, vcc, 0, v135, vcc
	global_store_dword v[142:143], v144, off nt
	v_mul_f32_e32 v143, v47, v141
	v_mul_f32_e32 v142, v46, v141
	v_mul_f32_e32 v144, v48, v141
	v_rndne_f32_e32 v143, v143
	v_rndne_f32_e32 v142, v142
	v_cvt_i32_f32_e32 v143, v143
	v_rndne_f32_e32 v144, v144
	v_rndne_f32_e32 v145, v145
	v_cvt_i32_f32_e32 v142, v142
	v_cvt_i32_f32_sdwa v144, v144 dst_sel:WORD_1 dst_unused:UNUSED_PAD src0_sel:DWORD
	v_cvt_i32_f32_e32 v145, v145
	v_lshlrev_b32_e32 v143, 8, v143
	v_and_b32_e32 v143, 0xff00, v143
	v_and_b32_e32 v144, 0xff0000, v144
	v_perm_b32 v142, v145, v142, s20
	v_or3_b32 v144, v142, v143, v144
	v_add_co_u32_e32 v142, vcc, s31, v134
	v_mul_f32_e32 v145, v53, v141
	s_nop 0
	v_addc_co_u32_e32 v143, vcc, 0, v135, vcc
	global_store_dword v[142:143], v144, off nt
	v_mul_f32_e32 v143, v51, v141
	v_mul_f32_e32 v142, v50, v141
	v_mul_f32_e32 v144, v52, v141
	v_rndne_f32_e32 v143, v143
	v_rndne_f32_e32 v142, v142
	v_cvt_i32_f32_e32 v143, v143
	v_rndne_f32_e32 v144, v144
	v_rndne_f32_e32 v145, v145
	v_cvt_i32_f32_e32 v142, v142
	v_cvt_i32_f32_sdwa v144, v144 dst_sel:WORD_1 dst_unused:UNUSED_PAD src0_sel:DWORD
	v_cvt_i32_f32_e32 v145, v145
	v_lshlrev_b32_e32 v143, 8, v143
	v_and_b32_e32 v143, 0xff00, v143
	v_and_b32_e32 v144, 0xff0000, v144
	v_perm_b32 v142, v145, v142, s20
	v_or3_b32 v144, v142, v143, v144
	v_add_co_u32_e32 v142, vcc, s34, v134
	v_mul_f32_e32 v145, v57, v141
	s_nop 0
	v_addc_co_u32_e32 v143, vcc, 0, v135, vcc
	global_store_dword v[142:143], v144, off nt
	v_mul_f32_e32 v143, v55, v141
	v_mul_f32_e32 v142, v54, v141
	v_mul_f32_e32 v144, v56, v141
	v_rndne_f32_e32 v143, v143
	v_rndne_f32_e32 v142, v142
	v_cvt_i32_f32_e32 v143, v143
	v_rndne_f32_e32 v144, v144
	v_rndne_f32_e32 v145, v145
	v_cvt_i32_f32_e32 v142, v142
	v_cvt_i32_f32_sdwa v144, v144 dst_sel:WORD_1 dst_unused:UNUSED_PAD src0_sel:DWORD
	v_cvt_i32_f32_e32 v145, v145
	v_lshlrev_b32_e32 v143, 8, v143
	v_and_b32_e32 v143, 0xff00, v143
	v_and_b32_e32 v144, 0xff0000, v144
	v_perm_b32 v142, v145, v142, s20
	v_or3_b32 v144, v142, v143, v144
	v_add_co_u32_e32 v142, vcc, s35, v134
	v_mul_f32_e32 v145, v61, v141
	s_nop 0
	v_addc_co_u32_e32 v143, vcc, 0, v135, vcc
	global_store_dword v[142:143], v144, off nt
	v_mul_f32_e32 v143, v59, v141
	v_mul_f32_e32 v142, v58, v141
	v_mul_f32_e32 v144, v60, v141
	v_rndne_f32_e32 v143, v143
	v_rndne_f32_e32 v142, v142
	v_cvt_i32_f32_e32 v143, v143
	v_rndne_f32_e32 v144, v144
	v_rndne_f32_e32 v145, v145
	v_cvt_i32_f32_e32 v142, v142
	v_cvt_i32_f32_sdwa v144, v144 dst_sel:WORD_1 dst_unused:UNUSED_PAD src0_sel:DWORD
	v_cvt_i32_f32_e32 v145, v145
	v_lshlrev_b32_e32 v143, 8, v143
	v_and_b32_e32 v143, 0xff00, v143
	v_and_b32_e32 v144, 0xff0000, v144
	v_perm_b32 v142, v145, v142, s20
	v_or3_b32 v144, v142, v143, v144
	v_add_co_u32_e32 v142, vcc, s36, v134
	s_nop 1
	v_addc_co_u32_e32 v143, vcc, 0, v135, vcc
	global_store_dword v[142:143], v144, off nt
	v_mul_f32_e32 v143, v63, v141
	v_mul_f32_e32 v142, v62, v141
	v_mul_f32_e32 v144, v64, v141
	v_mul_f32_e32 v141, v65, v141
	v_rndne_f32_e32 v143, v143
	v_rndne_f32_e32 v142, v142
	v_cvt_i32_f32_e32 v143, v143
	v_rndne_f32_e32 v144, v144
	v_rndne_f32_e32 v141, v141
	v_cvt_i32_f32_e32 v142, v142
	v_cvt_i32_f32_sdwa v144, v144 dst_sel:WORD_1 dst_unused:UNUSED_PAD src0_sel:DWORD
	v_cvt_i32_f32_e32 v141, v141
	v_lshlrev_b32_e32 v143, 8, v143
	v_and_b32_e32 v143, 0xff00, v143
	v_and_b32_e32 v144, 0xff0000, v144
	v_perm_b32 v141, v141, v142, s20
	v_add_co_u32_e32 v134, vcc, 0x3c00000, v134
	v_or3_b32 v141, v141, v143, v144
	s_nop 0
	v_addc_co_u32_e32 v135, vcc, 0, v135, vcc
	global_store_dword v[134:135], v141, off nt
	s_and_saveexec_b64 s[4:5], s[6:7]
	s_cbranch_execnz .LBB0_233
	s_or_b64 exec, exec, s[4:5]
	s_andn2_b64 vcc, exec, s[0:1]
	s_mov_b64 s[0:1], -1
	s_cbranch_vccnz .LBB0_228
	s_branch .LBB0_234
.LBB0_233:
	s_and_b64 s[2:3], s[2:3], exec
	s_cselect_b32 s2, s37, 0x8010000
	s_add_u32 s2, s33, s2
	s_addc_u32 s3, s46, 0
	s_lshl_b32 s40, s40, 2
	v_mul_f32_e32 v131, 0x3c010204, v131
	v_mov_b32_e32 v134, s40
	global_store_dword v134, v131, s[2:3] nt
	s_or_b64 exec, exec, s[4:5]
	s_andn2_b64 vcc, exec, s[0:1]
	s_mov_b64 s[0:1], -1
	s_cbranch_vccnz .LBB0_228

; __device__ __forceinline__ void pt_proc(unsigned char* PT, const f32x4* v, int r, int lane) {
;     const int tb = r >> 14, e = r & 16383; unsigned char* tab = PT + (tb ? PT_V8 : 0); float amax = 0.f;
; #pragma unroll
;     for (int j = 0; j < 16; ++j) amax = fmaxf(fmaxf(amax, fmaxf(fabsf(v[j].x), fabsf(v[j].y))), fmaxf(fabsf(v[j].z), fabsf(v[j].w)));
;     amax = wave_max(amax); const float scale = amax > 0.f ? 127.f / amax : 0.f;
.LBB0_236:
	v_max_f32_e64 v131, |v79|, |v79|
	v_max_f32_e64 v134, |v78|, |v78|
	v_max_f32_e32 v131, v134, v131
	v_max_f32_e64 v134, |v81|, |v81|
	v_max_f32_e64 v135, |v80|, |v80|
	v_max_f32_e32 v134, v135, v134
	v_max3_f32 v131, v131, 0, v134
	v_max_f32_e64 v134, |v75|, |v75|
	v_max_f32_e64 v135, |v74|, |v74|
	v_max_f32_e32 v134, v135, v134
	v_max_f32_e64 v135, |v77|, |v77|
	v_max_f32_e64 v141, |v76|, |v76|
	v_max_f32_e32 v135, v141, v135
	v_max3_f32 v131, v131, v134, v135
	v_max_f32_e64 v134, |v71|, |v71|
	v_max_f32_e64 v135, |v70|, |v70|
	v_max_f32_e32 v134, v135, v134
	v_max_f32_e64 v135, |v73|, |v73|
	v_max_f32_e64 v141, |v72|, |v72|
	v_max_f32_e32 v135, v141, v135
	v_max3_f32 v131, v131, v134, v135
	v_max_f32_e64 v134, |v67|, |v67|
	v_max_f32_e64 v135, |v66|, |v66|
	v_max_f32_e32 v134, v135, v134
	v_max_f32_e64 v135, |v69|, |v69|
	v_max_f32_e64 v141, |v68|, |v68|
	v_max_f32_e32 v135, v141, v135
	v_max3_f32 v131, v131, v134, v135
	v_max_f32_e64 v134, |v95|, |v95|
	v_max_f32_e64 v135, |v94|, |v94|
	v_max_f32_e32 v134, v135, v134
	v_max_f32_e64 v135, |v97|, |v97|
	v_max_f32_e64 v141, |v96|, |v96|
	v_max_f32_e32 v135, v141, v135
	v_max3_f32 v131, v131, v134, v135
	v_max_f32_e64 v134, |v91|, |v91|
	v_max_f32_e64 v135, |v90|, |v90|
	v_max_f32_e32 v134, v135, v134
	v_max_f32_e64 v135, |v93|, |v93|
	v_max_f32_e64 v141, |v92|, |v92|
	v_max_f32_e32 v135, v141, v135
	v_max3_f32 v131, v131, v134, v135
	v_max_f32_e64 v134, |v87|, |v87|
	v_max_f32_e64 v135, |v86|, |v86|
	v_max_f32_e32 v134, v135, v134
	v_max_f32_e64 v135, |v89|, |v89|
	v_max_f32_e64 v141, |v88|, |v88|
	v_max_f32_e32 v135, v141, v135
	v_max3_f32 v131, v131, v134, v135
	v_max_f32_e64 v134, |v83|, |v83|
	v_max_f32_e64 v135, |v82|, |v82|
	v_max_f32_e32 v134, v135, v134
	v_max_f32_e64 v135, |v85|, |v85|
	v_max_f32_e64 v141, |v84|, |v84|
	v_max_f32_e32 v135, v141, v135
	v_max3_f32 v131, v131, v134, v135
	v_max_f32_e64 v134, |v111|, |v111|
	v_max_f32_e64 v135, |v110|, |v110|
	v_max_f32_e32 v134, v135, v134
	v_max_f32_e64 v135, |v113|, |v113|
	v_max_f32_e64 v141, |v112|, |v112|
	v_max_f32_e32 v135, v141, v135
	v_max3_f32 v131, v131, v134, v135
	v_max_f32_e64 v134, |v107|, |v107|
	v_max_f32_e64 v135, |v106|, |v106|
	v_max_f32_e32 v134, v135, v134
	v_max_f32_e64 v135, |v109|, |v109|
	v_max_f32_e64 v141, |v108|, |v108|
	v_max_f32_e32 v135, v141, v135
	v_max3_f32 v131, v131, v134, v135
	v_max_f32_e64 v134, |v103|, |v103|
	v_max_f32_e64 v135, |v102|, |v102|
	v_max_f32_e32 v134, v135, v134
	v_max_f32_e64 v135, |v105|, |v105|
	v_max_f32_e64 v141, |v104|, |v104|
	v_max_f32_e32 v135, v141, v135
	v_max3_f32 v131, v131, v134, v135
	v_max_f32_e64 v134, |v99|, |v99|
	v_max_f32_e64 v135, |v98|, |v98|
	v_max_f32_e32 v134, v135, v134
	v_max_f32_e64 v135, |v101|, |v101|
	v_max_f32_e64 v141, |v100|, |v100|
	v_max_f32_e32 v135, v141, v135
	v_max3_f32 v131, v131, v134, v135
	v_max_f32_e64 v134, |v127|, |v127|
	v_max_f32_e64 v135, |v126|, |v126|
	v_max_f32_e32 v134, v135, v134
	v_max_f32_e64 v135, |v129|, |v129|
	v_max_f32_e64 v141, |v128|, |v128|
	v_max_f32_e32 v135, v141, v135
	v_max3_f32 v131, v131, v134, v135
	v_max_f32_e64 v134, |v123|, |v123|
	v_max_f32_e64 v135, |v122|, |v122|
	v_max_f32_e32 v134, v135, v134
	v_max_f32_e64 v135, |v125|, |v125|
	v_max_f32_e64 v141, |v124|, |v124|
	v_max_f32_e32 v135, v141, v135
	v_max3_f32 v131, v131, v134, v135
	v_max_f32_e64 v134, |v119|, |v119|
	v_max_f32_e64 v135, |v118|, |v118|
	v_max_f32_e32 v134, v135, v134
	v_max_f32_e64 v135, |v121|, |v121|
	v_max_f32_e64 v141, |v120|, |v120|
	v_max_f32_e32 v135, v141, v135
	v_max3_f32 v131, v131, v134, v135
	v_max_f32_e64 v134, |v115|, |v115|
	v_max_f32_e64 v135, |v114|, |v114|
	v_max_f32_e32 v134, v135, v134
	v_max_f32_e64 v135, |v117|, |v117|
	v_max_f32_e64 v141, |v116|, |v116|
	v_max_f32_e32 v135, v141, v135
	v_max3_f32 v131, v131, v134, v135
	ds_bpermute_b32 v134, v1, v131
	s_cmpk_lt_u32 s38, 0x4000
	s_cselect_b64 s[0:1], -1, 0
	s_and_b64 s[2:3], s[0:1], exec
	s_cselect_b32 s5, 0, 0x4000000
	s_waitcnt lgkmcnt(0)
	v_max_f32_e32 v134, v134, v134
	v_max_f32_e32 v131, v131, v134
	ds_bpermute_b32 v134, v136, v131
	s_and_b32 s4, s38, 0x3fff
	s_waitcnt lgkmcnt(0)
	v_max_f32_e32 v134, v134, v134
	v_max_f32_e32 v131, v131, v134
	ds_bpermute_b32 v134, v137, v131
	s_waitcnt lgkmcnt(0)
	v_max_f32_e32 v134, v134, v134
	v_max_f32_e32 v131, v131, v134
	ds_bpermute_b32 v134, v138, v131
	s_waitcnt lgkmcnt(0)
	v_max_f32_e32 v134, v134, v134
	v_max_f32_e32 v131, v131, v134
	ds_bpermute_b32 v134, v139, v131
	s_waitcnt lgkmcnt(0)
	v_max_f32_e32 v134, v134, v134
	v_max_f32_e32 v131, v131, v134
	ds_bpermute_b32 v134, v140, v131
	s_waitcnt lgkmcnt(0)
; __device__ __forceinline__ void pt_proc(unsigned char* PT, const f32x4* v, int r, int lane) {
;     ...
;     amax = wave_max(amax); const float scale = amax > 0.f ? 127.f / amax : 0.f;
; #pragma unroll
;     for (int j = 0; j < 16; ++j) ((unsigned*)(tab + (size_t)j * PT_SLICE + (size_t)e * 256))[lane] = pack_i8x4(v[j].x * scale, v[j].y * scale, v[j].z * scale, v[j].w * scale);
	v_max_f32_e32 v134, v134, v134
	v_max_f32_e32 v131, v131, v134
	v_div_scale_f32 v134, s[2:3], v131, v131, s19
	v_rcp_f32_e32 v135, v134
	s_add_u32 s2, s33, s5
	s_addc_u32 s3, s46, 0
	s_lshl_b32 s5, s4, 8
	v_fma_f32 v141, -v134, v135, 1.0
	v_fmac_f32_e32 v135, v141, v135
	v_div_scale_f32 v141, vcc, s19, v131, s19
	v_mul_f32_e32 v142, v141, v135
	v_fma_f32 v143, -v134, v142, v141
	v_fmac_f32_e32 v142, v143, v135
	v_fma_f32 v134, -v134, v142, v141
	v_div_fmas_f32 v134, v134, v135, v142
	v_div_fixup_f32 v134, v134, v131, s19
	v_cmp_lt_f32_e32 vcc, 0, v131
	s_add_u32 s2, s2, s5
	s_addc_u32 s3, s3, 0
	v_cndmask_b32_e32 v141, 0, v134, vcc
	v_mul_f32_e32 v143, v79, v141
	v_mul_f32_e32 v142, v78, v141
	v_mul_f32_e32 v144, v80, v141
	v_mul_f32_e32 v145, v81, v141
	v_rndne_f32_e32 v143, v143
	v_rndne_f32_e32 v142, v142
	v_cvt_i32_f32_e32 v143, v143
	v_rndne_f32_e32 v144, v144
	v_rndne_f32_e32 v145, v145
	v_cvt_i32_f32_e32 v142, v142
	v_cvt_i32_f32_sdwa v144, v144 dst_sel:WORD_1 dst_unused:UNUSED_PAD src0_sel:DWORD
	v_cvt_i32_f32_e32 v145, v145
	v_lshlrev_b32_e32 v143, 8, v143
	v_and_b32_e32 v143, 0xff00, v143
	v_and_b32_e32 v144, 0xff0000, v144
	v_perm_b32 v142, v145, v142, s20
	v_or3_b32 v142, v142, v143, v144
	global_store_dword v132, v142, s[2:3] nt
	v_mul_f32_e32 v142, v75, v141
	v_lshl_add_u64 v[134:135], s[2:3], 0, v[132:133]
	v_mul_f32_e32 v132, v74, v141
	v_mul_f32_e32 v143, v76, v141
	v_mul_f32_e32 v144, v77, v141
	v_rndne_f32_e32 v142, v142
	v_rndne_f32_e32 v132, v132
	v_cvt_i32_f32_e32 v142, v142
	v_rndne_f32_e32 v143, v143
	v_rndne_f32_e32 v144, v144
	v_cvt_i32_f32_e32 v132, v132
	v_cvt_i32_f32_sdwa v143, v143 dst_sel:WORD_1 dst_unused:UNUSED_PAD src0_sel:DWORD
	v_cvt_i32_f32_e32 v144, v144
	v_lshlrev_b32_e32 v142, 8, v142
	v_and_b32_e32 v142, 0xff00, v142
	v_and_b32_e32 v143, 0xff0000, v143
	v_perm_b32 v132, v144, v132, s20
	v_or3_b32 v132, v132, v142, v143
	v_add_co_u32_e32 v142, vcc, s21, v134
	v_mul_f32_e32 v144, v73, v141
	s_nop 0
	v_addc_co_u32_e32 v143, vcc, 0, v135, vcc
	global_store_dword v[142:143], v132, off nt
	v_mul_f32_e32 v142, v71, v141
	v_mul_f32_e32 v132, v70, v141
	v_mul_f32_e32 v143, v72, v141
	v_rndne_f32_e32 v142, v142
	v_rndne_f32_e32 v132, v132
	v_cvt_i32_f32_e32 v142, v142
	v_rndne_f32_e32 v143, v143
	v_rndne_f32_e32 v144, v144
	v_cvt_i32_f32_e32 v132, v132
	v_cvt_i32_f32_sdwa v143, v143 dst_sel:WORD_1 dst_unused:UNUSED_PAD src0_sel:DWORD
	v_cvt_i32_f32_e32 v144, v144
	v_lshlrev_b32_e32 v142, 8, v142
	v_and_b32_e32 v142, 0xff00, v142
	v_and_b32_e32 v143, 0xff0000, v143
	v_perm_b32 v132, v144, v132, s20
	v_or3_b32 v132, v132, v142, v143
	v_add_co_u32_e32 v142, vcc, s22, v134
	v_mul_f32_e32 v144, v69, v141
	s_nop 0
	v_addc_co_u32_e32 v143, vcc, 0, v135, vcc
	global_store_dword v[142:143], v132, off nt
	v_mul_f32_e32 v142, v67, v141
	v_mul_f32_e32 v132, v66, v141
	v_mul_f32_e32 v143, v68, v141
	v_rndne_f32_e32 v142, v142
	v_rndne_f32_e32 v132, v132
	v_cvt_i32_f32_e32 v142, v142
	v_rndne_f32_e32 v143, v143
	v_rndne_f32_e32 v144, v144
	v_cvt_i32_f32_e32 v132, v132
	v_cvt_i32_f32_sdwa v143, v143 dst_sel:WORD_1 dst_unused:UNUSED_PAD src0_sel:DWORD
	v_cvt_i32_f32_e32 v144, v144
	v_lshlrev_b32_e32 v142, 8, v142
	v_and_b32_e32 v142, 0xff00, v142
	v_and_b32_e32 v143, 0xff0000, v143
	v_perm_b32 v132, v144, v132, s20
	v_or3_b32 v132, v132, v142, v143
	v_add_co_u32_e32 v142, vcc, s23, v134
	v_mul_f32_e32 v144, v97, v141
	s_nop 0
	v_addc_co_u32_e32 v143, vcc, 0, v135, vcc
	global_store_dword v[142:143], v132, off nt
	v_mul_f32_e32 v142, v95, v141
	v_mul_f32_e32 v132, v94, v141
	v_mul_f32_e32 v143, v96, v141
	v_rndne_f32_e32 v142, v142
	v_rndne_f32_e32 v132, v132
	v_cvt_i32_f32_e32 v142, v142
	v_rndne_f32_e32 v143, v143
	v_rndne_f32_e32 v144, v144
	v_cvt_i32_f32_e32 v132, v132
	v_cvt_i32_f32_sdwa v143, v143 dst_sel:WORD_1 dst_unused:UNUSED_PAD src0_sel:DWORD
	v_cvt_i32_f32_e32 v144, v144
	v_lshlrev_b32_e32 v142, 8, v142
	v_and_b32_e32 v142, 0xff00, v142
	v_and_b32_e32 v143, 0xff0000, v143
	v_perm_b32 v132, v144, v132, s20
	v_or3_b32 v132, v132, v142, v143
	v_add_co_u32_e32 v142, vcc, s24, v134
	v_mul_f32_e32 v144, v93, v141
	s_nop 0
	v_addc_co_u32_e32 v143, vcc, 0, v135, vcc
	global_store_dword v[142:143], v132, off nt
	v_mul_f32_e32 v142, v91, v141
	v_mul_f32_e32 v132, v90, v141
	v_mul_f32_e32 v143, v92, v141
	v_rndne_f32_e32 v142, v142
	v_rndne_f32_e32 v132, v132
	v_cvt_i32_f32_e32 v142, v142
	v_rndne_f32_e32 v143, v143
	v_rndne_f32_e32 v144, v144
	v_cvt_i32_f32_e32 v132, v132
	v_cvt_i32_f32_sdwa v143, v143 dst_sel:WORD_1 dst_unused:UNUSED_PAD src0_sel:DWORD
	v_cvt_i32_f32_e32 v144, v144
	v_lshlrev_b32_e32 v142, 8, v142
	v_and_b32_e32 v142, 0xff00, v142
	v_and_b32_e32 v143, 0xff0000, v143
	v_perm_b32 v132, v144, v132, s20
	v_or3_b32 v132, v132, v142, v143
	v_add_co_u32_e32 v142, vcc, s25, v134
	v_mul_f32_e32 v144, v89, v141
	s_nop 0
	v_addc_co_u32_e32 v143, vcc, 0, v135, vcc
	global_store_dword v[142:143], v132, off nt
	v_mul_f32_e32 v142, v87, v141
	v_mul_f32_e32 v132, v86, v141
	v_mul_f32_e32 v143, v88, v141
	v_rndne_f32_e32 v142, v142
	v_rndne_f32_e32 v132, v132
	v_cvt_i32_f32_e32 v142, v142
	v_rndne_f32_e32 v143, v143
	v_rndne_f32_e32 v144, v144
	v_cvt_i32_f32_e32 v132, v132
	v_cvt_i32_f32_sdwa v143, v143 dst_sel:WORD_1 dst_unused:UNUSED_PAD src0_sel:DWORD
	v_cvt_i32_f32_e32 v144, v144
	v_lshlrev_b32_e32 v142, 8, v142
	v_and_b32_e32 v142, 0xff00, v142
	v_and_b32_e32 v143, 0xff0000, v143
	v_perm_b32 v132, v144, v132, s20
	v_or3_b32 v132, v132, v142, v143
	v_add_co_u32_e32 v142, vcc, s26, v134
	v_mul_f32_e32 v144, v85, v141
	s_nop 0
	v_addc_co_u32_e32 v143, vcc, 0, v135, vcc
	global_store_dword v[142:143], v132, off nt
; __device__ __forceinline__ void pt_proc(unsigned char* PT, const f32x4* v, int r, int lane) {
;     ...
;     for (int j = 0; j < 16; ++j) ((unsigned*)(tab + (size_t)j * PT_SLICE + (size_t)e * 256))[lane] = pack_i8x4(v[j].x * scale, v[j].y * scale, v[j].z * scale, v[j].w * scale);
;     if (lane == 0) ((float*)(PT + (tb ? PT_VS : PT_US)))[e] = amax * (1.f / 127.f);
; __device__ __forceinline__ void phase_peer_tables(const Frame& F, const Args& a, int r_lo, int r_hi, int gw, int NGW) {
;     ...
;     for (;;) {
;         const int r1 = r + NGW; const bool h1 = r1 < r_hi;
;         if (h1) pt_load(a.in[17], a.in[18], vB, r1, lane);
;         pt_proc(PT, vA, r, lane);
;         if (!h1) break;
;         const int r2 = r1 + NGW; const bool h2 = r2 < r_hi;
;         if (h2) pt_load(a.in[17], a.in[18], vA, r2, lane);
;         pt_proc(PT, vB, r1, lane);
;         if (!h2) break;
;         r = r2;
;     }
	v_mul_f32_e32 v142, v83, v141
	v_mul_f32_e32 v132, v82, v141
	v_mul_f32_e32 v143, v84, v141
	v_rndne_f32_e32 v142, v142
	v_rndne_f32_e32 v132, v132
	v_cvt_i32_f32_e32 v142, v142
	v_rndne_f32_e32 v143, v143
	v_rndne_f32_e32 v144, v144
	v_cvt_i32_f32_e32 v132, v132
	v_cvt_i32_f32_sdwa v143, v143 dst_sel:WORD_1 dst_unused:UNUSED_PAD src0_sel:DWORD
	v_cvt_i32_f32_e32 v144, v144
	v_lshlrev_b32_e32 v142, 8, v142
	v_and_b32_e32 v142, 0xff00, v142
	v_and_b32_e32 v143, 0xff0000, v143
	v_perm_b32 v132, v144, v132, s20
	v_or3_b32 v132, v132, v142, v143
	v_add_co_u32_e32 v142, vcc, s27, v134
	v_mul_f32_e32 v144, v113, v141
	s_nop 0
	v_addc_co_u32_e32 v143, vcc, 0, v135, vcc
	global_store_dword v[142:143], v132, off nt
	v_mul_f32_e32 v142, v111, v141
	v_mul_f32_e32 v132, v110, v141
	v_mul_f32_e32 v143, v112, v141
	v_rndne_f32_e32 v142, v142
	v_rndne_f32_e32 v132, v132
	v_cvt_i32_f32_e32 v142, v142
	v_rndne_f32_e32 v143, v143
	v_rndne_f32_e32 v144, v144
	v_cvt_i32_f32_e32 v132, v132
	v_cvt_i32_f32_sdwa v143, v143 dst_sel:WORD_1 dst_unused:UNUSED_PAD src0_sel:DWORD
	v_cvt_i32_f32_e32 v144, v144
	v_lshlrev_b32_e32 v142, 8, v142
	v_and_b32_e32 v142, 0xff00, v142
	v_and_b32_e32 v143, 0xff0000, v143
	v_perm_b32 v132, v144, v132, s20
	v_or3_b32 v132, v132, v142, v143
	v_add_co_u32_e32 v142, vcc, s28, v134
	v_mul_f32_e32 v144, v109, v141
	s_nop 0
	v_addc_co_u32_e32 v143, vcc, 0, v135, vcc
	global_store_dword v[142:143], v132, off nt
	v_mul_f32_e32 v142, v107, v141
	v_mul_f32_e32 v132, v106, v141
	v_mul_f32_e32 v143, v108, v141
	v_rndne_f32_e32 v142, v142
	v_rndne_f32_e32 v132, v132
	v_cvt_i32_f32_e32 v142, v142
	v_rndne_f32_e32 v143, v143
	v_rndne_f32_e32 v144, v144
	v_cvt_i32_f32_e32 v132, v132
	v_cvt_i32_f32_sdwa v143, v143 dst_sel:WORD_1 dst_unused:UNUSED_PAD src0_sel:DWORD
	v_cvt_i32_f32_e32 v144, v144
	v_lshlrev_b32_e32 v142, 8, v142
	v_and_b32_e32 v142, 0xff00, v142
	v_and_b32_e32 v143, 0xff0000, v143
	v_perm_b32 v132, v144, v132, s20
	v_or3_b32 v132, v132, v142, v143
	v_add_co_u32_e32 v142, vcc, s29, v134
	v_mul_f32_e32 v144, v105, v141
	s_nop 0
	v_addc_co_u32_e32 v143, vcc, 0, v135, vcc
	global_store_dword v[142:143], v132, off nt
	v_mul_f32_e32 v142, v103, v141
	v_mul_f32_e32 v132, v102, v141
	v_mul_f32_e32 v143, v104, v141
	v_rndne_f32_e32 v142, v142
	v_rndne_f32_e32 v132, v132
	v_cvt_i32_f32_e32 v142, v142
	v_rndne_f32_e32 v143, v143
	v_rndne_f32_e32 v144, v144
	v_cvt_i32_f32_e32 v132, v132
	v_cvt_i32_f32_sdwa v143, v143 dst_sel:WORD_1 dst_unused:UNUSED_PAD src0_sel:DWORD
	v_cvt_i32_f32_e32 v144, v144
	v_lshlrev_b32_e32 v142, 8, v142
	v_and_b32_e32 v142, 0xff00, v142
	v_and_b32_e32 v143, 0xff0000, v143
	v_perm_b32 v132, v144, v132, s20
	v_or3_b32 v132, v132, v142, v143
	v_add_co_u32_e32 v142, vcc, s30, v134
	v_mul_f32_e32 v144, v101, v141
	s_nop 0
	v_addc_co_u32_e32 v143, vcc, 0, v135, vcc
	global_store_dword v[142:143], v132, off nt
	v_mul_f32_e32 v142, v99, v141
	v_mul_f32_e32 v132, v98, v141
	v_mul_f32_e32 v143, v100, v141
	v_rndne_f32_e32 v142, v142
	v_rndne_f32_e32 v132, v132
	v_cvt_i32_f32_e32 v142, v142
	v_rndne_f32_e32 v143, v143
	v_rndne_f32_e32 v144, v144
	v_cvt_i32_f32_e32 v132, v132
	v_cvt_i32_f32_sdwa v143, v143 dst_sel:WORD_1 dst_unused:UNUSED_PAD src0_sel:DWORD
	v_cvt_i32_f32_e32 v144, v144
	v_lshlrev_b32_e32 v142, 8, v142
	v_and_b32_e32 v142, 0xff00, v142
	v_and_b32_e32 v143, 0xff0000, v143
	v_perm_b32 v132, v144, v132, s20
	v_or3_b32 v132, v132, v142, v143
	v_add_co_u32_e32 v142, vcc, s31, v134
	v_mul_f32_e32 v144, v129, v141
	s_nop 0
	v_addc_co_u32_e32 v143, vcc, 0, v135, vcc
	global_store_dword v[142:143], v132, off nt
	v_mul_f32_e32 v142, v127, v141
	v_mul_f32_e32 v132, v126, v141
	v_mul_f32_e32 v143, v128, v141
	v_rndne_f32_e32 v142, v142
	v_rndne_f32_e32 v132, v132
	v_cvt_i32_f32_e32 v142, v142
	v_rndne_f32_e32 v143, v143
	v_rndne_f32_e32 v144, v144
	v_cvt_i32_f32_e32 v132, v132
	v_cvt_i32_f32_sdwa v143, v143 dst_sel:WORD_1 dst_unused:UNUSED_PAD src0_sel:DWORD
	v_cvt_i32_f32_e32 v144, v144
	v_lshlrev_b32_e32 v142, 8, v142
	v_and_b32_e32 v142, 0xff00, v142
	v_and_b32_e32 v143, 0xff0000, v143
	v_perm_b32 v132, v144, v132, s20
	v_or3_b32 v132, v132, v142, v143
	v_add_co_u32_e32 v142, vcc, s34, v134
	v_mul_f32_e32 v144, v125, v141
	s_nop 0
	v_addc_co_u32_e32 v143, vcc, 0, v135, vcc
	global_store_dword v[142:143], v132, off nt
	v_mul_f32_e32 v142, v123, v141
	v_mul_f32_e32 v132, v122, v141
	v_mul_f32_e32 v143, v124, v141
	v_rndne_f32_e32 v142, v142
	v_rndne_f32_e32 v132, v132
	v_cvt_i32_f32_e32 v142, v142
	v_rndne_f32_e32 v143, v143
	v_rndne_f32_e32 v144, v144
	v_cvt_i32_f32_e32 v132, v132
	v_cvt_i32_f32_sdwa v143, v143 dst_sel:WORD_1 dst_unused:UNUSED_PAD src0_sel:DWORD
	v_cvt_i32_f32_e32 v144, v144
	v_lshlrev_b32_e32 v142, 8, v142
	v_and_b32_e32 v142, 0xff00, v142
	v_and_b32_e32 v143, 0xff0000, v143
	v_perm_b32 v132, v144, v132, s20
	v_or3_b32 v132, v132, v142, v143
	v_add_co_u32_e32 v142, vcc, s35, v134
	v_mul_f32_e32 v144, v121, v141
	s_nop 0
	v_addc_co_u32_e32 v143, vcc, 0, v135, vcc
	global_store_dword v[142:143], v132, off nt
	v_mul_f32_e32 v142, v119, v141
	v_mul_f32_e32 v132, v118, v141
	v_mul_f32_e32 v143, v120, v141
	v_rndne_f32_e32 v142, v142
	v_rndne_f32_e32 v132, v132
	v_cvt_i32_f32_e32 v142, v142
	v_rndne_f32_e32 v143, v143
	v_rndne_f32_e32 v144, v144
	v_cvt_i32_f32_e32 v132, v132
	v_cvt_i32_f32_sdwa v143, v143 dst_sel:WORD_1 dst_unused:UNUSED_PAD src0_sel:DWORD
	v_cvt_i32_f32_e32 v144, v144
	v_lshlrev_b32_e32 v142, 8, v142
	v_and_b32_e32 v142, 0xff00, v142
	v_and_b32_e32 v143, 0xff0000, v143
	v_perm_b32 v132, v144, v132, s20
	v_or3_b32 v132, v132, v142, v143
	v_add_co_u32_e32 v142, vcc, s36, v134
	s_nop 1
	v_addc_co_u32_e32 v143, vcc, 0, v135, vcc
	global_store_dword v[142:143], v132, off nt
	v_mul_f32_e32 v142, v115, v141
	v_mul_f32_e32 v132, v114, v141
	v_mul_f32_e32 v143, v116, v141
	v_mul_f32_e32 v141, v117, v141
	v_rndne_f32_e32 v142, v142
	v_rndne_f32_e32 v132, v132
	v_cvt_i32_f32_e32 v142, v142
	v_rndne_f32_e32 v143, v143
	v_rndne_f32_e32 v141, v141
	v_cvt_i32_f32_e32 v132, v132
	v_cvt_i32_f32_sdwa v143, v143 dst_sel:WORD_1 dst_unused:UNUSED_PAD src0_sel:DWORD
	v_cvt_i32_f32_e32 v141, v141
	v_lshlrev_b32_e32 v142, 8, v142
	v_and_b32_e32 v142, 0xff00, v142
	v_and_b32_e32 v143, 0xff0000, v143
	v_perm_b32 v132, v141, v132, s20
	v_add_co_u32_e32 v134, vcc, 0x3c00000, v134
	v_or3_b32 v132, v132, v142, v143
	s_nop 0
	v_addc_co_u32_e32 v135, vcc, 0, v135, vcc
	global_store_dword v[134:135], v132, off nt
	s_and_saveexec_b64 s[2:3], s[6:7]
	s_cbranch_execz .LBB0_227
	s_and_b64 s[0:1], s[0:1], exec
	s_cselect_b32 s0, s37, 0x8010000
	s_add_u32 s0, s33, s0
	s_addc_u32 s1, s46, 0
	s_lshl_b32 s4, s4, 2
	v_mul_f32_e32 v131, 0x3c010204, v131
	v_mov_b32_e32 v132, s4
	global_store_dword v132, v131, s[0:1] nt
	s_branch .LBB0_227

; __device__ __forceinline__ void pt_proc(unsigned char* PT, const f32x4* v, int r, int lane) {
;     const int tb = r >> 14, e = r & 16383; unsigned char* tab = PT + (tb ? PT_V8 : 0); float amax = 0.f;
; #pragma unroll
;     for (int j = 0; j < 16; ++j) amax = fmaxf(fmaxf(amax, fmaxf(fabsf(v[j].x), fabsf(v[j].y))), fmaxf(fabsf(v[j].z), fabsf(v[j].w)));
;     amax = wave_max(amax); const float scale = amax > 0.f ? 127.f / amax : 0.f;
.Lpt3_1254:
	s_waitcnt vmcnt(1)
	v_max_f32_e64 v131, |v27|, |v27|
	v_max_f32_e64 v132, |v26|, |v26|
	v_max_f32_e32 v131, v132, v131
	v_max_f32_e64 v132, |v29|, |v29|
	v_max_f32_e64 v134, |v28|, |v28|
	v_max_f32_e32 v132, v134, v132
	v_max3_f32 v131, v131, 0, v132
	v_max_f32_e64 v132, |v3|, |v3|
	v_max_f32_e64 v134, |v2|, |v2|
	v_max_f32_e32 v132, v134, v132
	v_max_f32_e64 v134, |v5|, |v5|
	v_max_f32_e64 v135, |v4|, |v4|
	v_max_f32_e32 v134, v135, v134
	v_max3_f32 v131, v131, v132, v134
	v_max_f32_e64 v132, |v7|, |v7|
	v_max_f32_e64 v134, |v6|, |v6|
	v_max_f32_e32 v132, v134, v132
	v_max_f32_e64 v134, |v9|, |v9|
	v_max_f32_e64 v135, |v8|, |v8|
	v_max_f32_e32 v134, v135, v134
	v_max3_f32 v131, v131, v132, v134
	v_max_f32_e64 v132, |v11|, |v11|
	v_max_f32_e64 v134, |v10|, |v10|
	v_max_f32_e32 v132, v134, v132
	v_max_f32_e64 v134, |v13|, |v13|
	v_max_f32_e64 v135, |v12|, |v12|
	v_max_f32_e32 v134, v135, v134
	v_max3_f32 v131, v131, v132, v134
	v_max_f32_e64 v132, |v15|, |v15|
	v_max_f32_e64 v134, |v14|, |v14|
	v_max_f32_e32 v132, v134, v132
	v_max_f32_e64 v134, |v17|, |v17|
	v_max_f32_e64 v135, |v16|, |v16|
	v_max_f32_e32 v134, v135, v134
	v_max3_f32 v131, v131, v132, v134
	v_max_f32_e64 v132, |v19|, |v19|
	v_max_f32_e64 v134, |v18|, |v18|
	v_max_f32_e32 v132, v134, v132
	v_max_f32_e64 v134, |v21|, |v21|
	v_max_f32_e64 v135, |v20|, |v20|
	v_max_f32_e32 v134, v135, v134
	v_max3_f32 v131, v131, v132, v134
	v_max_f32_e64 v132, |v23|, |v23|
	v_max_f32_e64 v134, |v22|, |v22|
	v_max_f32_e32 v132, v134, v132
	v_max_f32_e64 v134, |v25|, |v25|
	v_max_f32_e64 v135, |v24|, |v24|
	v_max_f32_e32 v134, v135, v134
	v_max3_f32 v131, v131, v132, v134
	v_max_f32_e64 v132, |v35|, |v35|
	v_max_f32_e64 v134, |v34|, |v34|
	v_max_f32_e32 v132, v134, v132
	v_max_f32_e64 v134, |v37|, |v37|
	v_max_f32_e64 v135, |v36|, |v36|
	v_max_f32_e32 v134, v135, v134
	v_max3_f32 v131, v131, v132, v134
	v_max_f32_e64 v132, |v31|, |v31|
	v_max_f32_e64 v134, |v30|, |v30|
	v_max_f32_e32 v132, v134, v132
	v_max_f32_e64 v134, |v33|, |v33|
	v_max_f32_e64 v135, |v32|, |v32|
	v_max_f32_e32 v134, v135, v134
	v_max3_f32 v131, v131, v132, v134
	v_max_f32_e64 v132, |v39|, |v39|
	v_max_f32_e64 v134, |v38|, |v38|
	v_max_f32_e32 v132, v134, v132
	v_max_f32_e64 v134, |v41|, |v41|
	v_max_f32_e64 v135, |v40|, |v40|
	v_max_f32_e32 v134, v135, v134
	v_max3_f32 v131, v131, v132, v134
	v_max_f32_e64 v132, |v43|, |v43|
	v_max_f32_e64 v134, |v42|, |v42|
	v_max_f32_e32 v132, v134, v132
	v_max_f32_e64 v134, |v45|, |v45|
	v_max_f32_e64 v135, |v44|, |v44|
	v_max_f32_e32 v134, v135, v134
	v_max3_f32 v131, v131, v132, v134
	v_max_f32_e64 v132, |v47|, |v47|
	v_max_f32_e64 v134, |v46|, |v46|
	v_max_f32_e32 v132, v134, v132
	v_max_f32_e64 v134, |v49|, |v49|
	v_max_f32_e64 v135, |v48|, |v48|
	v_max_f32_e32 v134, v135, v134
	v_max3_f32 v131, v131, v132, v134
	v_max_f32_e64 v132, |v51|, |v51|
	v_max_f32_e64 v134, |v50|, |v50|
	v_max_f32_e32 v132, v134, v132
	v_max_f32_e64 v134, |v53|, |v53|
	v_max_f32_e64 v135, |v52|, |v52|
	v_max_f32_e32 v134, v135, v134
	v_max3_f32 v131, v131, v132, v134
	v_max_f32_e64 v132, |v55|, |v55|
	v_max_f32_e64 v134, |v54|, |v54|
	v_max_f32_e32 v132, v134, v132
	v_max_f32_e64 v134, |v57|, |v57|
	v_max_f32_e64 v135, |v56|, |v56|
	v_max_f32_e32 v134, v135, v134
	v_max3_f32 v131, v131, v132, v134
	v_max_f32_e64 v132, |v59|, |v59|
	v_max_f32_e64 v134, |v58|, |v58|
	v_max_f32_e32 v132, v134, v132
	v_max_f32_e64 v134, |v61|, |v61|
	v_max_f32_e64 v135, |v60|, |v60|
	v_max_f32_e32 v134, v135, v134
	v_max3_f32 v131, v131, v132, v134
	s_waitcnt vmcnt(0)
	v_max_f32_e64 v132, |v63|, |v63|
	v_max_f32_e64 v134, |v62|, |v62|
	v_max_f32_e32 v132, v134, v132
	v_max_f32_e64 v134, |v65|, |v65|
	v_max_f32_e64 v135, |v64|, |v64|
	v_max_f32_e32 v134, v135, v134
	v_max3_f32 v131, v131, v132, v134
	ds_bpermute_b32 v132, v1, v131
	s_cmpk_lt_u32 s41, 0x4000
	s_cselect_b64 s[4:5], -1, 0
	s_and_b64 s[8:9], s[4:5], exec
	s_cselect_b32 s43, 0, 0x4000000
	s_waitcnt lgkmcnt(0)
	v_max_f32_e32 v132, v132, v132
	v_max_f32_e32 v131, v131, v132
	ds_bpermute_b32 v132, v136, v131
	s_and_b32 s42, s41, 0x3fff
	s_waitcnt lgkmcnt(0)
	v_max_f32_e32 v132, v132, v132
	v_max_f32_e32 v131, v131, v132
	ds_bpermute_b32 v132, v137, v131
	s_waitcnt lgkmcnt(0)
	v_max_f32_e32 v132, v132, v132
	v_max_f32_e32 v131, v131, v132
	ds_bpermute_b32 v132, v138, v131
	s_waitcnt lgkmcnt(0)
	v_max_f32_e32 v132, v132, v132
	v_max_f32_e32 v131, v131, v132
	ds_bpermute_b32 v132, v139, v131
	s_waitcnt lgkmcnt(0)
	v_max_f32_e32 v132, v132, v132
	v_max_f32_e32 v131, v131, v132
	ds_bpermute_b32 v132, v140, v131
	s_waitcnt lgkmcnt(0)
; __device__ __forceinline__ float wave_max(float v) {
;     ...
;     for (int o = 1; o < 64; o <<= 1) v = fmaxf(v, __shfl_xor(v, o));
; __device__ __forceinline__ void pt_proc(unsigned char* PT, const f32x4* v, int r, int lane) {
;     ...
;     amax = wave_max(amax); const float scale = amax > 0.f ? 127.f / amax : 0.f;
; #pragma unroll
;     for (int j = 0; j < 16; ++j) ((unsigned*)(tab + (size_t)j * PT_SLICE + (size_t)e * 256))[lane] = pack_i8x4(v[j].x * scale, v[j].y * scale, v[j].z * scale, v[j].w * scale);
	v_max_f32_e32 v132, v132, v132
	v_max_f32_e32 v131, v131, v132
	v_div_scale_f32 v132, s[8:9], v131, v131, s22
	v_rcp_f32_e32 v134, v132
	s_add_u32 s8, s1, s43
	s_addc_u32 s9, s10, 0
	s_lshl_b32 s43, s42, 8
	v_fma_f32 v135, -v132, v134, 1.0
	v_fmac_f32_e32 v134, v135, v134
	v_div_scale_f32 v135, vcc, s22, v131, s22
	v_mul_f32_e32 v141, v135, v134
	v_fma_f32 v142, -v132, v141, v135
	v_fmac_f32_e32 v141, v142, v134
	v_fma_f32 v132, -v132, v141, v135
	v_div_fmas_f32 v132, v132, v134, v141
	v_div_fixup_f32 v132, v132, v131, s22
	v_cmp_lt_f32_e32 vcc, 0, v131
	s_add_u32 s8, s8, s43
	s_addc_u32 s9, s9, 0
	v_cndmask_b32_e32 v141, 0, v132, vcc
	v_mul_f32_e32 v143, v27, v141
	v_mul_f32_e32 v142, v26, v141
	v_mul_f32_e32 v144, v28, v141
	v_mul_f32_e32 v145, v29, v141
	v_rndne_f32_e32 v143, v143
	v_rndne_f32_e32 v142, v142
	v_cvt_i32_f32_e32 v143, v143
	v_rndne_f32_e32 v144, v144
	v_rndne_f32_e32 v145, v145
	v_cvt_i32_f32_e32 v142, v142
	v_cvt_i32_f32_sdwa v144, v144 dst_sel:WORD_1 dst_unused:UNUSED_PAD src0_sel:DWORD
	v_cvt_i32_f32_e32 v145, v145
	v_lshlrev_b32_e32 v143, 8, v143
	v_and_b32_e32 v143, 0xff00, v143
	v_and_b32_e32 v144, 0xff0000, v144
	v_perm_b32 v142, v145, v142, s23
	v_lshlrev_b32_e32 v132, 2, v194
	v_or3_b32 v142, v142, v143, v144
	v_mul_f32_e32 v143, v3, v141
	global_store_dword v132, v142, s[8:9] nt
	v_mul_f32_e32 v142, v2, v141
	v_mul_f32_e32 v144, v4, v141
	v_mul_f32_e32 v145, v5, v141
	v_rndne_f32_e32 v143, v143
	v_rndne_f32_e32 v142, v142
	v_cvt_i32_f32_e32 v143, v143
	v_rndne_f32_e32 v144, v144
	v_rndne_f32_e32 v145, v145
	v_cvt_i32_f32_e32 v142, v142
	v_cvt_i32_f32_sdwa v144, v144 dst_sel:WORD_1 dst_unused:UNUSED_PAD src0_sel:DWORD
	v_cvt_i32_f32_e32 v145, v145
	v_lshlrev_b32_e32 v143, 8, v143
	v_lshl_add_u64 v[134:135], s[8:9], 0, v[132:133]
	v_and_b32_e32 v143, 0xff00, v143
	v_and_b32_e32 v144, 0xff0000, v144
	v_perm_b32 v142, v145, v142, s23
	v_or3_b32 v144, v142, v143, v144
	v_add_co_u32_e32 v142, vcc, s24, v134
	v_mul_f32_e32 v145, v9, v141
	s_nop 0
	v_addc_co_u32_e32 v143, vcc, 0, v135, vcc
	global_store_dword v[142:143], v144, off nt
	v_mul_f32_e32 v143, v7, v141
	v_mul_f32_e32 v142, v6, v141
	v_mul_f32_e32 v144, v8, v141
	v_rndne_f32_e32 v143, v143
	v_rndne_f32_e32 v142, v142
	v_cvt_i32_f32_e32 v143, v143
	v_rndne_f32_e32 v144, v144
	v_rndne_f32_e32 v145, v145
	v_cvt_i32_f32_e32 v142, v142
	v_cvt_i32_f32_sdwa v144, v144 dst_sel:WORD_1 dst_unused:UNUSED_PAD src0_sel:DWORD
	v_cvt_i32_f32_e32 v145, v145
	v_lshlrev_b32_e32 v143, 8, v143
	v_and_b32_e32 v143, 0xff00, v143
	v_and_b32_e32 v144, 0xff0000, v144
	v_perm_b32 v142, v145, v142, s23
	v_or3_b32 v144, v142, v143, v144
	v_add_co_u32_e32 v142, vcc, s25, v134
	v_mul_f32_e32 v145, v13, v141
	s_nop 0
	v_addc_co_u32_e32 v143, vcc, 0, v135, vcc
	global_store_dword v[142:143], v144, off nt
	v_mul_f32_e32 v143, v11, v141
	v_mul_f32_e32 v142, v10, v141
	v_mul_f32_e32 v144, v12, v141
	v_rndne_f32_e32 v143, v143
	v_rndne_f32_e32 v142, v142
	v_cvt_i32_f32_e32 v143, v143
	v_rndne_f32_e32 v144, v144
	v_rndne_f32_e32 v145, v145
	v_cvt_i32_f32_e32 v142, v142
	v_cvt_i32_f32_sdwa v144, v144 dst_sel:WORD_1 dst_unused:UNUSED_PAD src0_sel:DWORD
	v_cvt_i32_f32_e32 v145, v145
	v_lshlrev_b32_e32 v143, 8, v143
	v_and_b32_e32 v143, 0xff00, v143
	v_and_b32_e32 v144, 0xff0000, v144
	v_perm_b32 v142, v145, v142, s23
	v_or3_b32 v144, v142, v143, v144
	v_add_co_u32_e32 v142, vcc, s26, v134
	v_mul_f32_e32 v145, v17, v141
	s_nop 0
	v_addc_co_u32_e32 v143, vcc, 0, v135, vcc
	global_store_dword v[142:143], v144, off nt
	v_mul_f32_e32 v143, v15, v141
	v_mul_f32_e32 v142, v14, v141
	v_mul_f32_e32 v144, v16, v141
	v_rndne_f32_e32 v143, v143
	v_rndne_f32_e32 v142, v142
	v_cvt_i32_f32_e32 v143, v143
	v_rndne_f32_e32 v144, v144
	v_rndne_f32_e32 v145, v145
	v_cvt_i32_f32_e32 v142, v142
	v_cvt_i32_f32_sdwa v144, v144 dst_sel:WORD_1 dst_unused:UNUSED_PAD src0_sel:DWORD
	v_cvt_i32_f32_e32 v145, v145
	v_lshlrev_b32_e32 v143, 8, v143
	v_and_b32_e32 v143, 0xff00, v143
	v_and_b32_e32 v144, 0xff0000, v144
	v_perm_b32 v142, v145, v142, s23
	v_or3_b32 v144, v142, v143, v144
	v_add_co_u32_e32 v142, vcc, s27, v134
	v_mul_f32_e32 v145, v21, v141
	s_nop 0
	v_addc_co_u32_e32 v143, vcc, 0, v135, vcc
	global_store_dword v[142:143], v144, off nt
	v_mul_f32_e32 v143, v19, v141
	v_mul_f32_e32 v142, v18, v141
	v_mul_f32_e32 v144, v20, v141
	v_rndne_f32_e32 v143, v143
	v_rndne_f32_e32 v142, v142
	v_cvt_i32_f32_e32 v143, v143
	v_rndne_f32_e32 v144, v144
	v_rndne_f32_e32 v145, v145
	v_cvt_i32_f32_e32 v142, v142
	v_cvt_i32_f32_sdwa v144, v144 dst_sel:WORD_1 dst_unused:UNUSED_PAD src0_sel:DWORD
	v_cvt_i32_f32_e32 v145, v145
	v_lshlrev_b32_e32 v143, 8, v143
	v_and_b32_e32 v143, 0xff00, v143
	v_and_b32_e32 v144, 0xff0000, v144
	v_perm_b32 v142, v145, v142, s23
	v_or3_b32 v144, v142, v143, v144
	v_add_co_u32_e32 v142, vcc, s28, v134
	v_mul_f32_e32 v145, v25, v141
	s_nop 0
	v_addc_co_u32_e32 v143, vcc, 0, v135, vcc
	global_store_dword v[142:143], v144, off nt
	v_mul_f32_e32 v143, v23, v141
	v_mul_f32_e32 v142, v22, v141
	v_mul_f32_e32 v144, v24, v141
	v_rndne_f32_e32 v143, v143
	v_rndne_f32_e32 v142, v142
	v_cvt_i32_f32_e32 v143, v143
	v_rndne_f32_e32 v144, v144
	v_rndne_f32_e32 v145, v145
	v_cvt_i32_f32_e32 v142, v142
	v_cvt_i32_f32_sdwa v144, v144 dst_sel:WORD_1 dst_unused:UNUSED_PAD src0_sel:DWORD
	v_cvt_i32_f32_e32 v145, v145
	v_lshlrev_b32_e32 v143, 8, v143
	v_and_b32_e32 v143, 0xff00, v143
	v_and_b32_e32 v144, 0xff0000, v144
	v_perm_b32 v142, v145, v142, s23
	v_or3_b32 v144, v142, v143, v144
	v_add_co_u32_e32 v142, vcc, s29, v134
	v_mul_f32_e32 v145, v37, v141
	s_nop 0
	v_addc_co_u32_e32 v143, vcc, 0, v135, vcc
; __device__ __forceinline__ void pt_proc(unsigned char* PT, const f32x4* v, int r, int lane) {
;     ...
;     for (int j = 0; j < 16; ++j) ((unsigned*)(tab + (size_t)j * PT_SLICE + (size_t)e * 256))[lane] = pack_i8x4(v[j].x * scale, v[j].y * scale, v[j].z * scale, v[j].w * scale);
;     if (lane == 0) ((float*)(PT + (tb ? PT_VS : PT_US)))[e] = amax * (1.f / 127.f);
	global_store_dword v[142:143], v144, off nt
	v_mul_f32_e32 v143, v35, v141
	v_mul_f32_e32 v142, v34, v141
	v_mul_f32_e32 v144, v36, v141
	v_rndne_f32_e32 v143, v143
	v_rndne_f32_e32 v142, v142
	v_cvt_i32_f32_e32 v143, v143
	v_rndne_f32_e32 v144, v144
	v_rndne_f32_e32 v145, v145
	v_cvt_i32_f32_e32 v142, v142
	v_cvt_i32_f32_sdwa v144, v144 dst_sel:WORD_1 dst_unused:UNUSED_PAD src0_sel:DWORD
	v_cvt_i32_f32_e32 v145, v145
	v_lshlrev_b32_e32 v143, 8, v143
	v_and_b32_e32 v143, 0xff00, v143
	v_and_b32_e32 v144, 0xff0000, v144
	v_perm_b32 v142, v145, v142, s23
	v_or3_b32 v144, v142, v143, v144
	v_add_co_u32_e32 v142, vcc, s30, v134
	v_mul_f32_e32 v145, v33, v141
	s_nop 0
	v_addc_co_u32_e32 v143, vcc, 0, v135, vcc
	global_store_dword v[142:143], v144, off nt
	v_mul_f32_e32 v143, v31, v141
	v_mul_f32_e32 v142, v30, v141
	v_mul_f32_e32 v144, v32, v141
	v_rndne_f32_e32 v143, v143
	v_rndne_f32_e32 v142, v142
	v_cvt_i32_f32_e32 v143, v143
	v_rndne_f32_e32 v144, v144
	v_rndne_f32_e32 v145, v145
	v_cvt_i32_f32_e32 v142, v142
	v_cvt_i32_f32_sdwa v144, v144 dst_sel:WORD_1 dst_unused:UNUSED_PAD src0_sel:DWORD
	v_cvt_i32_f32_e32 v145, v145
	v_lshlrev_b32_e32 v143, 8, v143
	v_and_b32_e32 v143, 0xff00, v143
	v_and_b32_e32 v144, 0xff0000, v144
	v_perm_b32 v142, v145, v142, s23
	v_or3_b32 v144, v142, v143, v144
	v_add_co_u32_e32 v142, vcc, s31, v134
	v_mul_f32_e32 v145, v41, v141
	s_nop 0
	v_addc_co_u32_e32 v143, vcc, 0, v135, vcc
	global_store_dword v[142:143], v144, off nt
	v_mul_f32_e32 v143, v39, v141
	v_mul_f32_e32 v142, v38, v141
	v_mul_f32_e32 v144, v40, v141
	v_rndne_f32_e32 v143, v143
	v_rndne_f32_e32 v142, v142
	v_cvt_i32_f32_e32 v143, v143
	v_rndne_f32_e32 v144, v144
	v_rndne_f32_e32 v145, v145
	v_cvt_i32_f32_e32 v142, v142
	v_cvt_i32_f32_sdwa v144, v144 dst_sel:WORD_1 dst_unused:UNUSED_PAD src0_sel:DWORD
	v_cvt_i32_f32_e32 v145, v145
	v_lshlrev_b32_e32 v143, 8, v143
	v_and_b32_e32 v143, 0xff00, v143
	v_and_b32_e32 v144, 0xff0000, v144
	v_perm_b32 v142, v145, v142, s23
	v_or3_b32 v144, v142, v143, v144
	v_add_co_u32_e32 v142, vcc, s33, v134
	v_mul_f32_e32 v145, v45, v141
	s_nop 0
	v_addc_co_u32_e32 v143, vcc, 0, v135, vcc
	global_store_dword v[142:143], v144, off nt
	v_mul_f32_e32 v143, v43, v141
	v_mul_f32_e32 v142, v42, v141
	v_mul_f32_e32 v144, v44, v141
	v_rndne_f32_e32 v143, v143
	v_rndne_f32_e32 v142, v142
	v_cvt_i32_f32_e32 v143, v143
	v_rndne_f32_e32 v144, v144
	v_rndne_f32_e32 v145, v145
	v_cvt_i32_f32_e32 v142, v142
	v_cvt_i32_f32_sdwa v144, v144 dst_sel:WORD_1 dst_unused:UNUSED_PAD src0_sel:DWORD
	v_cvt_i32_f32_e32 v145, v145
	v_lshlrev_b32_e32 v143, 8, v143
	v_and_b32_e32 v143, 0xff00, v143
	v_and_b32_e32 v144, 0xff0000, v144
	v_perm_b32 v142, v145, v142, s23
	v_or3_b32 v144, v142, v143, v144
	v_add_co_u32_e32 v142, vcc, s34, v134
	v_mul_f32_e32 v145, v49, v141
	s_nop 0
	v_addc_co_u32_e32 v143, vcc, 0, v135, vcc
	global_store_dword v[142:143], v144, off nt
	v_mul_f32_e32 v143, v47, v141
	v_mul_f32_e32 v142, v46, v141
	v_mul_f32_e32 v144, v48, v141
	v_rndne_f32_e32 v143, v143
	v_rndne_f32_e32 v142, v142
	v_cvt_i32_f32_e32 v143, v143
	v_rndne_f32_e32 v144, v144
	v_rndne_f32_e32 v145, v145
	v_cvt_i32_f32_e32 v142, v142
	v_cvt_i32_f32_sdwa v144, v144 dst_sel:WORD_1 dst_unused:UNUSED_PAD src0_sel:DWORD
	v_cvt_i32_f32_e32 v145, v145
	v_lshlrev_b32_e32 v143, 8, v143
	v_and_b32_e32 v143, 0xff00, v143
	v_and_b32_e32 v144, 0xff0000, v144
	v_perm_b32 v142, v145, v142, s23
	v_or3_b32 v144, v142, v143, v144
	v_add_co_u32_e32 v142, vcc, s35, v134
	v_mul_f32_e32 v145, v53, v141
	s_nop 0
	v_addc_co_u32_e32 v143, vcc, 0, v135, vcc
	global_store_dword v[142:143], v144, off nt
	v_mul_f32_e32 v143, v51, v141
	v_mul_f32_e32 v142, v50, v141
	v_mul_f32_e32 v144, v52, v141
	v_rndne_f32_e32 v143, v143
	v_rndne_f32_e32 v142, v142
	v_cvt_i32_f32_e32 v143, v143
	v_rndne_f32_e32 v144, v144
	v_rndne_f32_e32 v145, v145
	v_cvt_i32_f32_e32 v142, v142
	v_cvt_i32_f32_sdwa v144, v144 dst_sel:WORD_1 dst_unused:UNUSED_PAD src0_sel:DWORD
	v_cvt_i32_f32_e32 v145, v145
	v_lshlrev_b32_e32 v143, 8, v143
	v_and_b32_e32 v143, 0xff00, v143
	v_and_b32_e32 v144, 0xff0000, v144
	v_perm_b32 v142, v145, v142, s23
	v_or3_b32 v144, v142, v143, v144
	v_add_co_u32_e32 v142, vcc, s36, v134
	v_mul_f32_e32 v145, v57, v141
	s_nop 0
	v_addc_co_u32_e32 v143, vcc, 0, v135, vcc
	global_store_dword v[142:143], v144, off nt
	v_mul_f32_e32 v143, v55, v141
	v_mul_f32_e32 v142, v54, v141
	v_mul_f32_e32 v144, v56, v141
	v_rndne_f32_e32 v143, v143
	v_rndne_f32_e32 v142, v142
	v_cvt_i32_f32_e32 v143, v143
	v_rndne_f32_e32 v144, v144
	v_rndne_f32_e32 v145, v145
	v_cvt_i32_f32_e32 v142, v142
	v_cvt_i32_f32_sdwa v144, v144 dst_sel:WORD_1 dst_unused:UNUSED_PAD src0_sel:DWORD
	v_cvt_i32_f32_e32 v145, v145
	v_lshlrev_b32_e32 v143, 8, v143
	v_and_b32_e32 v143, 0xff00, v143
	v_and_b32_e32 v144, 0xff0000, v144
	v_perm_b32 v142, v145, v142, s23
	v_or3_b32 v144, v142, v143, v144
	v_add_co_u32_e32 v142, vcc, s37, v134
	v_mul_f32_e32 v145, v61, v141
	s_nop 0
	v_addc_co_u32_e32 v143, vcc, 0, v135, vcc
	global_store_dword v[142:143], v144, off nt
	v_mul_f32_e32 v143, v59, v141
	v_mul_f32_e32 v142, v58, v141
	v_mul_f32_e32 v144, v60, v141
	v_rndne_f32_e32 v143, v143
	v_rndne_f32_e32 v142, v142
	v_cvt_i32_f32_e32 v143, v143
	v_rndne_f32_e32 v144, v144
	v_rndne_f32_e32 v145, v145
	v_cvt_i32_f32_e32 v142, v142
	v_cvt_i32_f32_sdwa v144, v144 dst_sel:WORD_1 dst_unused:UNUSED_PAD src0_sel:DWORD
	v_cvt_i32_f32_e32 v145, v145
	v_lshlrev_b32_e32 v143, 8, v143
	v_and_b32_e32 v143, 0xff00, v143
	v_and_b32_e32 v144, 0xff0000, v144
	v_perm_b32 v142, v145, v142, s23
	v_or3_b32 v144, v142, v143, v144
	v_add_co_u32_e32 v142, vcc, s38, v134
	s_nop 1
	v_addc_co_u32_e32 v143, vcc, 0, v135, vcc
	global_store_dword v[142:143], v144, off nt
	v_mul_f32_e32 v143, v63, v141
	v_mul_f32_e32 v142, v62, v141
	v_mul_f32_e32 v144, v64, v141
	v_mul_f32_e32 v141, v65, v141
	v_rndne_f32_e32 v143, v143
	v_rndne_f32_e32 v142, v142
	v_cvt_i32_f32_e32 v143, v143
	v_rndne_f32_e32 v144, v144
	v_rndne_f32_e32 v141, v141
	v_cvt_i32_f32_e32 v142, v142
	v_cvt_i32_f32_sdwa v144, v144 dst_sel:WORD_1 dst_unused:UNUSED_PAD src0_sel:DWORD
	v_cvt_i32_f32_e32 v141, v141
	v_lshlrev_b32_e32 v143, 8, v143
	v_and_b32_e32 v143, 0xff00, v143
	v_and_b32_e32 v144, 0xff0000, v144
	v_perm_b32 v141, v141, v142, s23
	v_add_co_u32_e32 v134, vcc, 0x3c00000, v134
	v_or3_b32 v141, v141, v143, v144
	s_nop 0
	v_addc_co_u32_e32 v135, vcc, 0, v135, vcc
	global_store_dword v[134:135], v141, off nt
	s_and_saveexec_b64 s[8:9], s[6:7]
	s_cbranch_execnz .Lpt3_1256
	s_or_b64 exec, exec, s[8:9]
	s_andn2_b64 vcc, exec, s[2:3]
	s_mov_b64 s[2:3], -1
	s_cbranch_vccnz .Lpt3_1251
	s_branch .Lpt3_1257
.Lpt3_1256:
	s_and_b64 s[4:5], s[4:5], exec
	s_cselect_b32 s4, s39, 0x8010000
	s_add_u32 s4, s1, s4
	s_addc_u32 s5, s10, 0
	s_lshl_b32 s42, s42, 2
	v_mul_f32_e32 v131, 0x3c010204, v131
	v_mov_b32_e32 v134, s42
	global_store_dword v134, v131, s[4:5] nt
	s_or_b64 exec, exec, s[8:9]
	s_andn2_b64 vcc, exec, s[2:3]
	s_mov_b64 s[2:3], -1
	s_cbranch_vccnz .Lpt3_1251

; __device__ __forceinline__ float wave_max(float v) {
;     ...
;     for (int o = 1; o < 64; o <<= 1) v = fmaxf(v, __shfl_xor(v, o));
; __device__ __forceinline__ void pt_proc(unsigned char* PT, const f32x4* v, int r, int lane) {
;     ...
;     for (int j = 0; j < 16; ++j) amax = fmaxf(fmaxf(amax, fmaxf(fabsf(v[j].x), fabsf(v[j].y))), fmaxf(fabsf(v[j].z), fabsf(v[j].w)));
;     amax = wave_max(amax); const float scale = amax > 0.f ? 127.f / amax : 0.f;
.Lpt3_1259:
	v_max_f32_e64 v131, |v79|, |v79|
	v_max_f32_e64 v134, |v78|, |v78|
	v_max_f32_e32 v131, v134, v131
	v_max_f32_e64 v134, |v81|, |v81|
	v_max_f32_e64 v135, |v80|, |v80|
	v_max_f32_e32 v134, v135, v134
	v_max3_f32 v131, v131, 0, v134
	v_max_f32_e64 v134, |v75|, |v75|
	v_max_f32_e64 v135, |v74|, |v74|
	v_max_f32_e32 v134, v135, v134
	v_max_f32_e64 v135, |v77|, |v77|
	v_max_f32_e64 v141, |v76|, |v76|
	v_max_f32_e32 v135, v141, v135
	v_max3_f32 v131, v131, v134, v135
	v_max_f32_e64 v134, |v71|, |v71|
	v_max_f32_e64 v135, |v70|, |v70|
	v_max_f32_e32 v134, v135, v134
	v_max_f32_e64 v135, |v73|, |v73|
	v_max_f32_e64 v141, |v72|, |v72|
	v_max_f32_e32 v135, v141, v135
	v_max3_f32 v131, v131, v134, v135
	v_max_f32_e64 v134, |v67|, |v67|
	v_max_f32_e64 v135, |v66|, |v66|
	v_max_f32_e32 v134, v135, v134
	v_max_f32_e64 v135, |v69|, |v69|
	v_max_f32_e64 v141, |v68|, |v68|
	v_max_f32_e32 v135, v141, v135
	v_max3_f32 v131, v131, v134, v135
	v_max_f32_e64 v134, |v95|, |v95|
	v_max_f32_e64 v135, |v94|, |v94|
	v_max_f32_e32 v134, v135, v134
	v_max_f32_e64 v135, |v97|, |v97|
	v_max_f32_e64 v141, |v96|, |v96|
	v_max_f32_e32 v135, v141, v135
	v_max3_f32 v131, v131, v134, v135
	v_max_f32_e64 v134, |v91|, |v91|
	v_max_f32_e64 v135, |v90|, |v90|
	v_max_f32_e32 v134, v135, v134
	v_max_f32_e64 v135, |v93|, |v93|
	v_max_f32_e64 v141, |v92|, |v92|
	v_max_f32_e32 v135, v141, v135
	v_max3_f32 v131, v131, v134, v135
	v_max_f32_e64 v134, |v87|, |v87|
	v_max_f32_e64 v135, |v86|, |v86|
	v_max_f32_e32 v134, v135, v134
	v_max_f32_e64 v135, |v89|, |v89|
	v_max_f32_e64 v141, |v88|, |v88|
	v_max_f32_e32 v135, v141, v135
	v_max3_f32 v131, v131, v134, v135
	v_max_f32_e64 v134, |v83|, |v83|
	v_max_f32_e64 v135, |v82|, |v82|
	v_max_f32_e32 v134, v135, v134
	v_max_f32_e64 v135, |v85|, |v85|
	v_max_f32_e64 v141, |v84|, |v84|
	v_max_f32_e32 v135, v141, v135
	v_max3_f32 v131, v131, v134, v135
	v_max_f32_e64 v134, |v111|, |v111|
	v_max_f32_e64 v135, |v110|, |v110|
	v_max_f32_e32 v134, v135, v134
	v_max_f32_e64 v135, |v113|, |v113|
	v_max_f32_e64 v141, |v112|, |v112|
	v_max_f32_e32 v135, v141, v135
	v_max3_f32 v131, v131, v134, v135
	v_max_f32_e64 v134, |v107|, |v107|
	v_max_f32_e64 v135, |v106|, |v106|
	v_max_f32_e32 v134, v135, v134
	v_max_f32_e64 v135, |v109|, |v109|
	v_max_f32_e64 v141, |v108|, |v108|
	v_max_f32_e32 v135, v141, v135
	v_max3_f32 v131, v131, v134, v135
	v_max_f32_e64 v134, |v103|, |v103|
	v_max_f32_e64 v135, |v102|, |v102|
	v_max_f32_e32 v134, v135, v134
	v_max_f32_e64 v135, |v105|, |v105|
	v_max_f32_e64 v141, |v104|, |v104|
	v_max_f32_e32 v135, v141, v135
	v_max3_f32 v131, v131, v134, v135
	v_max_f32_e64 v134, |v99|, |v99|
	v_max_f32_e64 v135, |v98|, |v98|
	v_max_f32_e32 v134, v135, v134
	v_max_f32_e64 v135, |v101|, |v101|
	v_max_f32_e64 v141, |v100|, |v100|
	v_max_f32_e32 v135, v141, v135
	v_max3_f32 v131, v131, v134, v135
	v_max_f32_e64 v134, |v127|, |v127|
	v_max_f32_e64 v135, |v126|, |v126|
	v_max_f32_e32 v134, v135, v134
	v_max_f32_e64 v135, |v129|, |v129|
	v_max_f32_e64 v141, |v128|, |v128|
	v_max_f32_e32 v135, v141, v135
	v_max3_f32 v131, v131, v134, v135
	v_max_f32_e64 v134, |v123|, |v123|
	v_max_f32_e64 v135, |v122|, |v122|
	v_max_f32_e32 v134, v135, v134
	v_max_f32_e64 v135, |v125|, |v125|
	v_max_f32_e64 v141, |v124|, |v124|
	v_max_f32_e32 v135, v141, v135
	v_max3_f32 v131, v131, v134, v135
	v_max_f32_e64 v134, |v119|, |v119|
	v_max_f32_e64 v135, |v118|, |v118|
	v_max_f32_e32 v134, v135, v134
	v_max_f32_e64 v135, |v121|, |v121|
	v_max_f32_e64 v141, |v120|, |v120|
	v_max_f32_e32 v135, v141, v135
	v_max3_f32 v131, v131, v134, v135
	v_max_f32_e64 v134, |v115|, |v115|
	v_max_f32_e64 v135, |v114|, |v114|
	v_max_f32_e32 v134, v135, v134
	v_max_f32_e64 v135, |v117|, |v117|
	v_max_f32_e64 v141, |v116|, |v116|
	v_max_f32_e32 v135, v141, v135
	v_max3_f32 v131, v131, v134, v135
	ds_bpermute_b32 v134, v1, v131
	s_cmpk_lt_u32 s40, 0x4000
	s_cselect_b64 s[2:3], -1, 0
	s_and_b64 s[4:5], s[2:3], exec
	s_cselect_b32 s9, 0, 0x4000000
	s_waitcnt lgkmcnt(0)
	v_max_f32_e32 v134, v134, v134
	v_max_f32_e32 v131, v131, v134
	ds_bpermute_b32 v134, v136, v131
	s_and_b32 s8, s40, 0x3fff
	s_waitcnt lgkmcnt(0)
	v_max_f32_e32 v134, v134, v134
	v_max_f32_e32 v131, v131, v134
	ds_bpermute_b32 v134, v137, v131
	s_waitcnt lgkmcnt(0)
	v_max_f32_e32 v134, v134, v134
	v_max_f32_e32 v131, v131, v134
	ds_bpermute_b32 v134, v138, v131
	s_waitcnt lgkmcnt(0)
	v_max_f32_e32 v134, v134, v134
	v_max_f32_e32 v131, v131, v134
	ds_bpermute_b32 v134, v139, v131
	s_waitcnt lgkmcnt(0)
	v_max_f32_e32 v134, v134, v134
	v_max_f32_e32 v131, v131, v134
	ds_bpermute_b32 v134, v140, v131
	s_waitcnt lgkmcnt(0)
; __device__ __forceinline__ void pt_proc(unsigned char* PT, const f32x4* v, int r, int lane) {
;     ...
;     amax = wave_max(amax); const float scale = amax > 0.f ? 127.f / amax : 0.f;
; #pragma unroll
;     for (int j = 0; j < 16; ++j) ((unsigned*)(tab + (size_t)j * PT_SLICE + (size_t)e * 256))[lane] = pack_i8x4(v[j].x * scale, v[j].y * scale, v[j].z * scale, v[j].w * scale);
	v_max_f32_e32 v134, v134, v134
	v_max_f32_e32 v131, v131, v134
	v_div_scale_f32 v134, s[4:5], v131, v131, s22
	v_rcp_f32_e32 v135, v134
	s_add_u32 s4, s1, s9
	s_addc_u32 s5, s10, 0
	s_lshl_b32 s9, s8, 8
	v_fma_f32 v141, -v134, v135, 1.0
	v_fmac_f32_e32 v135, v141, v135
	v_div_scale_f32 v141, vcc, s22, v131, s22
	v_mul_f32_e32 v142, v141, v135
	v_fma_f32 v143, -v134, v142, v141
	v_fmac_f32_e32 v142, v143, v135
	v_fma_f32 v134, -v134, v142, v141
	v_div_fmas_f32 v134, v134, v135, v142
	v_div_fixup_f32 v134, v134, v131, s22
	v_cmp_lt_f32_e32 vcc, 0, v131
	s_add_u32 s4, s4, s9
	s_addc_u32 s5, s5, 0
	v_cndmask_b32_e32 v141, 0, v134, vcc
	v_mul_f32_e32 v143, v79, v141
	v_mul_f32_e32 v142, v78, v141
	v_mul_f32_e32 v144, v80, v141
	v_mul_f32_e32 v145, v81, v141
	v_rndne_f32_e32 v143, v143
	v_rndne_f32_e32 v142, v142
	v_cvt_i32_f32_e32 v143, v143
	v_rndne_f32_e32 v144, v144
	v_rndne_f32_e32 v145, v145
	v_cvt_i32_f32_e32 v142, v142
	v_cvt_i32_f32_sdwa v144, v144 dst_sel:WORD_1 dst_unused:UNUSED_PAD src0_sel:DWORD
	v_cvt_i32_f32_e32 v145, v145
	v_lshlrev_b32_e32 v143, 8, v143
	v_and_b32_e32 v143, 0xff00, v143
	v_and_b32_e32 v144, 0xff0000, v144
	v_perm_b32 v142, v145, v142, s23
	v_or3_b32 v142, v142, v143, v144
	global_store_dword v132, v142, s[4:5] nt
	v_mul_f32_e32 v142, v75, v141
	v_lshl_add_u64 v[134:135], s[4:5], 0, v[132:133]
	v_mul_f32_e32 v132, v74, v141
	v_mul_f32_e32 v143, v76, v141
	v_mul_f32_e32 v144, v77, v141
	v_rndne_f32_e32 v142, v142
	v_rndne_f32_e32 v132, v132
	v_cvt_i32_f32_e32 v142, v142
	v_rndne_f32_e32 v143, v143
	v_rndne_f32_e32 v144, v144
	v_cvt_i32_f32_e32 v132, v132
	v_cvt_i32_f32_sdwa v143, v143 dst_sel:WORD_1 dst_unused:UNUSED_PAD src0_sel:DWORD
	v_cvt_i32_f32_e32 v144, v144
	v_lshlrev_b32_e32 v142, 8, v142
	v_and_b32_e32 v142, 0xff00, v142
	v_and_b32_e32 v143, 0xff0000, v143
	v_perm_b32 v132, v144, v132, s23
	v_or3_b32 v132, v132, v142, v143
	v_add_co_u32_e32 v142, vcc, s24, v134
	v_mul_f32_e32 v144, v73, v141
	s_nop 0
	v_addc_co_u32_e32 v143, vcc, 0, v135, vcc
	global_store_dword v[142:143], v132, off nt
	v_mul_f32_e32 v142, v71, v141
	v_mul_f32_e32 v132, v70, v141
	v_mul_f32_e32 v143, v72, v141
	v_rndne_f32_e32 v142, v142
	v_rndne_f32_e32 v132, v132
	v_cvt_i32_f32_e32 v142, v142
	v_rndne_f32_e32 v143, v143
	v_rndne_f32_e32 v144, v144
	v_cvt_i32_f32_e32 v132, v132
	v_cvt_i32_f32_sdwa v143, v143 dst_sel:WORD_1 dst_unused:UNUSED_PAD src0_sel:DWORD
	v_cvt_i32_f32_e32 v144, v144
	v_lshlrev_b32_e32 v142, 8, v142
	v_and_b32_e32 v142, 0xff00, v142
	v_and_b32_e32 v143, 0xff0000, v143
	v_perm_b32 v132, v144, v132, s23
	v_or3_b32 v132, v132, v142, v143
	v_add_co_u32_e32 v142, vcc, s25, v134
	v_mul_f32_e32 v144, v69, v141
	s_nop 0
	v_addc_co_u32_e32 v143, vcc, 0, v135, vcc
	global_store_dword v[142:143], v132, off nt
	v_mul_f32_e32 v142, v67, v141
	v_mul_f32_e32 v132, v66, v141
	v_mul_f32_e32 v143, v68, v141
	v_rndne_f32_e32 v142, v142
	v_rndne_f32_e32 v132, v132
	v_cvt_i32_f32_e32 v142, v142
	v_rndne_f32_e32 v143, v143
	v_rndne_f32_e32 v144, v144
	v_cvt_i32_f32_e32 v132, v132
	v_cvt_i32_f32_sdwa v143, v143 dst_sel:WORD_1 dst_unused:UNUSED_PAD src0_sel:DWORD
	v_cvt_i32_f32_e32 v144, v144
	v_lshlrev_b32_e32 v142, 8, v142
	v_and_b32_e32 v142, 0xff00, v142
	v_and_b32_e32 v143, 0xff0000, v143
	v_perm_b32 v132, v144, v132, s23
	v_or3_b32 v132, v132, v142, v143
	v_add_co_u32_e32 v142, vcc, s26, v134
	v_mul_f32_e32 v144, v97, v141
	s_nop 0
	v_addc_co_u32_e32 v143, vcc, 0, v135, vcc
	global_store_dword v[142:143], v132, off nt
	v_mul_f32_e32 v142, v95, v141
	v_mul_f32_e32 v132, v94, v141
	v_mul_f32_e32 v143, v96, v141
	v_rndne_f32_e32 v142, v142
	v_rndne_f32_e32 v132, v132
	v_cvt_i32_f32_e32 v142, v142
	v_rndne_f32_e32 v143, v143
	v_rndne_f32_e32 v144, v144
	v_cvt_i32_f32_e32 v132, v132
	v_cvt_i32_f32_sdwa v143, v143 dst_sel:WORD_1 dst_unused:UNUSED_PAD src0_sel:DWORD
	v_cvt_i32_f32_e32 v144, v144
	v_lshlrev_b32_e32 v142, 8, v142
	v_and_b32_e32 v142, 0xff00, v142
	v_and_b32_e32 v143, 0xff0000, v143
	v_perm_b32 v132, v144, v132, s23
	v_or3_b32 v132, v132, v142, v143
	v_add_co_u32_e32 v142, vcc, s27, v134
	v_mul_f32_e32 v144, v93, v141
	s_nop 0
	v_addc_co_u32_e32 v143, vcc, 0, v135, vcc
	global_store_dword v[142:143], v132, off nt
	v_mul_f32_e32 v142, v91, v141
	v_mul_f32_e32 v132, v90, v141
	v_mul_f32_e32 v143, v92, v141
	v_rndne_f32_e32 v142, v142
	v_rndne_f32_e32 v132, v132
	v_cvt_i32_f32_e32 v142, v142
	v_rndne_f32_e32 v143, v143
	v_rndne_f32_e32 v144, v144
	v_cvt_i32_f32_e32 v132, v132
	v_cvt_i32_f32_sdwa v143, v143 dst_sel:WORD_1 dst_unused:UNUSED_PAD src0_sel:DWORD
	v_cvt_i32_f32_e32 v144, v144
	v_lshlrev_b32_e32 v142, 8, v142
	v_and_b32_e32 v142, 0xff00, v142
	v_and_b32_e32 v143, 0xff0000, v143
	v_perm_b32 v132, v144, v132, s23
	v_or3_b32 v132, v132, v142, v143
	v_add_co_u32_e32 v142, vcc, s28, v134
	v_mul_f32_e32 v144, v89, v141
	s_nop 0
	v_addc_co_u32_e32 v143, vcc, 0, v135, vcc
	global_store_dword v[142:143], v132, off nt
	v_mul_f32_e32 v142, v87, v141
	v_mul_f32_e32 v132, v86, v141
	v_mul_f32_e32 v143, v88, v141
	v_rndne_f32_e32 v142, v142
	v_rndne_f32_e32 v132, v132
	v_cvt_i32_f32_e32 v142, v142
	v_rndne_f32_e32 v143, v143
	v_rndne_f32_e32 v144, v144
	v_cvt_i32_f32_e32 v132, v132
	v_cvt_i32_f32_sdwa v143, v143 dst_sel:WORD_1 dst_unused:UNUSED_PAD src0_sel:DWORD
	v_cvt_i32_f32_e32 v144, v144
	v_lshlrev_b32_e32 v142, 8, v142
	v_and_b32_e32 v142, 0xff00, v142
	v_and_b32_e32 v143, 0xff0000, v143
	v_perm_b32 v132, v144, v132, s23
	v_or3_b32 v132, v132, v142, v143
	v_add_co_u32_e32 v142, vcc, s29, v134
	v_mul_f32_e32 v144, v85, v141
	s_nop 0
	v_addc_co_u32_e32 v143, vcc, 0, v135, vcc
	global_store_dword v[142:143], v132, off nt
; __device__ __forceinline__ void pt_proc(unsigned char* PT, const f32x4* v, int r, int lane) {
;     ...
;     for (int j = 0; j < 16; ++j) ((unsigned*)(tab + (size_t)j * PT_SLICE + (size_t)e * 256))[lane] = pack_i8x4(v[j].x * scale, v[j].y * scale, v[j].z * scale, v[j].w * scale);
;     if (lane == 0) ((float*)(PT + (tb ? PT_VS : PT_US)))[e] = amax * (1.f / 127.f);
	v_mul_f32_e32 v142, v83, v141
	v_mul_f32_e32 v132, v82, v141
	v_mul_f32_e32 v143, v84, v141
	v_rndne_f32_e32 v142, v142
	v_rndne_f32_e32 v132, v132
	v_cvt_i32_f32_e32 v142, v142
	v_rndne_f32_e32 v143, v143
	v_rndne_f32_e32 v144, v144
	v_cvt_i32_f32_e32 v132, v132
	v_cvt_i32_f32_sdwa v143, v143 dst_sel:WORD_1 dst_unused:UNUSED_PAD src0_sel:DWORD
	v_cvt_i32_f32_e32 v144, v144
	v_lshlrev_b32_e32 v142, 8, v142
	v_and_b32_e32 v142, 0xff00, v142
	v_and_b32_e32 v143, 0xff0000, v143
	v_perm_b32 v132, v144, v132, s23
	v_or3_b32 v132, v132, v142, v143
	v_add_co_u32_e32 v142, vcc, s30, v134
	v_mul_f32_e32 v144, v113, v141
	s_nop 0
	v_addc_co_u32_e32 v143, vcc, 0, v135, vcc
	global_store_dword v[142:143], v132, off nt
	v_mul_f32_e32 v142, v111, v141
	v_mul_f32_e32 v132, v110, v141
	v_mul_f32_e32 v143, v112, v141
	v_rndne_f32_e32 v142, v142
	v_rndne_f32_e32 v132, v132
	v_cvt_i32_f32_e32 v142, v142
	v_rndne_f32_e32 v143, v143
	v_rndne_f32_e32 v144, v144
	v_cvt_i32_f32_e32 v132, v132
	v_cvt_i32_f32_sdwa v143, v143 dst_sel:WORD_1 dst_unused:UNUSED_PAD src0_sel:DWORD
	v_cvt_i32_f32_e32 v144, v144
	v_lshlrev_b32_e32 v142, 8, v142
	v_and_b32_e32 v142, 0xff00, v142
	v_and_b32_e32 v143, 0xff0000, v143
	v_perm_b32 v132, v144, v132, s23
	v_or3_b32 v132, v132, v142, v143
	v_add_co_u32_e32 v142, vcc, s31, v134
	v_mul_f32_e32 v144, v109, v141
	s_nop 0
	v_addc_co_u32_e32 v143, vcc, 0, v135, vcc
	global_store_dword v[142:143], v132, off nt
	v_mul_f32_e32 v142, v107, v141
	v_mul_f32_e32 v132, v106, v141
	v_mul_f32_e32 v143, v108, v141
	v_rndne_f32_e32 v142, v142
	v_rndne_f32_e32 v132, v132
	v_cvt_i32_f32_e32 v142, v142
	v_rndne_f32_e32 v143, v143
	v_rndne_f32_e32 v144, v144
	v_cvt_i32_f32_e32 v132, v132
	v_cvt_i32_f32_sdwa v143, v143 dst_sel:WORD_1 dst_unused:UNUSED_PAD src0_sel:DWORD
	v_cvt_i32_f32_e32 v144, v144
	v_lshlrev_b32_e32 v142, 8, v142
	v_and_b32_e32 v142, 0xff00, v142
	v_and_b32_e32 v143, 0xff0000, v143
	v_perm_b32 v132, v144, v132, s23
	v_or3_b32 v132, v132, v142, v143
	v_add_co_u32_e32 v142, vcc, s33, v134
	v_mul_f32_e32 v144, v105, v141
	s_nop 0
	v_addc_co_u32_e32 v143, vcc, 0, v135, vcc
	global_store_dword v[142:143], v132, off nt
	v_mul_f32_e32 v142, v103, v141
	v_mul_f32_e32 v132, v102, v141
	v_mul_f32_e32 v143, v104, v141
	v_rndne_f32_e32 v142, v142
	v_rndne_f32_e32 v132, v132
	v_cvt_i32_f32_e32 v142, v142
	v_rndne_f32_e32 v143, v143
	v_rndne_f32_e32 v144, v144
	v_cvt_i32_f32_e32 v132, v132
	v_cvt_i32_f32_sdwa v143, v143 dst_sel:WORD_1 dst_unused:UNUSED_PAD src0_sel:DWORD
	v_cvt_i32_f32_e32 v144, v144
	v_lshlrev_b32_e32 v142, 8, v142
	v_and_b32_e32 v142, 0xff00, v142
	v_and_b32_e32 v143, 0xff0000, v143
	v_perm_b32 v132, v144, v132, s23
	v_or3_b32 v132, v132, v142, v143
	v_add_co_u32_e32 v142, vcc, s34, v134
	v_mul_f32_e32 v144, v101, v141
	s_nop 0
	v_addc_co_u32_e32 v143, vcc, 0, v135, vcc
	global_store_dword v[142:143], v132, off nt
	v_mul_f32_e32 v142, v99, v141
	v_mul_f32_e32 v132, v98, v141
	v_mul_f32_e32 v143, v100, v141
	v_rndne_f32_e32 v142, v142
	v_rndne_f32_e32 v132, v132
	v_cvt_i32_f32_e32 v142, v142
	v_rndne_f32_e32 v143, v143
	v_rndne_f32_e32 v144, v144
	v_cvt_i32_f32_e32 v132, v132
	v_cvt_i32_f32_sdwa v143, v143 dst_sel:WORD_1 dst_unused:UNUSED_PAD src0_sel:DWORD
	v_cvt_i32_f32_e32 v144, v144
	v_lshlrev_b32_e32 v142, 8, v142
	v_and_b32_e32 v142, 0xff00, v142
	v_and_b32_e32 v143, 0xff0000, v143
	v_perm_b32 v132, v144, v132, s23
	v_or3_b32 v132, v132, v142, v143
	v_add_co_u32_e32 v142, vcc, s35, v134
	v_mul_f32_e32 v144, v129, v141
	s_nop 0
	v_addc_co_u32_e32 v143, vcc, 0, v135, vcc
	global_store_dword v[142:143], v132, off nt
	v_mul_f32_e32 v142, v127, v141
	v_mul_f32_e32 v132, v126, v141
	v_mul_f32_e32 v143, v128, v141
	v_rndne_f32_e32 v142, v142
	v_rndne_f32_e32 v132, v132
	v_cvt_i32_f32_e32 v142, v142
	v_rndne_f32_e32 v143, v143
	v_rndne_f32_e32 v144, v144
	v_cvt_i32_f32_e32 v132, v132
	v_cvt_i32_f32_sdwa v143, v143 dst_sel:WORD_1 dst_unused:UNUSED_PAD src0_sel:DWORD
	v_cvt_i32_f32_e32 v144, v144
	v_lshlrev_b32_e32 v142, 8, v142
	v_and_b32_e32 v142, 0xff00, v142
	v_and_b32_e32 v143, 0xff0000, v143
	v_perm_b32 v132, v144, v132, s23
	v_or3_b32 v132, v132, v142, v143
	v_add_co_u32_e32 v142, vcc, s36, v134
	v_mul_f32_e32 v144, v125, v141
	s_nop 0
	v_addc_co_u32_e32 v143, vcc, 0, v135, vcc
	global_store_dword v[142:143], v132, off nt
	v_mul_f32_e32 v142, v123, v141
	v_mul_f32_e32 v132, v122, v141
	v_mul_f32_e32 v143, v124, v141
	v_rndne_f32_e32 v142, v142
	v_rndne_f32_e32 v132, v132
	v_cvt_i32_f32_e32 v142, v142
	v_rndne_f32_e32 v143, v143
	v_rndne_f32_e32 v144, v144
	v_cvt_i32_f32_e32 v132, v132
	v_cvt_i32_f32_sdwa v143, v143 dst_sel:WORD_1 dst_unused:UNUSED_PAD src0_sel:DWORD
	v_cvt_i32_f32_e32 v144, v144
	v_lshlrev_b32_e32 v142, 8, v142
	v_and_b32_e32 v142, 0xff00, v142
	v_and_b32_e32 v143, 0xff0000, v143
	v_perm_b32 v132, v144, v132, s23
	v_or3_b32 v132, v132, v142, v143
	v_add_co_u32_e32 v142, vcc, s37, v134
	v_mul_f32_e32 v144, v121, v141
	s_nop 0
	v_addc_co_u32_e32 v143, vcc, 0, v135, vcc
	global_store_dword v[142:143], v132, off nt
	v_mul_f32_e32 v142, v119, v141
	v_mul_f32_e32 v132, v118, v141
	v_mul_f32_e32 v143, v120, v141
	v_rndne_f32_e32 v142, v142
	v_rndne_f32_e32 v132, v132
	v_cvt_i32_f32_e32 v142, v142
	v_rndne_f32_e32 v143, v143
	v_rndne_f32_e32 v144, v144
	v_cvt_i32_f32_e32 v132, v132
	v_cvt_i32_f32_sdwa v143, v143 dst_sel:WORD_1 dst_unused:UNUSED_PAD src0_sel:DWORD
	v_cvt_i32_f32_e32 v144, v144
	v_lshlrev_b32_e32 v142, 8, v142
	v_and_b32_e32 v142, 0xff00, v142
	v_and_b32_e32 v143, 0xff0000, v143
	v_perm_b32 v132, v144, v132, s23
	v_or3_b32 v132, v132, v142, v143
	v_add_co_u32_e32 v142, vcc, s38, v134
	s_nop 1
	v_addc_co_u32_e32 v143, vcc, 0, v135, vcc
	global_store_dword v[142:143], v132, off nt
	v_mul_f32_e32 v142, v115, v141
	v_mul_f32_e32 v132, v114, v141
	v_mul_f32_e32 v143, v116, v141
	v_mul_f32_e32 v141, v117, v141
	v_rndne_f32_e32 v142, v142
	v_rndne_f32_e32 v132, v132
	v_cvt_i32_f32_e32 v142, v142
	v_rndne_f32_e32 v143, v143
	v_rndne_f32_e32 v141, v141
	v_cvt_i32_f32_e32 v132, v132
	v_cvt_i32_f32_sdwa v143, v143 dst_sel:WORD_1 dst_unused:UNUSED_PAD src0_sel:DWORD
	v_cvt_i32_f32_e32 v141, v141
	v_lshlrev_b32_e32 v142, 8, v142
	v_and_b32_e32 v142, 0xff00, v142
	v_and_b32_e32 v143, 0xff0000, v143
	v_perm_b32 v132, v141, v132, s23
	v_add_co_u32_e32 v134, vcc, 0x3c00000, v134
	v_or3_b32 v132, v132, v142, v143
	s_nop 0
	v_addc_co_u32_e32 v135, vcc, 0, v135, vcc
	global_store_dword v[134:135], v132, off nt
	s_and_saveexec_b64 s[4:5], s[6:7]
	s_cbranch_execz .Lpt3_1250
	s_and_b64 s[2:3], s[2:3], exec
	s_cselect_b32 s2, s39, 0x8010000
	s_add_u32 s2, s1, s2
	s_addc_u32 s3, s10, 0
	s_lshl_b32 s8, s8, 2
	v_mul_f32_e32 v131, 0x3c010204, v131
	v_mov_b32_e32 v132, s8
	global_store_dword v132, v131, s[2:3] nt
	s_branch .Lpt3_1250
